# speedup vs baseline: 1.0772x; 1.0772x over previous
.LBB0_2:
	s_or_b64 exec, exec, s[14:15]
	s_load_dwordx2 s[0:1], s[0:1], 0x18
	v_lshrrev_b32_e32 v67, 5, v206
	v_or_b32_e32 v132, s11, v67
	s_lshl_b64 s[14:15], s[18:19], 14
	v_ashrrev_i32_e32 v133, 31, v132
	v_and_b32_e32 v124, 31, v0
	s_waitcnt lgkmcnt(0)
	s_add_u32 s14, s0, s14
	v_lshlrev_b64 v[2:3], 12, v[132:133]
	s_addc_u32 s15, s1, s15
	s_add_i32 s0, s7, 0x100
	v_lshl_add_u64 v[2:3], s[8:9], 0, v[2:3]
	v_lshlrev_b32_e32 v190, 4, v124
	v_mov_b32_e32 v191, 0
	s_and_b32 s26, s0, 0x300
	v_lshl_add_u64 v[130:131], v[2:3], 0, v[190:191]
	s_mov_b64 s[0:1], 0x30000
	v_lshl_add_u64 v[126:127], v[130:131], 0, s[0:1]
	s_mov_b64 s[0:1], 0x32000
	v_lshl_add_u64 v[128:129], v[130:131], 0, s[0:1]
	s_mov_b64 s[0:1], 0x34000
	v_lshl_add_u64 v[134:135], v[130:131], 0, s[0:1]
	s_mov_b64 s[0:1], 0x36000
	v_lshl_add_u64 v[136:137], v[130:131], 0, s[0:1]
	s_mov_b64 s[0:1], 0x38000
	v_lshl_add_u64 v[138:139], v[130:131], 0, s[0:1]
	s_mov_b64 s[0:1], 0x3a000
	v_lshl_add_u64 v[140:141], v[130:131], 0, s[0:1]
	s_mov_b64 s[0:1], 0x3c000
	s_or_b32 s24, s7, 0x80
	v_lshl_add_u64 v[142:143], v[130:131], 0, s[0:1]
	s_mov_b64 s[0:1], 0x3e000
	s_lshl_b32 s20, s7, 2
	v_lshl_add_u64 v[144:145], v[130:131], 0, s[0:1]
	s_lshl_b32 s8, s24, 2
	s_mov_b32 s9, s21
	v_lshl_add_u64 v[2:3], v[126:127], 0, s[20:21]
	v_lshl_add_u64 v[4:5], v[128:129], 0, s[20:21]
	v_lshl_add_u64 v[6:7], v[134:135], 0, s[20:21]
	v_lshl_add_u64 v[8:9], v[136:137], 0, s[20:21]
	v_lshl_add_u64 v[10:11], v[138:139], 0, s[20:21]
	v_lshl_add_u64 v[12:13], v[140:141], 0, s[20:21]
	v_lshl_add_u64 v[14:15], v[142:143], 0, s[20:21]
	v_lshl_add_u64 v[16:17], v[144:145], 0, s[20:21]
	v_lshl_add_u64 v[18:19], v[126:127], 0, s[8:9]
	v_lshl_add_u64 v[20:21], v[128:129], 0, s[8:9]
	v_lshl_add_u64 v[22:23], v[134:135], 0, s[8:9]
	v_lshl_add_u64 v[24:25], v[136:137], 0, s[8:9]
	s_lshl_b32 s0, s26, 2
	s_mov_b32 s1, s21
	v_lshl_add_u64 v[72:73], v[138:139], 0, s[8:9]
	v_lshl_add_u64 v[102:103], v[140:141], 0, s[8:9]
	v_lshl_add_u64 v[104:105], v[142:143], 0, s[8:9]
	v_lshl_add_u64 v[106:107], v[144:145], 0, s[8:9]
	v_lshl_add_u64 v[108:109], v[126:127], 0, s[0:1]
	v_lshl_add_u64 v[110:111], v[128:129], 0, s[0:1]
	v_lshl_add_u64 v[112:113], v[134:135], 0, s[0:1]
	v_lshl_add_u64 v[114:115], v[136:137], 0, s[0:1]
	v_lshl_add_u64 v[116:117], v[138:139], 0, s[0:1]
	v_lshl_add_u64 v[118:119], v[140:141], 0, s[0:1]
	v_lshl_add_u64 v[120:121], v[142:143], 0, s[0:1]
	v_lshl_add_u64 v[122:123], v[144:145], 0, s[0:1]
	global_load_dwordx4 v[68:71], v[2:3], off nt
	global_load_dwordx4 v[78:81], v[4:5], off nt
	global_load_dwordx4 v[82:85], v[6:7], off nt
	global_load_dwordx4 v[90:93], v[8:9], off nt
	global_load_dwordx4 v[98:101], v[10:11], off nt
	global_load_dwordx4 v[62:65], v[12:13], off nt
	global_load_dwordx4 v[54:57], v[14:15], off nt
	global_load_dwordx4 v[46:49], v[16:17], off nt
	global_load_dwordx4 v[94:97], v[18:19], off nt
	global_load_dwordx4 v[86:89], v[20:21], off nt
	global_load_dwordx4 v[74:77], v[22:23], off nt
	global_load_dwordx4 v[58:61], v[24:25], off nt
	global_load_dwordx4 v[50:53], v[72:73], off nt
	global_load_dwordx4 v[42:45], v[102:103], off nt
	global_load_dwordx4 v[38:41], v[104:105], off nt
	global_load_dwordx4 v[34:37], v[106:107], off nt
	global_load_dwordx4 v[30:33], v[108:109], off nt
	global_load_dwordx4 v[26:29], v[110:111], off nt
	s_nop 0
	global_load_dwordx4 v[22:25], v[112:113], off nt
	global_load_dwordx4 v[18:21], v[114:115], off nt
	global_load_dwordx4 v[14:17], v[116:117], off nt
	global_load_dwordx4 v[10:13], v[118:119], off nt
	global_load_dwordx4 v[6:9], v[120:121], off nt
	global_load_dwordx4 v[2:5], v[122:123], off nt
	s_waitcnt vmcnt(25)
	v_div_scale_f32 v72, s[22:23], v207, v207, 1.0
	v_rcp_f32_e32 v73, v72
	s_lshl_b32 s11, s10, 2
	s_mul_i32 s19, s35, 0x1100
	s_add_i32 s22, s11, 0x26600
	v_fma_f32 v103, -v72, v73, 1.0
	v_fmac_f32_e32 v73, v103, v73
	v_div_scale_f32 v103, vcc, 1.0, v207, 1.0
	v_mul_f32_e32 v104, v103, v73
	v_fma_f32 v105, -v72, v104, v103
	v_fmac_f32_e32 v104, v105, v73
	v_fma_f32 v72, -v72, v104, v103
	v_div_fmas_f32 v72, v72, v73, v104
	v_div_fixup_f32 v72, v72, v207, 1.0
	s_waitcnt vmcnt(24)
	v_fma_f32 v208, v72, v1, -v66
	v_lshl_add_u32 v1, v206, 2, s22
	s_add_i32 s19, s19, 0x22200
	ds_write_b32 v1, v72
	v_lshl_or_b32 v1, v124, 3, s19
	v_lshl_add_u32 v187, v67, 2, s22
	s_movk_i32 s22, 0x110
	v_mad_u32_u24 v186, v67, s22, v1
	s_add_i32 s22, s7, 0x180
	v_and_b32_e32 v102, 15, v0
	s_lshl_b32 s27, s34, 8
	s_and_b32 s25, s22, 0x380
	s_add_i32 s22, s7, 0x280
	v_lshlrev_b32_e32 v66, 2, v124
	v_mul_u32_u24_e32 v1, 0x110, v102
	v_and_b32_e32 v209, 48, v0
	s_and_b32 s23, s22, 0x380
	s_add_i32 s22, s7, 0x300
	v_mov_b32_e32 v67, 0x200
	s_addk_i32 s27, 0x380
	v_or_b32_e32 v133, s7, v66
	v_add3_u32 v1, s19, v1, v209
	s_lshl_b32 s19, s35, 15
	v_lshlrev_b32_e32 v210, 4, v206
	v_or_b32_e32 v189, s24, v66
	s_xor_b32 s24, s7, 0x200
	s_and_b32 s22, s22, 0x300
	v_bitop3_b32 v197, s7, v66, v67 bitop3:0xde
	s_and_b32 s7, s27, 0x380
	v_lshrrev_b32_e32 v185, 4, v206
	s_ashr_i32 s11, s10, 31
	v_or_b32_e32 v184, s19, v210
	v_or_b32_e32 v188, s26, v66
	v_or_b32_e32 v198, s25, v66
	v_or_b32_e32 v196, s23, v66
	v_or_b32_e32 v195, s22, v66
	v_or_b32_e32 v194, s7, v66
	v_mov_b32_e32 v102, v133
	s_waitcnt vmcnt(23)
	s_waitcnt vmcnt(22)
	s_waitcnt vmcnt(21)
	s_waitcnt vmcnt(20)
	s_waitcnt vmcnt(19)
	s_waitcnt vmcnt(18)
	s_waitcnt vmcnt(17)
	s_waitcnt vmcnt(16)
	ds_read_b32 v66, v187 offset:192
	v_or_b32_e32 v103, 48, v132
	v_add_u32_e32 v104, 1, v102
	v_cmp_eq_u32_e32 vcc, v102, v103
	v_add_u32_e32 v105, 3, v102
	v_add_u32_e32 v106, 2, v102
	v_cndmask_b32_e64 v72, 0, 1.0, vcc
	v_cmp_eq_u32_e32 vcc, v104, v103
	v_or_b32_e32 v107, 50, v132
	v_or_b32_e32 v108, 52, v132
	v_cndmask_b32_e64 v73, 0, 1.0, vcc
	v_cmp_eq_u32_e32 vcc, v105, v103
	s_waitcnt lgkmcnt(0)
	v_pk_fma_f32 v[68:69], v[66:67], v[68:69], v[72:73] op_sel_hi:[0,1,1] neg_lo:[1,0,0] neg_hi:[1,0,0]
	v_cvt_pk_bf16_f32 v68, v68, v69
	v_cndmask_b32_e64 v73, 0, 1.0, vcc
	v_cmp_eq_u32_e32 vcc, v106, v103
	v_or_b32_e32 v109, 54, v132
	v_or_b32_e32 v110, 56, v132
	v_cndmask_b32_e64 v72, 0, 1.0, vcc
	v_pk_fma_f32 v[66:67], v[66:67], v[70:71], v[72:73] op_sel_hi:[0,1,1] neg_lo:[1,0,0] neg_hi:[1,0,0]
	v_cvt_pk_bf16_f32 v69, v66, v67
	ds_write_b64 v186, v[68:69]
	ds_read_b32 v66, v187 offset:200
	v_cmp_eq_u32_e32 vcc, v102, v107
	v_or_b32_e32 v111, 58, v132
	v_or_b32_e32 v112, 60, v132
	v_cndmask_b32_e64 v68, 0, 1.0, vcc
	v_cmp_eq_u32_e32 vcc, v104, v107
	v_or_b32_e32 v113, 62, v132
	v_or_b32_e32 v193, 2, v132
	v_cndmask_b32_e64 v69, 0, 1.0, vcc
	v_cmp_eq_u32_e32 vcc, v105, v107
	s_waitcnt lgkmcnt(0)
	v_pk_fma_f32 v[68:69], v[66:67], v[78:79], v[68:69] op_sel_hi:[0,1,1] neg_lo:[1,0,0] neg_hi:[1,0,0]
	v_cvt_pk_bf16_f32 v68, v68, v69
	v_cndmask_b32_e64 v71, 0, 1.0, vcc
	v_cmp_eq_u32_e32 vcc, v106, v107
	v_or_b32_e32 v192, 4, v132
	v_or_b32_e32 v190, 6, v132
	v_cndmask_b32_e64 v70, 0, 1.0, vcc
	v_pk_fma_f32 v[66:67], v[66:67], v[80:81], v[70:71] op_sel_hi:[0,1,1] neg_lo:[1,0,0] neg_hi:[1,0,0]
	v_cvt_pk_bf16_f32 v69, v66, v67
	ds_write_b64 v186, v[68:69] offset:544
	ds_read_b32 v66, v187 offset:208
	v_cmp_eq_u32_e32 vcc, v102, v108
	v_or_b32_e32 v149, 8, v132
	v_or_b32_e32 v148, 10, v132
	v_cndmask_b32_e64 v68, 0, 1.0, vcc
	v_cmp_eq_u32_e32 vcc, v104, v108
	v_or_b32_e32 v147, 12, v132
	v_or_b32_e32 v146, 14, v132
	v_cndmask_b32_e64 v69, 0, 1.0, vcc
	v_cmp_eq_u32_e32 vcc, v105, v108
	s_waitcnt lgkmcnt(0)
	v_pk_fma_f32 v[68:69], v[66:67], v[82:83], v[68:69] op_sel_hi:[0,1,1] neg_lo:[1,0,0] neg_hi:[1,0,0]
	v_cvt_pk_bf16_f32 v68, v68, v69
	v_cndmask_b32_e64 v71, 0, 1.0, vcc
	v_cmp_eq_u32_e32 vcc, v106, v108
	s_nop 1
	v_cndmask_b32_e64 v70, 0, 1.0, vcc
	v_pk_fma_f32 v[66:67], v[66:67], v[84:85], v[70:71] op_sel_hi:[0,1,1] neg_lo:[1,0,0] neg_hi:[1,0,0]
	v_cvt_pk_bf16_f32 v69, v66, v67
	ds_write_b64 v186, v[68:69] offset:1088
	ds_read_b32 v66, v187 offset:216
	v_cmp_eq_u32_e32 vcc, v102, v109
	s_nop 1
	v_cndmask_b32_e64 v68, 0, 1.0, vcc
	v_cmp_eq_u32_e32 vcc, v104, v109
	s_nop 1
	v_cndmask_b32_e64 v69, 0, 1.0, vcc
	v_cmp_eq_u32_e32 vcc, v105, v109
	s_waitcnt lgkmcnt(0)
	v_pk_fma_f32 v[68:69], v[66:67], v[90:91], v[68:69] op_sel_hi:[0,1,1] neg_lo:[1,0,0] neg_hi:[1,0,0]
	v_cvt_pk_bf16_f32 v68, v68, v69
	v_cndmask_b32_e64 v71, 0, 1.0, vcc
	v_cmp_eq_u32_e32 vcc, v106, v109
	s_nop 1
	v_cndmask_b32_e64 v70, 0, 1.0, vcc
	v_pk_fma_f32 v[66:67], v[66:67], v[92:93], v[70:71] op_sel_hi:[0,1,1] neg_lo:[1,0,0] neg_hi:[1,0,0]
	v_cvt_pk_bf16_f32 v69, v66, v67
	ds_write_b64 v186, v[68:69] offset:1632
	ds_read_b32 v66, v187 offset:224
	v_cmp_eq_u32_e32 vcc, v102, v110
	s_nop 1
	v_cndmask_b32_e64 v68, 0, 1.0, vcc
	v_cmp_eq_u32_e32 vcc, v104, v110
	s_nop 1
	v_cndmask_b32_e64 v69, 0, 1.0, vcc
	v_cmp_eq_u32_e32 vcc, v105, v110
	s_waitcnt lgkmcnt(0)
	v_pk_fma_f32 v[68:69], v[66:67], v[98:99], v[68:69] op_sel_hi:[0,1,1] neg_lo:[1,0,0] neg_hi:[1,0,0]
	v_cvt_pk_bf16_f32 v68, v68, v69
	v_cndmask_b32_e64 v71, 0, 1.0, vcc
	v_cmp_eq_u32_e32 vcc, v106, v110
	s_nop 1
	v_cndmask_b32_e64 v70, 0, 1.0, vcc
	v_pk_fma_f32 v[66:67], v[66:67], v[100:101], v[70:71] op_sel_hi:[0,1,1] neg_lo:[1,0,0] neg_hi:[1,0,0]
	v_cvt_pk_bf16_f32 v69, v66, v67
	ds_write_b64 v186, v[68:69] offset:2176
	ds_read_b32 v66, v187 offset:232
	v_cmp_eq_u32_e32 vcc, v102, v111
	s_nop 1
	v_cndmask_b32_e64 v68, 0, 1.0, vcc
	v_cmp_eq_u32_e32 vcc, v104, v111
	s_nop 1
	v_cndmask_b32_e64 v69, 0, 1.0, vcc
	v_cmp_eq_u32_e32 vcc, v105, v111
	s_waitcnt lgkmcnt(0)
	v_pk_fma_f32 v[62:63], v[66:67], v[62:63], v[68:69] op_sel_hi:[0,1,1] neg_lo:[1,0,0] neg_hi:[1,0,0]
	v_cvt_pk_bf16_f32 v62, v62, v63
	v_cndmask_b32_e64 v69, 0, 1.0, vcc
	v_cmp_eq_u32_e32 vcc, v106, v111
	s_nop 1
	v_cndmask_b32_e64 v68, 0, 1.0, vcc
	v_pk_fma_f32 v[64:65], v[66:67], v[64:65], v[68:69] op_sel_hi:[0,1,1] neg_lo:[1,0,0] neg_hi:[1,0,0]
	v_cvt_pk_bf16_f32 v63, v64, v65
	ds_write_b64 v186, v[62:63] offset:2720
	ds_read_b32 v62, v187 offset:240
	v_cmp_eq_u32_e32 vcc, v102, v112
	s_nop 1
	v_cndmask_b32_e64 v64, 0, 1.0, vcc
	v_cmp_eq_u32_e32 vcc, v104, v112
	s_nop 1
	v_cndmask_b32_e64 v65, 0, 1.0, vcc
	v_cmp_eq_u32_e32 vcc, v105, v112
	s_waitcnt lgkmcnt(0)
	v_pk_fma_f32 v[54:55], v[62:63], v[54:55], v[64:65] op_sel_hi:[0,1,1] neg_lo:[1,0,0] neg_hi:[1,0,0]
	v_cvt_pk_bf16_f32 v54, v54, v55
	v_cndmask_b32_e64 v65, 0, 1.0, vcc
	v_cmp_eq_u32_e32 vcc, v106, v112
	s_nop 1
	v_cndmask_b32_e64 v64, 0, 1.0, vcc
	v_pk_fma_f32 v[56:57], v[62:63], v[56:57], v[64:65] op_sel_hi:[0,1,1] neg_lo:[1,0,0] neg_hi:[1,0,0]
	v_cvt_pk_bf16_f32 v55, v56, v57
	ds_write_b64 v186, v[54:55] offset:3264
	ds_read_b32 v54, v187 offset:248
	v_cmp_eq_u32_e32 vcc, v102, v113
	s_nop 1
	v_cndmask_b32_e64 v56, 0, 1.0, vcc
	v_cmp_eq_u32_e32 vcc, v104, v113
	s_nop 1
	v_cndmask_b32_e64 v57, 0, 1.0, vcc
	v_cmp_eq_u32_e32 vcc, v105, v113
	s_waitcnt lgkmcnt(0)
	v_pk_fma_f32 v[46:47], v[54:55], v[46:47], v[56:57] op_sel_hi:[0,1,1] neg_lo:[1,0,0] neg_hi:[1,0,0]
	v_cvt_pk_bf16_f32 v46, v46, v47
	v_cndmask_b32_e64 v57, 0, 1.0, vcc
	v_cmp_eq_u32_e32 vcc, v106, v113
	s_nop 1
	v_cndmask_b32_e64 v56, 0, 1.0, vcc
	v_pk_fma_f32 v[48:49], v[54:55], v[48:49], v[56:57] op_sel_hi:[0,1,1] neg_lo:[1,0,0] neg_hi:[1,0,0]
	v_cvt_pk_bf16_f32 v47, v48, v49
	ds_write_b64 v186, v[46:47] offset:3808
	ds_read_b128 v[46:49], v1
	s_waitcnt lgkmcnt(0)
	ds_write_b128 v184, v[46:49]
	ds_read_b128 v[46:49], v1 offset:64
	s_waitcnt lgkmcnt(0)
	ds_write_b128 v184, v[46:49] offset:1024
	ds_read_b128 v[46:49], v1 offset:128
	s_waitcnt lgkmcnt(0)
	ds_write_b128 v184, v[46:49] offset:2048
	ds_read_b128 v[46:49], v1 offset:192
	s_waitcnt lgkmcnt(0)
	ds_write_b128 v184, v[46:49] offset:3072
	s_lshl_b32 s30, s25, 2
	s_mov_b32 s31, s21
	v_lshl_add_u64 v[46:47], v[126:127], 0, s[30:31]
	v_lshl_add_u64 v[48:49], v[128:129], 0, s[30:31]
	v_lshl_add_u64 v[54:55], v[134:135], 0, s[30:31]
	v_lshl_add_u64 v[56:57], v[136:137], 0, s[30:31]
	v_lshl_add_u64 v[62:63], v[138:139], 0, s[30:31]
	v_lshl_add_u64 v[64:65], v[140:141], 0, s[30:31]
	v_lshl_add_u64 v[98:99], v[142:143], 0, s[30:31]
	v_lshl_add_u64 v[100:101], v[144:145], 0, s[30:31]
	global_load_dwordx4 v[90:93], v[46:47], off nt
	global_load_dwordx4 v[82:85], v[48:49], off nt
	global_load_dwordx4 v[78:81], v[54:55], off nt
	global_load_dwordx4 v[70:73], v[56:57], off nt
	global_load_dwordx4 v[66:69], v[62:63], off nt
	s_nop 0
	global_load_dwordx4 v[62:65], v[64:65], off nt
	s_nop 0
	global_load_dwordx4 v[54:57], v[98:99], off nt
	global_load_dwordx4 v[46:49], v[100:101], off nt
	v_mov_b32_e32 v99, v189
	s_waitcnt vmcnt(23)
	s_waitcnt vmcnt(22)
	s_waitcnt vmcnt(21)
	s_waitcnt vmcnt(20)
	s_waitcnt vmcnt(19)
	s_waitcnt vmcnt(18)
	s_waitcnt vmcnt(17)
	s_waitcnt vmcnt(16)
	ds_read_b32 v98, v187 offset:192
	v_add_u32_e32 v102, 1, v99
	v_cmp_eq_u32_e32 vcc, v99, v103
	v_add_u32_e32 v104, 3, v99
	v_add_u32_e32 v105, 2, v99
	v_cndmask_b32_e64 v100, 0, 1.0, vcc
	v_cmp_eq_u32_e32 vcc, v102, v103
	s_nop 1
	v_cndmask_b32_e64 v101, 0, 1.0, vcc
	v_cmp_eq_u32_e32 vcc, v104, v103
	s_waitcnt lgkmcnt(0)
	v_pk_fma_f32 v[94:95], v[98:99], v[94:95], v[100:101] op_sel_hi:[0,1,1] neg_lo:[1,0,0] neg_hi:[1,0,0]
	v_cvt_pk_bf16_f32 v94, v94, v95
	v_cndmask_b32_e64 v101, 0, 1.0, vcc
	v_cmp_eq_u32_e32 vcc, v105, v103
	s_nop 1
	v_cndmask_b32_e64 v100, 0, 1.0, vcc
	v_pk_fma_f32 v[96:97], v[98:99], v[96:97], v[100:101] op_sel_hi:[0,1,1] neg_lo:[1,0,0] neg_hi:[1,0,0]
	v_cvt_pk_bf16_f32 v95, v96, v97
	ds_write_b64 v186, v[94:95]
	ds_read_b32 v94, v187 offset:200
	v_cmp_eq_u32_e32 vcc, v99, v107
	s_nop 1
	v_cndmask_b32_e64 v96, 0, 1.0, vcc
	v_cmp_eq_u32_e32 vcc, v102, v107
	s_nop 1
	v_cndmask_b32_e64 v97, 0, 1.0, vcc
	v_cmp_eq_u32_e32 vcc, v104, v107
	s_waitcnt lgkmcnt(0)
	v_pk_fma_f32 v[86:87], v[94:95], v[86:87], v[96:97] op_sel_hi:[0,1,1] neg_lo:[1,0,0] neg_hi:[1,0,0]
	v_cvt_pk_bf16_f32 v86, v86, v87
	v_cndmask_b32_e64 v97, 0, 1.0, vcc
	v_cmp_eq_u32_e32 vcc, v105, v107
	s_nop 1
	v_cndmask_b32_e64 v96, 0, 1.0, vcc
	v_pk_fma_f32 v[88:89], v[94:95], v[88:89], v[96:97] op_sel_hi:[0,1,1] neg_lo:[1,0,0] neg_hi:[1,0,0]
	v_cvt_pk_bf16_f32 v87, v88, v89
	ds_write_b64 v186, v[86:87] offset:544
	ds_read_b32 v86, v187 offset:208
	v_cmp_eq_u32_e32 vcc, v99, v108
	s_nop 1
	v_cndmask_b32_e64 v88, 0, 1.0, vcc
	v_cmp_eq_u32_e32 vcc, v102, v108
	s_nop 1
	v_cndmask_b32_e64 v89, 0, 1.0, vcc
	v_cmp_eq_u32_e32 vcc, v104, v108
	s_waitcnt lgkmcnt(0)
	v_pk_fma_f32 v[74:75], v[86:87], v[74:75], v[88:89] op_sel_hi:[0,1,1] neg_lo:[1,0,0] neg_hi:[1,0,0]
	v_cvt_pk_bf16_f32 v74, v74, v75
	v_cndmask_b32_e64 v89, 0, 1.0, vcc
	v_cmp_eq_u32_e32 vcc, v105, v108
	s_nop 1
	v_cndmask_b32_e64 v88, 0, 1.0, vcc
	v_pk_fma_f32 v[76:77], v[86:87], v[76:77], v[88:89] op_sel_hi:[0,1,1] neg_lo:[1,0,0] neg_hi:[1,0,0]
	v_cvt_pk_bf16_f32 v75, v76, v77
	ds_write_b64 v186, v[74:75] offset:1088
	ds_read_b32 v74, v187 offset:216
	v_cmp_eq_u32_e32 vcc, v99, v109
	s_nop 1
	v_cndmask_b32_e64 v76, 0, 1.0, vcc
	v_cmp_eq_u32_e32 vcc, v102, v109
	s_nop 1
	v_cndmask_b32_e64 v77, 0, 1.0, vcc
	v_cmp_eq_u32_e32 vcc, v104, v109
	s_waitcnt lgkmcnt(0)
	v_pk_fma_f32 v[58:59], v[74:75], v[58:59], v[76:77] op_sel_hi:[0,1,1] neg_lo:[1,0,0] neg_hi:[1,0,0]
	v_cvt_pk_bf16_f32 v58, v58, v59
	v_cndmask_b32_e64 v77, 0, 1.0, vcc
	v_cmp_eq_u32_e32 vcc, v105, v109
	s_nop 1
	v_cndmask_b32_e64 v76, 0, 1.0, vcc
	v_pk_fma_f32 v[60:61], v[74:75], v[60:61], v[76:77] op_sel_hi:[0,1,1] neg_lo:[1,0,0] neg_hi:[1,0,0]
	v_cvt_pk_bf16_f32 v59, v60, v61
	ds_write_b64 v186, v[58:59] offset:1632
	ds_read_b32 v58, v187 offset:224
	v_cmp_eq_u32_e32 vcc, v99, v110
	s_nop 1
	v_cndmask_b32_e64 v60, 0, 1.0, vcc
	v_cmp_eq_u32_e32 vcc, v102, v110
	s_nop 1
	v_cndmask_b32_e64 v61, 0, 1.0, vcc
	v_cmp_eq_u32_e32 vcc, v104, v110
	s_waitcnt lgkmcnt(0)
	v_pk_fma_f32 v[50:51], v[58:59], v[50:51], v[60:61] op_sel_hi:[0,1,1] neg_lo:[1,0,0] neg_hi:[1,0,0]
	v_cvt_pk_bf16_f32 v50, v50, v51
	v_cndmask_b32_e64 v61, 0, 1.0, vcc
	v_cmp_eq_u32_e32 vcc, v105, v110
	s_nop 1
	v_cndmask_b32_e64 v60, 0, 1.0, vcc
	v_pk_fma_f32 v[52:53], v[58:59], v[52:53], v[60:61] op_sel_hi:[0,1,1] neg_lo:[1,0,0] neg_hi:[1,0,0]
	v_cvt_pk_bf16_f32 v51, v52, v53
	ds_write_b64 v186, v[50:51] offset:2176
	ds_read_b32 v50, v187 offset:232
	v_cmp_eq_u32_e32 vcc, v99, v111
	s_nop 1
	v_cndmask_b32_e64 v52, 0, 1.0, vcc
	v_cmp_eq_u32_e32 vcc, v102, v111
	s_nop 1
	v_cndmask_b32_e64 v53, 0, 1.0, vcc
	v_cmp_eq_u32_e32 vcc, v104, v111
	s_waitcnt lgkmcnt(0)
	v_pk_fma_f32 v[42:43], v[50:51], v[42:43], v[52:53] op_sel_hi:[0,1,1] neg_lo:[1,0,0] neg_hi:[1,0,0]
	v_cvt_pk_bf16_f32 v42, v42, v43
	v_cndmask_b32_e64 v53, 0, 1.0, vcc
	v_cmp_eq_u32_e32 vcc, v105, v111
	s_nop 1
	v_cndmask_b32_e64 v52, 0, 1.0, vcc
	v_pk_fma_f32 v[44:45], v[50:51], v[44:45], v[52:53] op_sel_hi:[0,1,1] neg_lo:[1,0,0] neg_hi:[1,0,0]
	v_cvt_pk_bf16_f32 v43, v44, v45
	ds_write_b64 v186, v[42:43] offset:2720
	ds_read_b32 v42, v187 offset:240
	v_cmp_eq_u32_e32 vcc, v99, v112
	s_nop 1
	v_cndmask_b32_e64 v44, 0, 1.0, vcc
	v_cmp_eq_u32_e32 vcc, v102, v112
	s_nop 1
	v_cndmask_b32_e64 v45, 0, 1.0, vcc
	v_cmp_eq_u32_e32 vcc, v104, v112
	s_waitcnt lgkmcnt(0)
	v_pk_fma_f32 v[38:39], v[42:43], v[38:39], v[44:45] op_sel_hi:[0,1,1] neg_lo:[1,0,0] neg_hi:[1,0,0]
	v_cvt_pk_bf16_f32 v38, v38, v39
	v_cndmask_b32_e64 v45, 0, 1.0, vcc
	v_cmp_eq_u32_e32 vcc, v105, v112
	s_nop 1
	v_cndmask_b32_e64 v44, 0, 1.0, vcc
	v_pk_fma_f32 v[40:41], v[42:43], v[40:41], v[44:45] op_sel_hi:[0,1,1] neg_lo:[1,0,0] neg_hi:[1,0,0]
	v_cvt_pk_bf16_f32 v39, v40, v41
	ds_write_b64 v186, v[38:39] offset:3264
	ds_read_b32 v38, v187 offset:248
	v_cmp_eq_u32_e32 vcc, v99, v113
	s_nop 1
	v_cndmask_b32_e64 v40, 0, 1.0, vcc
	v_cmp_eq_u32_e32 vcc, v102, v113
	s_nop 1
	v_cndmask_b32_e64 v41, 0, 1.0, vcc
	v_cmp_eq_u32_e32 vcc, v104, v113
	s_waitcnt lgkmcnt(0)
	v_pk_fma_f32 v[34:35], v[38:39], v[34:35], v[40:41] op_sel_hi:[0,1,1] neg_lo:[1,0,0] neg_hi:[1,0,0]
	v_cvt_pk_bf16_f32 v34, v34, v35
	v_cndmask_b32_e64 v41, 0, 1.0, vcc
	v_cmp_eq_u32_e32 vcc, v105, v113
	s_nop 1
	v_cndmask_b32_e64 v40, 0, 1.0, vcc
	v_pk_fma_f32 v[36:37], v[38:39], v[36:37], v[40:41] op_sel_hi:[0,1,1] neg_lo:[1,0,0] neg_hi:[1,0,0]
	v_cvt_pk_bf16_f32 v35, v36, v37
	ds_write_b64 v186, v[34:35] offset:3808
	ds_read_b128 v[34:37], v1
	s_waitcnt lgkmcnt(0)
	ds_write_b128 v184, v[34:37] offset:4096
	ds_read_b128 v[34:37], v1 offset:64
	s_waitcnt lgkmcnt(0)
	ds_write_b128 v184, v[34:37] offset:5120
	ds_read_b128 v[34:37], v1 offset:128
	s_waitcnt lgkmcnt(0)
	ds_write_b128 v184, v[34:37] offset:6144
	ds_read_b128 v[34:37], v1 offset:192
	s_waitcnt lgkmcnt(0)
	ds_write_b128 v184, v[34:37] offset:7168
	s_lshl_b32 s28, s24, 2
	s_mov_b32 s29, s21
	v_lshl_add_u64 v[34:35], v[126:127], 0, s[28:29]
	v_lshl_add_u64 v[36:37], v[128:129], 0, s[28:29]
	v_lshl_add_u64 v[38:39], v[134:135], 0, s[28:29]
	v_lshl_add_u64 v[40:41], v[136:137], 0, s[28:29]
	v_lshl_add_u64 v[42:43], v[138:139], 0, s[28:29]
	v_lshl_add_u64 v[44:45], v[140:141], 0, s[28:29]
	v_lshl_add_u64 v[50:51], v[142:143], 0, s[28:29]
	v_lshl_add_u64 v[52:53], v[144:145], 0, s[28:29]
	global_load_dwordx4 v[122:125], v[34:35], off nt
	global_load_dwordx4 v[114:117], v[36:37], off nt
	global_load_dwordx4 v[106:109], v[38:39], off nt
	global_load_dwordx4 v[86:89], v[40:41], off nt
	global_load_dwordx4 v[74:77], v[42:43], off nt
	s_nop 0
	global_load_dwordx4 v[42:45], v[44:45], off nt
	s_nop 0
	global_load_dwordx4 v[38:41], v[50:51], off nt
	global_load_dwordx4 v[34:37], v[52:53], off nt
	v_mov_b32_e32 v50, v188
	s_waitcnt vmcnt(23)
	s_waitcnt vmcnt(22)
	s_waitcnt vmcnt(21)
	s_waitcnt vmcnt(20)
	s_waitcnt vmcnt(19)
	s_waitcnt vmcnt(18)
	s_waitcnt vmcnt(17)
	s_waitcnt vmcnt(16)
	ds_read_b32 v50, v187 offset:192
	s_waitcnt lgkmcnt(0)
	v_pk_fma_f32 v[30:31], v[50:51], v[30:31], 0 op_sel_hi:[0,1,0] neg_lo:[1,0,0] neg_hi:[1,0,0]
	v_pk_fma_f32 v[32:33], v[50:51], v[32:33], 0 op_sel_hi:[0,1,0] neg_lo:[1,0,0] neg_hi:[1,0,0]
	v_cvt_pk_bf16_f32 v30, v30, v31
	v_cvt_pk_bf16_f32 v31, v32, v33
	ds_write_b64 v186, v[30:31]
	ds_read_b32 v30, v187 offset:200
	s_waitcnt lgkmcnt(0)
	v_pk_fma_f32 v[26:27], v[30:31], v[26:27], 0 op_sel_hi:[0,1,0] neg_lo:[1,0,0] neg_hi:[1,0,0]
	v_pk_fma_f32 v[28:29], v[30:31], v[28:29], 0 op_sel_hi:[0,1,0] neg_lo:[1,0,0] neg_hi:[1,0,0]
	v_cvt_pk_bf16_f32 v26, v26, v27
	v_cvt_pk_bf16_f32 v27, v28, v29
	ds_write_b64 v186, v[26:27] offset:544
	ds_read_b32 v26, v187 offset:208
	s_waitcnt lgkmcnt(0)
	v_pk_fma_f32 v[22:23], v[26:27], v[22:23], 0 op_sel_hi:[0,1,0] neg_lo:[1,0,0] neg_hi:[1,0,0]
	v_pk_fma_f32 v[24:25], v[26:27], v[24:25], 0 op_sel_hi:[0,1,0] neg_lo:[1,0,0] neg_hi:[1,0,0]
	v_cvt_pk_bf16_f32 v22, v22, v23
	v_cvt_pk_bf16_f32 v23, v24, v25
	ds_write_b64 v186, v[22:23] offset:1088
	ds_read_b32 v22, v187 offset:216
	s_waitcnt lgkmcnt(0)
	v_pk_fma_f32 v[18:19], v[22:23], v[18:19], 0 op_sel_hi:[0,1,0] neg_lo:[1,0,0] neg_hi:[1,0,0]
	v_pk_fma_f32 v[20:21], v[22:23], v[20:21], 0 op_sel_hi:[0,1,0] neg_lo:[1,0,0] neg_hi:[1,0,0]
	v_cvt_pk_bf16_f32 v18, v18, v19
	v_cvt_pk_bf16_f32 v19, v20, v21
	ds_write_b64 v186, v[18:19] offset:1632
	ds_read_b32 v18, v187 offset:224
	s_waitcnt lgkmcnt(0)
	v_pk_fma_f32 v[14:15], v[18:19], v[14:15], 0 op_sel_hi:[0,1,0] neg_lo:[1,0,0] neg_hi:[1,0,0]
	v_pk_fma_f32 v[16:17], v[18:19], v[16:17], 0 op_sel_hi:[0,1,0] neg_lo:[1,0,0] neg_hi:[1,0,0]
	v_cvt_pk_bf16_f32 v14, v14, v15
	v_cvt_pk_bf16_f32 v15, v16, v17
	ds_write_b64 v186, v[14:15] offset:2176
	ds_read_b32 v14, v187 offset:232
	s_waitcnt lgkmcnt(0)
	v_pk_fma_f32 v[10:11], v[14:15], v[10:11], 0 op_sel_hi:[0,1,0] neg_lo:[1,0,0] neg_hi:[1,0,0]
	v_pk_fma_f32 v[12:13], v[14:15], v[12:13], 0 op_sel_hi:[0,1,0] neg_lo:[1,0,0] neg_hi:[1,0,0]
	v_cvt_pk_bf16_f32 v10, v10, v11
	v_cvt_pk_bf16_f32 v11, v12, v13
	ds_write_b64 v186, v[10:11] offset:2720
	ds_read_b32 v10, v187 offset:240
	s_waitcnt lgkmcnt(0)
	v_pk_fma_f32 v[6:7], v[10:11], v[6:7], 0 op_sel_hi:[0,1,0] neg_lo:[1,0,0] neg_hi:[1,0,0]
	v_pk_fma_f32 v[8:9], v[10:11], v[8:9], 0 op_sel_hi:[0,1,0] neg_lo:[1,0,0] neg_hi:[1,0,0]
	v_cvt_pk_bf16_f32 v6, v6, v7
	v_cvt_pk_bf16_f32 v7, v8, v9
	ds_write_b64 v186, v[6:7] offset:3264
	ds_read_b32 v6, v187 offset:248
	s_waitcnt lgkmcnt(0)
	v_pk_fma_f32 v[2:3], v[6:7], v[2:3], 0 op_sel_hi:[0,1,0] neg_lo:[1,0,0] neg_hi:[1,0,0]
	v_pk_fma_f32 v[4:5], v[6:7], v[4:5], 0 op_sel_hi:[0,1,0] neg_lo:[1,0,0] neg_hi:[1,0,0]
	v_cvt_pk_bf16_f32 v2, v2, v3
	v_cvt_pk_bf16_f32 v3, v4, v5
	ds_write_b64 v186, v[2:3] offset:3808
	ds_read_b128 v[2:5], v1
	s_waitcnt lgkmcnt(0)
	ds_write_b128 v184, v[2:5] offset:8192
	ds_read_b128 v[2:5], v1 offset:64
	s_waitcnt lgkmcnt(0)
	ds_write_b128 v184, v[2:5] offset:9216
	ds_read_b128 v[2:5], v1 offset:128
	s_waitcnt lgkmcnt(0)
	ds_write_b128 v184, v[2:5] offset:10240
	ds_read_b128 v[2:5], v1 offset:192
	s_waitcnt lgkmcnt(0)
	ds_write_b128 v184, v[2:5] offset:11264
	s_lshl_b32 s26, s23, 2
	s_mov_b32 s27, s21
	v_lshl_add_u64 v[2:3], v[126:127], 0, s[26:27]
	v_lshl_add_u64 v[4:5], v[128:129], 0, s[26:27]
	v_lshl_add_u64 v[6:7], v[134:135], 0, s[26:27]
	v_lshl_add_u64 v[8:9], v[136:137], 0, s[26:27]
	v_lshl_add_u64 v[10:11], v[138:139], 0, s[26:27]
	v_lshl_add_u64 v[12:13], v[140:141], 0, s[26:27]
	v_lshl_add_u64 v[14:15], v[142:143], 0, s[26:27]
	v_lshl_add_u64 v[16:17], v[144:145], 0, s[26:27]
	global_load_dwordx4 v[118:121], v[2:3], off nt
	global_load_dwordx4 v[110:113], v[4:5], off nt
	global_load_dwordx4 v[102:105], v[6:7], off nt
	global_load_dwordx4 v[98:101], v[8:9], off nt
	global_load_dwordx4 v[58:61], v[10:11], off nt
	global_load_dwordx4 v[50:53], v[12:13], off nt
	global_load_dwordx4 v[30:33], v[14:15], off nt
	global_load_dwordx4 v[22:25], v[16:17], off nt
	v_mov_b32_e32 v2, v198
	s_waitcnt vmcnt(23)
	s_waitcnt vmcnt(22)
	s_waitcnt vmcnt(21)
	s_waitcnt vmcnt(20)
	s_waitcnt vmcnt(19)
	s_waitcnt vmcnt(18)
	s_waitcnt vmcnt(17)
	s_waitcnt vmcnt(16)
	ds_read_b32 v2, v187 offset:192
	s_waitcnt lgkmcnt(0)
	v_pk_fma_f32 v[4:5], v[2:3], v[90:91], 0 op_sel_hi:[0,1,0] neg_lo:[1,0,0] neg_hi:[1,0,0]
	v_pk_fma_f32 v[2:3], v[2:3], v[92:93], 0 op_sel_hi:[0,1,0] neg_lo:[1,0,0] neg_hi:[1,0,0]
	v_cvt_pk_bf16_f32 v4, v4, v5
	v_cvt_pk_bf16_f32 v5, v2, v3
	ds_write_b64 v186, v[4:5]
	ds_read_b32 v2, v187 offset:200
	s_waitcnt lgkmcnt(0)
	v_pk_fma_f32 v[4:5], v[2:3], v[82:83], 0 op_sel_hi:[0,1,0] neg_lo:[1,0,0] neg_hi:[1,0,0]
	v_pk_fma_f32 v[2:3], v[2:3], v[84:85], 0 op_sel_hi:[0,1,0] neg_lo:[1,0,0] neg_hi:[1,0,0]
	v_cvt_pk_bf16_f32 v4, v4, v5
	v_cvt_pk_bf16_f32 v5, v2, v3
	ds_write_b64 v186, v[4:5] offset:544
	ds_read_b32 v2, v187 offset:208
	s_waitcnt lgkmcnt(0)
	v_pk_fma_f32 v[4:5], v[2:3], v[78:79], 0 op_sel_hi:[0,1,0] neg_lo:[1,0,0] neg_hi:[1,0,0]
	v_pk_fma_f32 v[2:3], v[2:3], v[80:81], 0 op_sel_hi:[0,1,0] neg_lo:[1,0,0] neg_hi:[1,0,0]
	v_cvt_pk_bf16_f32 v4, v4, v5
	v_cvt_pk_bf16_f32 v5, v2, v3
	ds_write_b64 v186, v[4:5] offset:1088
	ds_read_b32 v2, v187 offset:216
	s_waitcnt lgkmcnt(0)
	v_pk_fma_f32 v[4:5], v[2:3], v[70:71], 0 op_sel_hi:[0,1,0] neg_lo:[1,0,0] neg_hi:[1,0,0]
	v_pk_fma_f32 v[2:3], v[2:3], v[72:73], 0 op_sel_hi:[0,1,0] neg_lo:[1,0,0] neg_hi:[1,0,0]
	v_cvt_pk_bf16_f32 v4, v4, v5
	v_cvt_pk_bf16_f32 v5, v2, v3
	ds_write_b64 v186, v[4:5] offset:1632
	ds_read_b32 v2, v187 offset:224
	s_waitcnt lgkmcnt(0)
	v_pk_fma_f32 v[4:5], v[2:3], v[66:67], 0 op_sel_hi:[0,1,0] neg_lo:[1,0,0] neg_hi:[1,0,0]
	v_pk_fma_f32 v[2:3], v[2:3], v[68:69], 0 op_sel_hi:[0,1,0] neg_lo:[1,0,0] neg_hi:[1,0,0]
	v_cvt_pk_bf16_f32 v4, v4, v5
	v_cvt_pk_bf16_f32 v5, v2, v3
	ds_write_b64 v186, v[4:5] offset:2176
	ds_read_b32 v2, v187 offset:232
	s_waitcnt lgkmcnt(0)
	v_pk_fma_f32 v[4:5], v[2:3], v[62:63], 0 op_sel_hi:[0,1,0] neg_lo:[1,0,0] neg_hi:[1,0,0]
	v_pk_fma_f32 v[2:3], v[2:3], v[64:65], 0 op_sel_hi:[0,1,0] neg_lo:[1,0,0] neg_hi:[1,0,0]
	v_cvt_pk_bf16_f32 v4, v4, v5
	v_cvt_pk_bf16_f32 v5, v2, v3
	ds_write_b64 v186, v[4:5] offset:2720
	ds_read_b32 v2, v187 offset:240
	s_waitcnt lgkmcnt(0)
	v_pk_fma_f32 v[4:5], v[2:3], v[54:55], 0 op_sel_hi:[0,1,0] neg_lo:[1,0,0] neg_hi:[1,0,0]
	v_pk_fma_f32 v[2:3], v[2:3], v[56:57], 0 op_sel_hi:[0,1,0] neg_lo:[1,0,0] neg_hi:[1,0,0]
	v_cvt_pk_bf16_f32 v4, v4, v5
	v_cvt_pk_bf16_f32 v5, v2, v3
	ds_write_b64 v186, v[4:5] offset:3264
	ds_read_b32 v2, v187 offset:248
	s_waitcnt lgkmcnt(0)
	v_pk_fma_f32 v[4:5], v[2:3], v[46:47], 0 op_sel_hi:[0,1,0] neg_lo:[1,0,0] neg_hi:[1,0,0]
	v_pk_fma_f32 v[2:3], v[2:3], v[48:49], 0 op_sel_hi:[0,1,0] neg_lo:[1,0,0] neg_hi:[1,0,0]
	v_cvt_pk_bf16_f32 v4, v4, v5
	v_cvt_pk_bf16_f32 v5, v2, v3
	ds_write_b64 v186, v[4:5] offset:3808
	ds_read_b128 v[2:5], v1
	s_waitcnt lgkmcnt(0)
	ds_write_b128 v184, v[2:5] offset:12288
	ds_read_b128 v[2:5], v1 offset:64
	s_waitcnt lgkmcnt(0)
	ds_write_b128 v184, v[2:5] offset:13312
	ds_read_b128 v[2:5], v1 offset:128
	s_waitcnt lgkmcnt(0)
	ds_write_b128 v184, v[2:5] offset:14336
	ds_read_b128 v[2:5], v1 offset:192
	s_waitcnt lgkmcnt(0)
	ds_write_b128 v184, v[2:5] offset:15360
	s_lshl_b32 s24, s22, 2
	s_mov_b32 s25, s21
	v_lshl_add_u64 v[2:3], v[126:127], 0, s[24:25]
	v_lshl_add_u64 v[6:7], v[134:135], 0, s[24:25]
	v_lshl_add_u64 v[8:9], v[136:137], 0, s[24:25]
	v_lshl_add_u64 v[14:15], v[142:143], 0, s[24:25]
	v_lshl_add_u64 v[4:5], v[128:129], 0, s[24:25]
	v_lshl_add_u64 v[10:11], v[138:139], 0, s[24:25]
	v_lshl_add_u64 v[12:13], v[140:141], 0, s[24:25]
	v_lshl_add_u64 v[18:19], v[144:145], 0, s[24:25]
	global_load_dwordx4 v[94:97], v[2:3], off nt
	global_load_dwordx4 v[90:93], v[4:5], off nt
	global_load_dwordx4 v[82:85], v[6:7], off nt
	global_load_dwordx4 v[70:73], v[8:9], off nt
	global_load_dwordx4 v[54:57], v[10:11], off nt
	global_load_dwordx4 v[26:29], v[12:13], off nt
	s_nop 0
	global_load_dwordx4 v[14:17], v[14:15], off nt
	s_nop 0
	global_load_dwordx4 v[6:9], v[18:19], off nt
	v_mov_b32_e32 v2, v197
	s_waitcnt vmcnt(23)
	s_waitcnt vmcnt(22)
	s_waitcnt vmcnt(21)
	s_waitcnt vmcnt(20)
	s_waitcnt vmcnt(19)
	s_waitcnt vmcnt(18)
	s_waitcnt vmcnt(17)
	s_waitcnt vmcnt(16)
	ds_read_b32 v2, v187 offset:192
	s_waitcnt lgkmcnt(0)
	v_pk_fma_f32 v[4:5], v[2:3], v[122:123], 0 op_sel_hi:[0,1,0] neg_lo:[1,0,0] neg_hi:[1,0,0]
	v_pk_fma_f32 v[2:3], v[2:3], v[124:125], 0 op_sel_hi:[0,1,0] neg_lo:[1,0,0] neg_hi:[1,0,0]
	v_cvt_pk_bf16_f32 v4, v4, v5
	v_cvt_pk_bf16_f32 v5, v2, v3
	ds_write_b64 v186, v[4:5]
	ds_read_b32 v2, v187 offset:200
	s_waitcnt lgkmcnt(0)
	v_pk_fma_f32 v[4:5], v[2:3], v[114:115], 0 op_sel_hi:[0,1,0] neg_lo:[1,0,0] neg_hi:[1,0,0]
	v_pk_fma_f32 v[2:3], v[2:3], v[116:117], 0 op_sel_hi:[0,1,0] neg_lo:[1,0,0] neg_hi:[1,0,0]
	v_cvt_pk_bf16_f32 v4, v4, v5
	v_cvt_pk_bf16_f32 v5, v2, v3
	ds_write_b64 v186, v[4:5] offset:544
	ds_read_b32 v2, v187 offset:208
	s_waitcnt lgkmcnt(0)
	v_pk_fma_f32 v[4:5], v[2:3], v[106:107], 0 op_sel_hi:[0,1,0] neg_lo:[1,0,0] neg_hi:[1,0,0]
	v_pk_fma_f32 v[2:3], v[2:3], v[108:109], 0 op_sel_hi:[0,1,0] neg_lo:[1,0,0] neg_hi:[1,0,0]
	v_cvt_pk_bf16_f32 v4, v4, v5
	v_cvt_pk_bf16_f32 v5, v2, v3
	ds_write_b64 v186, v[4:5] offset:1088
	ds_read_b32 v2, v187 offset:216
	s_waitcnt lgkmcnt(0)
	v_pk_fma_f32 v[4:5], v[2:3], v[86:87], 0 op_sel_hi:[0,1,0] neg_lo:[1,0,0] neg_hi:[1,0,0]
	v_pk_fma_f32 v[2:3], v[2:3], v[88:89], 0 op_sel_hi:[0,1,0] neg_lo:[1,0,0] neg_hi:[1,0,0]
	v_cvt_pk_bf16_f32 v4, v4, v5
	v_cvt_pk_bf16_f32 v5, v2, v3
	ds_write_b64 v186, v[4:5] offset:1632
	ds_read_b32 v2, v187 offset:224
	s_waitcnt lgkmcnt(0)
	v_pk_fma_f32 v[4:5], v[2:3], v[74:75], 0 op_sel_hi:[0,1,0] neg_lo:[1,0,0] neg_hi:[1,0,0]
	v_pk_fma_f32 v[2:3], v[2:3], v[76:77], 0 op_sel_hi:[0,1,0] neg_lo:[1,0,0] neg_hi:[1,0,0]
	v_cvt_pk_bf16_f32 v4, v4, v5
	v_cvt_pk_bf16_f32 v5, v2, v3
	ds_write_b64 v186, v[4:5] offset:2176
	ds_read_b32 v2, v187 offset:232
	s_waitcnt lgkmcnt(0)
	v_pk_fma_f32 v[4:5], v[2:3], v[42:43], 0 op_sel_hi:[0,1,0] neg_lo:[1,0,0] neg_hi:[1,0,0]
	v_pk_fma_f32 v[2:3], v[2:3], v[44:45], 0 op_sel_hi:[0,1,0] neg_lo:[1,0,0] neg_hi:[1,0,0]
	v_cvt_pk_bf16_f32 v4, v4, v5
	v_cvt_pk_bf16_f32 v5, v2, v3
	ds_write_b64 v186, v[4:5] offset:2720
	ds_read_b32 v2, v187 offset:240
	s_waitcnt lgkmcnt(0)
	v_pk_fma_f32 v[4:5], v[2:3], v[38:39], 0 op_sel_hi:[0,1,0] neg_lo:[1,0,0] neg_hi:[1,0,0]
	v_pk_fma_f32 v[2:3], v[2:3], v[40:41], 0 op_sel_hi:[0,1,0] neg_lo:[1,0,0] neg_hi:[1,0,0]
	v_cvt_pk_bf16_f32 v4, v4, v5
	v_cvt_pk_bf16_f32 v5, v2, v3
	ds_write_b64 v186, v[4:5] offset:3264
	ds_read_b32 v2, v187 offset:248
	s_waitcnt lgkmcnt(0)
	v_pk_fma_f32 v[4:5], v[2:3], v[34:35], 0 op_sel_hi:[0,1,0] neg_lo:[1,0,0] neg_hi:[1,0,0]
	v_pk_fma_f32 v[2:3], v[2:3], v[36:37], 0 op_sel_hi:[0,1,0] neg_lo:[1,0,0] neg_hi:[1,0,0]
	v_cvt_pk_bf16_f32 v4, v4, v5
	v_cvt_pk_bf16_f32 v5, v2, v3
	ds_write_b64 v186, v[4:5] offset:3808
	ds_read_b128 v[2:5], v1
	s_waitcnt lgkmcnt(0)
	ds_write_b128 v184, v[2:5] offset:16384
	ds_read_b128 v[2:5], v1 offset:64
	s_waitcnt lgkmcnt(0)
	ds_write_b128 v184, v[2:5] offset:17408
	ds_read_b128 v[2:5], v1 offset:128
	s_waitcnt lgkmcnt(0)
	ds_write_b128 v184, v[2:5] offset:18432
	ds_read_b128 v[2:5], v1 offset:192
	s_waitcnt lgkmcnt(0)
	ds_write_b128 v184, v[2:5] offset:19456
	s_lshl_b32 s22, s7, 2
	s_mov_b32 s23, s21
	v_lshl_add_u64 v[2:3], v[126:127], 0, s[22:23]
	v_lshl_add_u64 v[4:5], v[128:129], 0, s[22:23]
	v_lshl_add_u64 v[10:11], v[134:135], 0, s[22:23]
	v_lshl_add_u64 v[12:13], v[136:137], 0, s[22:23]
	v_lshl_add_u64 v[34:35], v[138:139], 0, s[22:23]
	v_lshl_add_u64 v[36:37], v[140:141], 0, s[22:23]
	v_lshl_add_u64 v[46:47], v[142:143], 0, s[22:23]
	v_lshl_add_u64 v[48:49], v[144:145], 0, s[22:23]
	global_load_dwordx4 v[86:89], v[2:3], off nt
	global_load_dwordx4 v[78:81], v[4:5], off nt
	global_load_dwordx4 v[66:69], v[10:11], off nt
	global_load_dwordx4 v[42:45], v[12:13], off nt
	global_load_dwordx4 v[38:41], v[34:35], off nt
	global_load_dwordx4 v[18:21], v[36:37], off nt
	s_nop 0
	global_load_dwordx4 v[10:13], v[46:47], off nt
	global_load_dwordx4 v[2:5], v[48:49], off nt
	v_mov_b32_e32 v34, v196
	s_waitcnt vmcnt(23)
	s_waitcnt vmcnt(22)
	s_waitcnt vmcnt(21)
	s_waitcnt vmcnt(20)
	s_waitcnt vmcnt(19)
	s_waitcnt vmcnt(18)
	s_waitcnt vmcnt(17)
	s_waitcnt vmcnt(16)
	ds_read_b32 v34, v187 offset:192
	s_waitcnt lgkmcnt(0)
	v_pk_fma_f32 v[36:37], v[34:35], v[118:119], 0 op_sel_hi:[0,1,0] neg_lo:[1,0,0] neg_hi:[1,0,0]
	v_pk_fma_f32 v[34:35], v[34:35], v[120:121], 0 op_sel_hi:[0,1,0] neg_lo:[1,0,0] neg_hi:[1,0,0]
	v_cvt_pk_bf16_f32 v36, v36, v37
	v_cvt_pk_bf16_f32 v37, v34, v35
	ds_write_b64 v186, v[36:37]
	ds_read_b32 v34, v187 offset:200
	s_waitcnt lgkmcnt(0)
	v_pk_fma_f32 v[36:37], v[34:35], v[110:111], 0 op_sel_hi:[0,1,0] neg_lo:[1,0,0] neg_hi:[1,0,0]
	v_pk_fma_f32 v[34:35], v[34:35], v[112:113], 0 op_sel_hi:[0,1,0] neg_lo:[1,0,0] neg_hi:[1,0,0]
	v_cvt_pk_bf16_f32 v36, v36, v37
	v_cvt_pk_bf16_f32 v37, v34, v35
	ds_write_b64 v186, v[36:37] offset:544
	ds_read_b32 v34, v187 offset:208
	s_waitcnt lgkmcnt(0)
	v_pk_fma_f32 v[36:37], v[34:35], v[102:103], 0 op_sel_hi:[0,1,0] neg_lo:[1,0,0] neg_hi:[1,0,0]
	v_pk_fma_f32 v[34:35], v[34:35], v[104:105], 0 op_sel_hi:[0,1,0] neg_lo:[1,0,0] neg_hi:[1,0,0]
	v_cvt_pk_bf16_f32 v36, v36, v37
	v_cvt_pk_bf16_f32 v37, v34, v35
	ds_write_b64 v186, v[36:37] offset:1088
	ds_read_b32 v34, v187 offset:216
	s_waitcnt lgkmcnt(0)
	v_pk_fma_f32 v[36:37], v[34:35], v[98:99], 0 op_sel_hi:[0,1,0] neg_lo:[1,0,0] neg_hi:[1,0,0]
	v_pk_fma_f32 v[34:35], v[34:35], v[100:101], 0 op_sel_hi:[0,1,0] neg_lo:[1,0,0] neg_hi:[1,0,0]
	v_cvt_pk_bf16_f32 v36, v36, v37
	v_cvt_pk_bf16_f32 v37, v34, v35
	ds_write_b64 v186, v[36:37] offset:1632
	ds_read_b32 v34, v187 offset:224
	s_waitcnt lgkmcnt(0)
	v_pk_fma_f32 v[36:37], v[34:35], v[58:59], 0 op_sel_hi:[0,1,0] neg_lo:[1,0,0] neg_hi:[1,0,0]
	v_pk_fma_f32 v[34:35], v[34:35], v[60:61], 0 op_sel_hi:[0,1,0] neg_lo:[1,0,0] neg_hi:[1,0,0]
	v_cvt_pk_bf16_f32 v36, v36, v37
	v_cvt_pk_bf16_f32 v37, v34, v35
	ds_write_b64 v186, v[36:37] offset:2176
	ds_read_b32 v34, v187 offset:232
	s_waitcnt lgkmcnt(0)
	v_pk_fma_f32 v[36:37], v[34:35], v[50:51], 0 op_sel_hi:[0,1,0] neg_lo:[1,0,0] neg_hi:[1,0,0]
	v_pk_fma_f32 v[34:35], v[34:35], v[52:53], 0 op_sel_hi:[0,1,0] neg_lo:[1,0,0] neg_hi:[1,0,0]
	v_cvt_pk_bf16_f32 v36, v36, v37
	v_cvt_pk_bf16_f32 v37, v34, v35
	ds_write_b64 v186, v[36:37] offset:2720
	ds_read_b32 v34, v187 offset:240
	s_waitcnt lgkmcnt(0)
	v_pk_fma_f32 v[30:31], v[34:35], v[30:31], 0 op_sel_hi:[0,1,0] neg_lo:[1,0,0] neg_hi:[1,0,0]
	v_pk_fma_f32 v[32:33], v[34:35], v[32:33], 0 op_sel_hi:[0,1,0] neg_lo:[1,0,0] neg_hi:[1,0,0]
	v_cvt_pk_bf16_f32 v30, v30, v31
	v_cvt_pk_bf16_f32 v31, v32, v33
	ds_write_b64 v186, v[30:31] offset:3264
	ds_read_b32 v30, v187 offset:248
	s_waitcnt lgkmcnt(0)
	v_pk_fma_f32 v[22:23], v[30:31], v[22:23], 0 op_sel_hi:[0,1,0] neg_lo:[1,0,0] neg_hi:[1,0,0]
	v_pk_fma_f32 v[24:25], v[30:31], v[24:25], 0 op_sel_hi:[0,1,0] neg_lo:[1,0,0] neg_hi:[1,0,0]
	v_cvt_pk_bf16_f32 v22, v22, v23
	v_cvt_pk_bf16_f32 v23, v24, v25
	ds_write_b64 v186, v[22:23] offset:3808
	ds_read_b128 v[22:25], v1
	s_waitcnt lgkmcnt(0)
	ds_write_b128 v184, v[22:25] offset:20480
	ds_read_b128 v[22:25], v1 offset:64
	s_waitcnt lgkmcnt(0)
	ds_write_b128 v184, v[22:25] offset:21504
	ds_read_b128 v[22:25], v1 offset:128
	s_waitcnt lgkmcnt(0)
	ds_write_b128 v184, v[22:25] offset:22528
	ds_read_b128 v[22:25], v1 offset:192
	s_waitcnt lgkmcnt(0)
	ds_write_b128 v184, v[22:25] offset:23552
	v_lshl_add_u64 v[22:23], v[130:131], 0, s[30:31]
	s_movk_i32 s7, 0x2000
	v_add_co_u32_e32 v24, vcc, s7, v22
	s_movk_i32 s36, 0x4000
	s_nop 0
	v_addc_co_u32_e32 v25, vcc, 0, v23, vcc
	global_load_dwordx4 v[74:77], v[22:23], off nt
	global_load_dwordx4 v[62:65], v[24:25], off nt
	v_add_co_u32_e32 v24, vcc, s36, v22
	s_movk_i32 s37, 0x6000
	s_nop 0
	v_addc_co_u32_e32 v25, vcc, 0, v23, vcc
	v_add_co_u32_e32 v30, vcc, s37, v22
	s_mov_b32 s38, 0x8000
	s_nop 0
	v_addc_co_u32_e32 v31, vcc, 0, v23, vcc
	global_load_dwordx4 v[58:61], v[24:25], off nt
	global_load_dwordx4 v[46:49], v[30:31], off nt
	v_add_co_u32_e32 v24, vcc, s38, v22
	s_mov_b32 s39, 0xa000
	s_nop 0
	v_addc_co_u32_e32 v25, vcc, 0, v23, vcc
	v_add_co_u32_e32 v34, vcc, s39, v22
	s_mov_b32 s41, 0xc000
	s_nop 0
	v_addc_co_u32_e32 v35, vcc, 0, v23, vcc
	global_load_dwordx4 v[50:53], v[24:25], off nt
	global_load_dwordx4 v[30:33], v[34:35], off nt
	v_add_co_u32_e32 v24, vcc, s41, v22
	s_mov_b32 s42, 0xe000
	s_nop 0
	v_addc_co_u32_e32 v25, vcc, 0, v23, vcc
	v_add_co_u32_e32 v22, vcc, s42, v22
	s_nop 1
	v_addc_co_u32_e32 v23, vcc, 0, v23, vcc
	global_load_dwordx4 v[34:37], v[24:25], off nt
	s_nop 0
	global_load_dwordx4 v[22:25], v[22:23], off nt
	v_mov_b32_e32 v98, v195
	s_waitcnt vmcnt(23)
	s_waitcnt vmcnt(22)
	s_waitcnt vmcnt(21)
	s_waitcnt vmcnt(20)
	s_waitcnt vmcnt(19)
	s_waitcnt vmcnt(18)
	s_waitcnt vmcnt(17)
	s_waitcnt vmcnt(16)
	ds_read_b32 v98, v187 offset:192
	s_waitcnt lgkmcnt(0)
	v_pk_fma_f32 v[94:95], v[98:99], v[94:95], 0 op_sel_hi:[0,1,0] neg_lo:[1,0,0] neg_hi:[1,0,0]
	v_pk_fma_f32 v[96:97], v[98:99], v[96:97], 0 op_sel_hi:[0,1,0] neg_lo:[1,0,0] neg_hi:[1,0,0]
	v_cvt_pk_bf16_f32 v94, v94, v95
	v_cvt_pk_bf16_f32 v95, v96, v97
	ds_write_b64 v186, v[94:95]
	ds_read_b32 v94, v187 offset:200
	s_waitcnt lgkmcnt(0)
	v_pk_fma_f32 v[90:91], v[94:95], v[90:91], 0 op_sel_hi:[0,1,0] neg_lo:[1,0,0] neg_hi:[1,0,0]
	v_pk_fma_f32 v[92:93], v[94:95], v[92:93], 0 op_sel_hi:[0,1,0] neg_lo:[1,0,0] neg_hi:[1,0,0]
	v_cvt_pk_bf16_f32 v90, v90, v91
	v_cvt_pk_bf16_f32 v91, v92, v93
	ds_write_b64 v186, v[90:91] offset:544
	ds_read_b32 v90, v187 offset:208
	s_waitcnt lgkmcnt(0)
	v_pk_fma_f32 v[82:83], v[90:91], v[82:83], 0 op_sel_hi:[0,1,0] neg_lo:[1,0,0] neg_hi:[1,0,0]
	v_pk_fma_f32 v[84:85], v[90:91], v[84:85], 0 op_sel_hi:[0,1,0] neg_lo:[1,0,0] neg_hi:[1,0,0]
	v_cvt_pk_bf16_f32 v82, v82, v83
	v_cvt_pk_bf16_f32 v83, v84, v85
	ds_write_b64 v186, v[82:83] offset:1088
	ds_read_b32 v82, v187 offset:216
	s_waitcnt lgkmcnt(0)
	v_pk_fma_f32 v[70:71], v[82:83], v[70:71], 0 op_sel_hi:[0,1,0] neg_lo:[1,0,0] neg_hi:[1,0,0]
	v_pk_fma_f32 v[72:73], v[82:83], v[72:73], 0 op_sel_hi:[0,1,0] neg_lo:[1,0,0] neg_hi:[1,0,0]
	v_cvt_pk_bf16_f32 v70, v70, v71
	v_cvt_pk_bf16_f32 v71, v72, v73
	ds_write_b64 v186, v[70:71] offset:1632
	ds_read_b32 v70, v187 offset:224
	s_waitcnt lgkmcnt(0)
	v_pk_fma_f32 v[54:55], v[70:71], v[54:55], 0 op_sel_hi:[0,1,0] neg_lo:[1,0,0] neg_hi:[1,0,0]
	v_pk_fma_f32 v[56:57], v[70:71], v[56:57], 0 op_sel_hi:[0,1,0] neg_lo:[1,0,0] neg_hi:[1,0,0]
	v_cvt_pk_bf16_f32 v54, v54, v55
	v_cvt_pk_bf16_f32 v55, v56, v57
	ds_write_b64 v186, v[54:55] offset:2176
	ds_read_b32 v54, v187 offset:232
	s_waitcnt lgkmcnt(0)
	v_pk_fma_f32 v[26:27], v[54:55], v[26:27], 0 op_sel_hi:[0,1,0] neg_lo:[1,0,0] neg_hi:[1,0,0]
	v_pk_fma_f32 v[28:29], v[54:55], v[28:29], 0 op_sel_hi:[0,1,0] neg_lo:[1,0,0] neg_hi:[1,0,0]
	v_cvt_pk_bf16_f32 v26, v26, v27
	v_cvt_pk_bf16_f32 v27, v28, v29
	ds_write_b64 v186, v[26:27] offset:2720
	ds_read_b32 v26, v187 offset:240
	s_waitcnt lgkmcnt(0)
	v_pk_fma_f32 v[14:15], v[26:27], v[14:15], 0 op_sel_hi:[0,1,0] neg_lo:[1,0,0] neg_hi:[1,0,0]
	v_pk_fma_f32 v[16:17], v[26:27], v[16:17], 0 op_sel_hi:[0,1,0] neg_lo:[1,0,0] neg_hi:[1,0,0]
	v_cvt_pk_bf16_f32 v14, v14, v15
	v_cvt_pk_bf16_f32 v15, v16, v17
	ds_write_b64 v186, v[14:15] offset:3264
	ds_read_b32 v14, v187 offset:248
	s_waitcnt lgkmcnt(0)
	v_pk_fma_f32 v[6:7], v[14:15], v[6:7], 0 op_sel_hi:[0,1,0] neg_lo:[1,0,0] neg_hi:[1,0,0]
	v_pk_fma_f32 v[8:9], v[14:15], v[8:9], 0 op_sel_hi:[0,1,0] neg_lo:[1,0,0] neg_hi:[1,0,0]
	v_cvt_pk_bf16_f32 v6, v6, v7
	v_cvt_pk_bf16_f32 v7, v8, v9
	ds_write_b64 v186, v[6:7] offset:3808
	ds_read_b128 v[6:9], v1
	s_waitcnt lgkmcnt(0)
	ds_write_b128 v184, v[6:9] offset:24576
	ds_read_b128 v[6:9], v1 offset:64
	s_waitcnt lgkmcnt(0)
	ds_write_b128 v184, v[6:9] offset:25600
	ds_read_b128 v[6:9], v1 offset:128
	s_waitcnt lgkmcnt(0)
	ds_write_b128 v184, v[6:9] offset:26624
	ds_read_b128 v[6:9], v1 offset:192
	s_waitcnt lgkmcnt(0)
	ds_write_b128 v184, v[6:9] offset:27648
	s_mov_b64 s[44:45], 0x10000
	v_lshl_add_u64 v[150:151], v[130:131], 0, s[44:45]
	s_mov_b64 s[44:45], 0x12000
	v_lshl_add_u64 v[152:153], v[130:131], 0, s[44:45]
	s_mov_b64 s[44:45], 0x14000
	v_lshl_add_u64 v[156:157], v[130:131], 0, s[44:45]
	s_mov_b64 s[44:45], 0x16000
	v_lshl_add_u64 v[158:159], v[130:131], 0, s[44:45]
	s_mov_b64 s[44:45], 0x18000
	v_lshl_add_u64 v[160:161], v[130:131], 0, s[44:45]
	s_mov_b64 s[44:45], 0x1a000
	v_lshl_add_u64 v[162:163], v[130:131], 0, s[44:45]
	s_mov_b64 s[44:45], 0x1c000
	v_lshl_add_u64 v[164:165], v[130:131], 0, s[44:45]
	s_mov_b64 s[44:45], 0x1e000
	v_lshl_add_u64 v[6:7], v[150:151], 0, s[30:31]
	v_lshl_add_u64 v[8:9], v[152:153], 0, s[30:31]
	v_lshl_add_u64 v[14:15], v[156:157], 0, s[30:31]
	v_lshl_add_u64 v[16:17], v[158:159], 0, s[30:31]
	v_lshl_add_u64 v[26:27], v[160:161], 0, s[30:31]
	v_lshl_add_u64 v[28:29], v[162:163], 0, s[30:31]
	v_lshl_add_u64 v[166:167], v[130:131], 0, s[44:45]
	v_lshl_add_u64 v[98:99], v[164:165], 0, s[30:31]
	v_lshl_add_u64 v[100:101], v[166:167], 0, s[30:31]
	global_load_dwordx4 v[94:97], v[6:7], off nt
	global_load_dwordx4 v[90:93], v[8:9], off nt
	global_load_dwordx4 v[82:85], v[14:15], off nt
	global_load_dwordx4 v[70:73], v[16:17], off nt
	global_load_dwordx4 v[54:57], v[26:27], off nt
	s_nop 0
	global_load_dwordx4 v[26:29], v[28:29], off nt
	s_nop 0
	global_load_dwordx4 v[14:17], v[98:99], off nt
	global_load_dwordx4 v[6:9], v[100:101], off nt
	v_mov_b32_e32 v98, v194
	s_waitcnt vmcnt(23)
	s_waitcnt vmcnt(22)
	s_waitcnt vmcnt(21)
	s_waitcnt vmcnt(20)
	s_waitcnt vmcnt(19)
	s_waitcnt vmcnt(18)
	s_waitcnt vmcnt(17)
	s_waitcnt vmcnt(16)
	ds_read_b32 v98, v187 offset:192
	s_waitcnt lgkmcnt(0)
	v_pk_fma_f32 v[86:87], v[98:99], v[86:87], 0 op_sel_hi:[0,1,0] neg_lo:[1,0,0] neg_hi:[1,0,0]
	v_pk_fma_f32 v[88:89], v[98:99], v[88:89], 0 op_sel_hi:[0,1,0] neg_lo:[1,0,0] neg_hi:[1,0,0]
	v_cvt_pk_bf16_f32 v86, v86, v87
	v_cvt_pk_bf16_f32 v87, v88, v89
	ds_write_b64 v186, v[86:87]
	ds_read_b32 v86, v187 offset:200
	s_waitcnt lgkmcnt(0)
	v_pk_fma_f32 v[78:79], v[86:87], v[78:79], 0 op_sel_hi:[0,1,0] neg_lo:[1,0,0] neg_hi:[1,0,0]
	v_pk_fma_f32 v[80:81], v[86:87], v[80:81], 0 op_sel_hi:[0,1,0] neg_lo:[1,0,0] neg_hi:[1,0,0]
	v_cvt_pk_bf16_f32 v78, v78, v79
	v_cvt_pk_bf16_f32 v79, v80, v81
	ds_write_b64 v186, v[78:79] offset:544
	ds_read_b32 v78, v187 offset:208
	s_waitcnt lgkmcnt(0)
	v_pk_fma_f32 v[66:67], v[78:79], v[66:67], 0 op_sel_hi:[0,1,0] neg_lo:[1,0,0] neg_hi:[1,0,0]
	v_pk_fma_f32 v[68:69], v[78:79], v[68:69], 0 op_sel_hi:[0,1,0] neg_lo:[1,0,0] neg_hi:[1,0,0]
	v_cvt_pk_bf16_f32 v66, v66, v67
	v_cvt_pk_bf16_f32 v67, v68, v69
	ds_write_b64 v186, v[66:67] offset:1088
	ds_read_b32 v66, v187 offset:216
	s_waitcnt lgkmcnt(0)
	v_pk_fma_f32 v[42:43], v[66:67], v[42:43], 0 op_sel_hi:[0,1,0] neg_lo:[1,0,0] neg_hi:[1,0,0]
	v_pk_fma_f32 v[44:45], v[66:67], v[44:45], 0 op_sel_hi:[0,1,0] neg_lo:[1,0,0] neg_hi:[1,0,0]
	v_cvt_pk_bf16_f32 v42, v42, v43
	v_cvt_pk_bf16_f32 v43, v44, v45
	ds_write_b64 v186, v[42:43] offset:1632
	ds_read_b32 v42, v187 offset:224
	s_waitcnt lgkmcnt(0)
	v_pk_fma_f32 v[38:39], v[42:43], v[38:39], 0 op_sel_hi:[0,1,0] neg_lo:[1,0,0] neg_hi:[1,0,0]
	v_pk_fma_f32 v[40:41], v[42:43], v[40:41], 0 op_sel_hi:[0,1,0] neg_lo:[1,0,0] neg_hi:[1,0,0]
	v_cvt_pk_bf16_f32 v38, v38, v39
	v_cvt_pk_bf16_f32 v39, v40, v41
	ds_write_b64 v186, v[38:39] offset:2176
	ds_read_b32 v38, v187 offset:232
	s_waitcnt lgkmcnt(0)
	v_pk_fma_f32 v[18:19], v[38:39], v[18:19], 0 op_sel_hi:[0,1,0] neg_lo:[1,0,0] neg_hi:[1,0,0]
	v_pk_fma_f32 v[20:21], v[38:39], v[20:21], 0 op_sel_hi:[0,1,0] neg_lo:[1,0,0] neg_hi:[1,0,0]
	v_cvt_pk_bf16_f32 v18, v18, v19
	v_cvt_pk_bf16_f32 v19, v20, v21
	ds_write_b64 v186, v[18:19] offset:2720
	ds_read_b32 v18, v187 offset:240
	s_waitcnt lgkmcnt(0)
	v_pk_fma_f32 v[10:11], v[18:19], v[10:11], 0 op_sel_hi:[0,1,0] neg_lo:[1,0,0] neg_hi:[1,0,0]
	v_pk_fma_f32 v[12:13], v[18:19], v[12:13], 0 op_sel_hi:[0,1,0] neg_lo:[1,0,0] neg_hi:[1,0,0]
	v_cvt_pk_bf16_f32 v10, v10, v11
	v_cvt_pk_bf16_f32 v11, v12, v13
	ds_write_b64 v186, v[10:11] offset:3264
	ds_read_b32 v10, v187 offset:248
	s_waitcnt lgkmcnt(0)
	v_pk_fma_f32 v[2:3], v[10:11], v[2:3], 0 op_sel_hi:[0,1,0] neg_lo:[1,0,0] neg_hi:[1,0,0]
	v_pk_fma_f32 v[4:5], v[10:11], v[4:5], 0 op_sel_hi:[0,1,0] neg_lo:[1,0,0] neg_hi:[1,0,0]
	v_cvt_pk_bf16_f32 v2, v2, v3
	v_cvt_pk_bf16_f32 v3, v4, v5
	ds_write_b64 v186, v[2:3] offset:3808
	ds_read_b128 v[2:5], v1
	s_waitcnt lgkmcnt(0)
	ds_write_b128 v184, v[2:5] offset:28672
	ds_read_b128 v[2:5], v1 offset:64
	s_waitcnt lgkmcnt(0)
	ds_write_b128 v184, v[2:5] offset:29696
	ds_read_b128 v[2:5], v1 offset:128
	s_waitcnt lgkmcnt(0)
	ds_write_b128 v184, v[2:5] offset:30720
	ds_read_b128 v[2:5], v1 offset:192
	s_waitcnt lgkmcnt(0)
	ds_write_b128 v184, v[2:5] offset:31744
	s_mov_b64 s[44:45], 0x20000
	v_lshl_add_u64 v[168:169], v[130:131], 0, s[44:45]
	s_mov_b64 s[44:45], 0x22000
	v_lshl_add_u64 v[170:171], v[130:131], 0, s[44:45]
	s_mov_b64 s[44:45], 0x24000
	v_lshl_add_u64 v[172:173], v[130:131], 0, s[44:45]
	s_mov_b64 s[44:45], 0x26000
	v_lshl_add_u64 v[174:175], v[130:131], 0, s[44:45]
	s_mov_b64 s[44:45], 0x28000
	v_lshl_add_u64 v[176:177], v[130:131], 0, s[44:45]
	s_mov_b64 s[44:45], 0x2a000
	v_lshl_add_u64 v[178:179], v[130:131], 0, s[44:45]
	s_mov_b64 s[44:45], 0x2c000
	v_lshl_add_u64 v[180:181], v[130:131], 0, s[44:45]
	s_mov_b64 s[44:45], 0x2e000
	v_lshl_add_u64 v[2:3], v[168:169], 0, s[30:31]
	v_lshl_add_u64 v[4:5], v[170:171], 0, s[30:31]
	v_lshl_add_u64 v[10:11], v[172:173], 0, s[30:31]
	v_lshl_add_u64 v[12:13], v[174:175], 0, s[30:31]
	v_lshl_add_u64 v[18:19], v[176:177], 0, s[30:31]
	v_lshl_add_u64 v[20:21], v[178:179], 0, s[30:31]
	v_lshl_add_u64 v[182:183], v[130:131], 0, s[44:45]
	v_lshl_add_u64 v[42:43], v[180:181], 0, s[30:31]
	v_lshl_add_u64 v[44:45], v[182:183], 0, s[30:31]
	global_load_dwordx4 v[106:109], v[2:3], off nt
	global_load_dwordx4 v[98:101], v[4:5], off nt
	global_load_dwordx4 v[78:81], v[10:11], off nt
	global_load_dwordx4 v[66:69], v[12:13], off nt
	global_load_dwordx4 v[38:41], v[18:19], off nt
	s_nop 0
	global_load_dwordx4 v[18:21], v[20:21], off nt
	s_nop 0
	global_load_dwordx4 v[10:13], v[42:43], off nt
	global_load_dwordx4 v[2:5], v[44:45], off nt
	v_mov_b32_e32 v42, v198
	s_waitcnt vmcnt(23)
	s_waitcnt vmcnt(22)
	s_waitcnt vmcnt(21)
	s_waitcnt vmcnt(20)
	s_waitcnt vmcnt(19)
	s_waitcnt vmcnt(18)
	s_waitcnt vmcnt(17)
	s_waitcnt vmcnt(16)
	ds_read_b32 v42, v187
	s_waitcnt lgkmcnt(0)
	v_pk_fma_f32 v[44:45], v[42:43], v[74:75], 0 op_sel_hi:[0,1,0] neg_lo:[1,0,0] neg_hi:[1,0,0]
	v_pk_fma_f32 v[42:43], v[42:43], v[76:77], 0 op_sel_hi:[0,1,0] neg_lo:[1,0,0] neg_hi:[1,0,0]
	v_cvt_pk_bf16_f32 v44, v44, v45
	v_cvt_pk_bf16_f32 v45, v42, v43
	ds_write_b64 v186, v[44:45]
	ds_read_b32 v42, v187 offset:8
	s_waitcnt lgkmcnt(0)
	v_pk_fma_f32 v[44:45], v[42:43], v[62:63], 0 op_sel_hi:[0,1,0] neg_lo:[1,0,0] neg_hi:[1,0,0]
	v_pk_fma_f32 v[42:43], v[42:43], v[64:65], 0 op_sel_hi:[0,1,0] neg_lo:[1,0,0] neg_hi:[1,0,0]
	v_cvt_pk_bf16_f32 v44, v44, v45
	v_cvt_pk_bf16_f32 v45, v42, v43
	ds_write_b64 v186, v[44:45] offset:544
	ds_read_b32 v42, v187 offset:16
	s_waitcnt lgkmcnt(0)
	v_pk_fma_f32 v[44:45], v[42:43], v[58:59], 0 op_sel_hi:[0,1,0] neg_lo:[1,0,0] neg_hi:[1,0,0]
	v_pk_fma_f32 v[42:43], v[42:43], v[60:61], 0 op_sel_hi:[0,1,0] neg_lo:[1,0,0] neg_hi:[1,0,0]
	v_cvt_pk_bf16_f32 v44, v44, v45
	v_cvt_pk_bf16_f32 v45, v42, v43
	ds_write_b64 v186, v[44:45] offset:1088
	ds_read_b32 v42, v187 offset:24
	s_waitcnt lgkmcnt(0)
	v_pk_fma_f32 v[44:45], v[42:43], v[46:47], 0 op_sel_hi:[0,1,0] neg_lo:[1,0,0] neg_hi:[1,0,0]
	v_pk_fma_f32 v[42:43], v[42:43], v[48:49], 0 op_sel_hi:[0,1,0] neg_lo:[1,0,0] neg_hi:[1,0,0]
	v_cvt_pk_bf16_f32 v44, v44, v45
	v_cvt_pk_bf16_f32 v45, v42, v43
	ds_write_b64 v186, v[44:45] offset:1632
	ds_read_b32 v42, v187 offset:32
	s_waitcnt lgkmcnt(0)
	v_pk_fma_f32 v[44:45], v[42:43], v[50:51], 0 op_sel_hi:[0,1,0] neg_lo:[1,0,0] neg_hi:[1,0,0]
	v_pk_fma_f32 v[42:43], v[42:43], v[52:53], 0 op_sel_hi:[0,1,0] neg_lo:[1,0,0] neg_hi:[1,0,0]
	v_cvt_pk_bf16_f32 v44, v44, v45
	v_cvt_pk_bf16_f32 v45, v42, v43
	ds_write_b64 v186, v[44:45] offset:2176
	ds_read_b32 v42, v187 offset:40
	s_waitcnt lgkmcnt(0)
	v_pk_fma_f32 v[30:31], v[42:43], v[30:31], 0 op_sel_hi:[0,1,0] neg_lo:[1,0,0] neg_hi:[1,0,0]
	v_pk_fma_f32 v[32:33], v[42:43], v[32:33], 0 op_sel_hi:[0,1,0] neg_lo:[1,0,0] neg_hi:[1,0,0]
	v_cvt_pk_bf16_f32 v30, v30, v31
	v_cvt_pk_bf16_f32 v31, v32, v33
	ds_write_b64 v186, v[30:31] offset:2720
	ds_read_b32 v30, v187 offset:48
	s_waitcnt lgkmcnt(0)
	v_pk_fma_f32 v[32:33], v[30:31], v[34:35], 0 op_sel_hi:[0,1,0] neg_lo:[1,0,0] neg_hi:[1,0,0]
	v_pk_fma_f32 v[30:31], v[30:31], v[36:37], 0 op_sel_hi:[0,1,0] neg_lo:[1,0,0] neg_hi:[1,0,0]
	v_cvt_pk_bf16_f32 v32, v32, v33
	v_cvt_pk_bf16_f32 v33, v30, v31
	ds_write_b64 v186, v[32:33] offset:3264
	ds_read_b32 v30, v187 offset:56
	s_waitcnt lgkmcnt(0)
	v_pk_fma_f32 v[22:23], v[30:31], v[22:23], 0 op_sel_hi:[0,1,0] neg_lo:[1,0,0] neg_hi:[1,0,0]
	v_pk_fma_f32 v[24:25], v[30:31], v[24:25], 0 op_sel_hi:[0,1,0] neg_lo:[1,0,0] neg_hi:[1,0,0]
	v_cvt_pk_bf16_f32 v22, v22, v23
	v_cvt_pk_bf16_f32 v23, v24, v25
	ds_write_b64 v186, v[22:23] offset:3808
	ds_read_b128 a[0:3], v1
	ds_read_b128 a[4:7], v1 offset:64
	ds_read_b128 a[8:11], v1 offset:128
	ds_read_b128 a[12:15], v1 offset:192
	v_lshl_add_u64 v[22:23], v[130:131], 0, s[28:29]
	v_add_co_u32_e32 v24, vcc, s7, v22
	s_nop 1
	v_addc_co_u32_e32 v25, vcc, 0, v23, vcc
	global_load_dwordx4 v[102:105], v[22:23], off nt
	global_load_dwordx4 v[86:89], v[24:25], off nt
	v_add_co_u32_e32 v24, vcc, s36, v22
	s_nop 1
	v_addc_co_u32_e32 v25, vcc, 0, v23, vcc
	v_add_co_u32_e32 v30, vcc, s37, v22
	s_nop 1
	v_addc_co_u32_e32 v31, vcc, 0, v23, vcc
	global_load_dwordx4 v[74:77], v[24:25], off nt
	global_load_dwordx4 v[62:65], v[30:31], off nt
	v_add_co_u32_e32 v24, vcc, s38, v22
	s_nop 1
	v_addc_co_u32_e32 v25, vcc, 0, v23, vcc
	v_add_co_u32_e32 v30, vcc, s39, v22
	s_nop 1
	v_addc_co_u32_e32 v31, vcc, 0, v23, vcc
	global_load_dwordx4 v[58:61], v[24:25], off nt
	global_load_dwordx4 v[46:49], v[30:31], off nt
	v_add_co_u32_e32 v24, vcc, s41, v22
	s_nop 1
	v_addc_co_u32_e32 v25, vcc, 0, v23, vcc
	v_add_co_u32_e32 v22, vcc, s42, v22
	s_nop 1
	v_addc_co_u32_e32 v23, vcc, 0, v23, vcc
	global_load_dwordx4 v[42:45], v[24:25], off nt
	global_load_dwordx4 v[30:33], v[22:23], off nt
	v_mov_b32_e32 v22, v198
	s_waitcnt vmcnt(23)
	s_waitcnt vmcnt(22)
	s_waitcnt vmcnt(21)
	s_waitcnt vmcnt(20)
	s_waitcnt vmcnt(19)
	s_waitcnt vmcnt(18)
	s_waitcnt vmcnt(17)
	s_waitcnt vmcnt(16)
	ds_read_b32 v22, v187 offset:64
	s_waitcnt lgkmcnt(0)
	v_pk_fma_f32 v[24:25], v[22:23], v[94:95], 0 op_sel_hi:[0,1,0] neg_lo:[1,0,0] neg_hi:[1,0,0]
	v_pk_fma_f32 v[22:23], v[22:23], v[96:97], 0 op_sel_hi:[0,1,0] neg_lo:[1,0,0] neg_hi:[1,0,0]
	v_cvt_pk_bf16_f32 v24, v24, v25
	v_cvt_pk_bf16_f32 v25, v22, v23
	ds_write_b64 v186, v[24:25]
	ds_read_b32 v22, v187 offset:72
	s_waitcnt lgkmcnt(0)
	v_pk_fma_f32 v[24:25], v[22:23], v[90:91], 0 op_sel_hi:[0,1,0] neg_lo:[1,0,0] neg_hi:[1,0,0]
	v_pk_fma_f32 v[22:23], v[22:23], v[92:93], 0 op_sel_hi:[0,1,0] neg_lo:[1,0,0] neg_hi:[1,0,0]
	v_cvt_pk_bf16_f32 v24, v24, v25
	v_cvt_pk_bf16_f32 v25, v22, v23
	ds_write_b64 v186, v[24:25] offset:544
	ds_read_b32 v22, v187 offset:80
	s_waitcnt lgkmcnt(0)
	v_pk_fma_f32 v[24:25], v[22:23], v[82:83], 0 op_sel_hi:[0,1,0] neg_lo:[1,0,0] neg_hi:[1,0,0]
	v_pk_fma_f32 v[22:23], v[22:23], v[84:85], 0 op_sel_hi:[0,1,0] neg_lo:[1,0,0] neg_hi:[1,0,0]
	v_cvt_pk_bf16_f32 v24, v24, v25
	v_cvt_pk_bf16_f32 v25, v22, v23
	ds_write_b64 v186, v[24:25] offset:1088
	ds_read_b32 v22, v187 offset:88
	s_waitcnt lgkmcnt(0)
	v_pk_fma_f32 v[24:25], v[22:23], v[70:71], 0 op_sel_hi:[0,1,0] neg_lo:[1,0,0] neg_hi:[1,0,0]
	v_pk_fma_f32 v[22:23], v[22:23], v[72:73], 0 op_sel_hi:[0,1,0] neg_lo:[1,0,0] neg_hi:[1,0,0]
	v_cvt_pk_bf16_f32 v24, v24, v25
	v_cvt_pk_bf16_f32 v25, v22, v23
	ds_write_b64 v186, v[24:25] offset:1632
	ds_read_b32 v22, v187 offset:96
	s_waitcnt lgkmcnt(0)
	v_pk_fma_f32 v[24:25], v[22:23], v[54:55], 0 op_sel_hi:[0,1,0] neg_lo:[1,0,0] neg_hi:[1,0,0]
	v_pk_fma_f32 v[22:23], v[22:23], v[56:57], 0 op_sel_hi:[0,1,0] neg_lo:[1,0,0] neg_hi:[1,0,0]
	v_cvt_pk_bf16_f32 v24, v24, v25
	v_cvt_pk_bf16_f32 v25, v22, v23
	ds_write_b64 v186, v[24:25] offset:2176
	ds_read_b32 v22, v187 offset:104
	s_waitcnt lgkmcnt(0)
	v_pk_fma_f32 v[24:25], v[22:23], v[26:27], 0 op_sel_hi:[0,1,0] neg_lo:[1,0,0] neg_hi:[1,0,0]
	v_pk_fma_f32 v[22:23], v[22:23], v[28:29], 0 op_sel_hi:[0,1,0] neg_lo:[1,0,0] neg_hi:[1,0,0]
	v_cvt_pk_bf16_f32 v24, v24, v25
	v_cvt_pk_bf16_f32 v25, v22, v23
	ds_write_b64 v186, v[24:25] offset:2720
	ds_read_b32 v22, v187 offset:112
	s_waitcnt lgkmcnt(0)
	v_pk_fma_f32 v[14:15], v[22:23], v[14:15], 0 op_sel_hi:[0,1,0] neg_lo:[1,0,0] neg_hi:[1,0,0]
	v_pk_fma_f32 v[16:17], v[22:23], v[16:17], 0 op_sel_hi:[0,1,0] neg_lo:[1,0,0] neg_hi:[1,0,0]
	v_cvt_pk_bf16_f32 v14, v14, v15
	v_cvt_pk_bf16_f32 v15, v16, v17
	ds_write_b64 v186, v[14:15] offset:3264
	ds_read_b32 v14, v187 offset:120
	s_waitcnt lgkmcnt(0)
	v_pk_fma_f32 v[6:7], v[14:15], v[6:7], 0 op_sel_hi:[0,1,0] neg_lo:[1,0,0] neg_hi:[1,0,0]
	v_pk_fma_f32 v[8:9], v[14:15], v[8:9], 0 op_sel_hi:[0,1,0] neg_lo:[1,0,0] neg_hi:[1,0,0]
	v_cvt_pk_bf16_f32 v6, v6, v7
	v_cvt_pk_bf16_f32 v7, v8, v9
	ds_write_b64 v186, v[6:7] offset:3808
	ds_read_b128 a[16:19], v1
	ds_read_b128 a[20:23], v1 offset:64
	ds_read_b128 a[24:27], v1 offset:128
	ds_read_b128 a[28:31], v1 offset:192
	v_lshl_add_u64 v[6:7], v[150:151], 0, s[28:29]
	v_lshl_add_u64 v[8:9], v[152:153], 0, s[28:29]
	v_lshl_add_u64 v[14:15], v[156:157], 0, s[28:29]
	v_lshl_add_u64 v[16:17], v[158:159], 0, s[28:29]
	v_lshl_add_u64 v[22:23], v[160:161], 0, s[28:29]
	v_lshl_add_u64 v[24:25], v[162:163], 0, s[28:29]
	v_lshl_add_u64 v[26:27], v[164:165], 0, s[28:29]
	v_lshl_add_u64 v[28:29], v[166:167], 0, s[28:29]
	global_load_dwordx4 v[110:113], v[6:7], off nt
	global_load_dwordx4 v[90:93], v[8:9], off nt
	global_load_dwordx4 v[70:73], v[14:15], off nt
	global_load_dwordx4 v[50:53], v[16:17], off nt
	global_load_dwordx4 v[34:37], v[22:23], off nt
	s_nop 0
	global_load_dwordx4 v[22:25], v[24:25], off nt
	s_nop 0
	global_load_dwordx4 v[14:17], v[26:27], off nt
	global_load_dwordx4 v[6:9], v[28:29], off nt
	s_waitcnt vmcnt(23)
	s_waitcnt vmcnt(22)
	s_waitcnt vmcnt(21)
	s_waitcnt vmcnt(20)
	s_waitcnt vmcnt(19)
	s_waitcnt vmcnt(18)
	s_waitcnt vmcnt(17)
	s_waitcnt vmcnt(16)
	ds_read_b32 v26, v187 offset:128
	s_waitcnt lgkmcnt(0)
	v_pk_fma_f32 v[28:29], v[26:27], v[106:107], 0 op_sel_hi:[0,1,0] neg_lo:[1,0,0] neg_hi:[1,0,0]
	v_pk_fma_f32 v[26:27], v[26:27], v[108:109], 0 op_sel_hi:[0,1,0] neg_lo:[1,0,0] neg_hi:[1,0,0]
	v_cvt_pk_bf16_f32 v28, v28, v29
	v_cvt_pk_bf16_f32 v29, v26, v27
	ds_write_b64 v186, v[28:29]
	ds_read_b32 v26, v187 offset:136
	s_waitcnt lgkmcnt(0)
	v_pk_fma_f32 v[28:29], v[26:27], v[98:99], 0 op_sel_hi:[0,1,0] neg_lo:[1,0,0] neg_hi:[1,0,0]
	v_pk_fma_f32 v[26:27], v[26:27], v[100:101], 0 op_sel_hi:[0,1,0] neg_lo:[1,0,0] neg_hi:[1,0,0]
	v_cvt_pk_bf16_f32 v28, v28, v29
	v_cvt_pk_bf16_f32 v29, v26, v27
	ds_write_b64 v186, v[28:29] offset:544
	ds_read_b32 v26, v187 offset:144
	s_waitcnt lgkmcnt(0)
	v_pk_fma_f32 v[28:29], v[26:27], v[78:79], 0 op_sel_hi:[0,1,0] neg_lo:[1,0,0] neg_hi:[1,0,0]
	v_pk_fma_f32 v[26:27], v[26:27], v[80:81], 0 op_sel_hi:[0,1,0] neg_lo:[1,0,0] neg_hi:[1,0,0]
	v_cvt_pk_bf16_f32 v28, v28, v29
	v_cvt_pk_bf16_f32 v29, v26, v27
	ds_write_b64 v186, v[28:29] offset:1088
	ds_read_b32 v26, v187 offset:152
	s_waitcnt lgkmcnt(0)
	v_pk_fma_f32 v[28:29], v[26:27], v[66:67], 0 op_sel_hi:[0,1,0] neg_lo:[1,0,0] neg_hi:[1,0,0]
	v_pk_fma_f32 v[26:27], v[26:27], v[68:69], 0 op_sel_hi:[0,1,0] neg_lo:[1,0,0] neg_hi:[1,0,0]
	v_cvt_pk_bf16_f32 v28, v28, v29
	v_cvt_pk_bf16_f32 v29, v26, v27
	ds_write_b64 v186, v[28:29] offset:1632
	ds_read_b32 v26, v187 offset:160
	s_waitcnt lgkmcnt(0)
	v_pk_fma_f32 v[28:29], v[26:27], v[38:39], 0 op_sel_hi:[0,1,0] neg_lo:[1,0,0] neg_hi:[1,0,0]
	v_pk_fma_f32 v[26:27], v[26:27], v[40:41], 0 op_sel_hi:[0,1,0] neg_lo:[1,0,0] neg_hi:[1,0,0]
	v_cvt_pk_bf16_f32 v28, v28, v29
	v_cvt_pk_bf16_f32 v29, v26, v27
	ds_write_b64 v186, v[28:29] offset:2176
	ds_read_b32 v26, v187 offset:168
	s_waitcnt lgkmcnt(0)
	v_pk_fma_f32 v[18:19], v[26:27], v[18:19], 0 op_sel_hi:[0,1,0] neg_lo:[1,0,0] neg_hi:[1,0,0]
	v_pk_fma_f32 v[20:21], v[26:27], v[20:21], 0 op_sel_hi:[0,1,0] neg_lo:[1,0,0] neg_hi:[1,0,0]
	v_cvt_pk_bf16_f32 v18, v18, v19
	v_cvt_pk_bf16_f32 v19, v20, v21
	ds_write_b64 v186, v[18:19] offset:2720
	ds_read_b32 v18, v187 offset:176
	s_waitcnt lgkmcnt(0)
	v_pk_fma_f32 v[10:11], v[18:19], v[10:11], 0 op_sel_hi:[0,1,0] neg_lo:[1,0,0] neg_hi:[1,0,0]
	v_pk_fma_f32 v[12:13], v[18:19], v[12:13], 0 op_sel_hi:[0,1,0] neg_lo:[1,0,0] neg_hi:[1,0,0]
	v_cvt_pk_bf16_f32 v10, v10, v11
	v_cvt_pk_bf16_f32 v11, v12, v13
	ds_write_b64 v186, v[10:11] offset:3264
	ds_read_b32 v10, v187 offset:184
	s_waitcnt lgkmcnt(0)
	v_pk_fma_f32 v[2:3], v[10:11], v[2:3], 0 op_sel_hi:[0,1,0] neg_lo:[1,0,0] neg_hi:[1,0,0]
	v_pk_fma_f32 v[4:5], v[10:11], v[4:5], 0 op_sel_hi:[0,1,0] neg_lo:[1,0,0] neg_hi:[1,0,0]
	v_cvt_pk_bf16_f32 v2, v2, v3
	v_cvt_pk_bf16_f32 v3, v4, v5
	ds_write_b64 v186, v[2:3] offset:3808
	ds_read_b128 a[32:35], v1
	ds_read_b128 a[36:39], v1 offset:64
	ds_read_b128 a[40:43], v1 offset:128
	ds_read_b128 a[44:47], v1 offset:192
	v_lshl_add_u64 v[2:3], v[168:169], 0, s[28:29]
	v_lshl_add_u64 v[4:5], v[170:171], 0, s[28:29]
	v_lshl_add_u64 v[10:11], v[172:173], 0, s[28:29]
	v_lshl_add_u64 v[12:13], v[174:175], 0, s[28:29]
	v_lshl_add_u64 v[18:19], v[176:177], 0, s[28:29]
	v_lshl_add_u64 v[20:21], v[178:179], 0, s[28:29]
	v_lshl_add_u64 v[26:27], v[180:181], 0, s[28:29]
	v_lshl_add_u64 v[28:29], v[182:183], 0, s[28:29]
	global_load_dwordx4 v[106:109], v[2:3], off nt
	global_load_dwordx4 v[94:97], v[4:5], off nt
	global_load_dwordx4 v[66:69], v[10:11], off nt
	global_load_dwordx4 v[54:57], v[12:13], off nt
	global_load_dwordx4 v[38:41], v[18:19], off nt
	s_nop 0
	global_load_dwordx4 v[18:21], v[20:21], off nt
	s_nop 0
	global_load_dwordx4 v[10:13], v[26:27], off nt
	global_load_dwordx4 v[2:5], v[28:29], off nt
	v_mov_b32_e32 v26, v197
	s_waitcnt vmcnt(23)
	s_waitcnt vmcnt(22)
	s_waitcnt vmcnt(21)
	s_waitcnt vmcnt(20)
	s_waitcnt vmcnt(19)
	s_waitcnt vmcnt(18)
	s_waitcnt vmcnt(17)
	s_waitcnt vmcnt(16)
	ds_read_b32 v26, v187
	s_waitcnt lgkmcnt(0)
	v_pk_fma_f32 v[28:29], v[26:27], v[102:103], 0 op_sel_hi:[0,1,0] neg_lo:[1,0,0] neg_hi:[1,0,0]
	v_pk_fma_f32 v[26:27], v[26:27], v[104:105], 0 op_sel_hi:[0,1,0] neg_lo:[1,0,0] neg_hi:[1,0,0]
	v_cvt_pk_bf16_f32 v28, v28, v29
	v_cvt_pk_bf16_f32 v29, v26, v27
	ds_write_b64 v186, v[28:29]
	ds_read_b32 v26, v187 offset:8
	s_waitcnt lgkmcnt(0)
	v_pk_fma_f32 v[28:29], v[26:27], v[86:87], 0 op_sel_hi:[0,1,0] neg_lo:[1,0,0] neg_hi:[1,0,0]
	v_pk_fma_f32 v[26:27], v[26:27], v[88:89], 0 op_sel_hi:[0,1,0] neg_lo:[1,0,0] neg_hi:[1,0,0]
	v_cvt_pk_bf16_f32 v28, v28, v29
	v_cvt_pk_bf16_f32 v29, v26, v27
	ds_write_b64 v186, v[28:29] offset:544
	ds_read_b32 v26, v187 offset:16
	s_waitcnt lgkmcnt(0)
	v_pk_fma_f32 v[28:29], v[26:27], v[74:75], 0 op_sel_hi:[0,1,0] neg_lo:[1,0,0] neg_hi:[1,0,0]
	v_pk_fma_f32 v[26:27], v[26:27], v[76:77], 0 op_sel_hi:[0,1,0] neg_lo:[1,0,0] neg_hi:[1,0,0]
	v_cvt_pk_bf16_f32 v28, v28, v29
	v_cvt_pk_bf16_f32 v29, v26, v27
	ds_write_b64 v186, v[28:29] offset:1088
	ds_read_b32 v26, v187 offset:24
	s_waitcnt lgkmcnt(0)
	v_pk_fma_f32 v[28:29], v[26:27], v[62:63], 0 op_sel_hi:[0,1,0] neg_lo:[1,0,0] neg_hi:[1,0,0]
	v_pk_fma_f32 v[26:27], v[26:27], v[64:65], 0 op_sel_hi:[0,1,0] neg_lo:[1,0,0] neg_hi:[1,0,0]
	v_cvt_pk_bf16_f32 v28, v28, v29
	v_cvt_pk_bf16_f32 v29, v26, v27
	ds_write_b64 v186, v[28:29] offset:1632
	ds_read_b32 v26, v187 offset:32
	s_waitcnt lgkmcnt(0)
	v_pk_fma_f32 v[28:29], v[26:27], v[58:59], 0 op_sel_hi:[0,1,0] neg_lo:[1,0,0] neg_hi:[1,0,0]
	v_pk_fma_f32 v[26:27], v[26:27], v[60:61], 0 op_sel_hi:[0,1,0] neg_lo:[1,0,0] neg_hi:[1,0,0]
	v_cvt_pk_bf16_f32 v28, v28, v29
	v_cvt_pk_bf16_f32 v29, v26, v27
	ds_write_b64 v186, v[28:29] offset:2176
	ds_read_b32 v26, v187 offset:40
	s_waitcnt lgkmcnt(0)
	v_pk_fma_f32 v[28:29], v[26:27], v[46:47], 0 op_sel_hi:[0,1,0] neg_lo:[1,0,0] neg_hi:[1,0,0]
	v_pk_fma_f32 v[26:27], v[26:27], v[48:49], 0 op_sel_hi:[0,1,0] neg_lo:[1,0,0] neg_hi:[1,0,0]
	v_cvt_pk_bf16_f32 v28, v28, v29
	v_cvt_pk_bf16_f32 v29, v26, v27
	ds_write_b64 v186, v[28:29] offset:2720
	ds_read_b32 v26, v187 offset:48
	s_waitcnt lgkmcnt(0)
	v_pk_fma_f32 v[28:29], v[26:27], v[42:43], 0 op_sel_hi:[0,1,0] neg_lo:[1,0,0] neg_hi:[1,0,0]
	v_pk_fma_f32 v[26:27], v[26:27], v[44:45], 0 op_sel_hi:[0,1,0] neg_lo:[1,0,0] neg_hi:[1,0,0]
	v_cvt_pk_bf16_f32 v28, v28, v29
	v_cvt_pk_bf16_f32 v29, v26, v27
	ds_write_b64 v186, v[28:29] offset:3264
	ds_read_b32 v26, v187 offset:56
	s_waitcnt lgkmcnt(0)
	v_pk_fma_f32 v[28:29], v[26:27], v[30:31], 0 op_sel_hi:[0,1,0] neg_lo:[1,0,0] neg_hi:[1,0,0]
	v_pk_fma_f32 v[26:27], v[26:27], v[32:33], 0 op_sel_hi:[0,1,0] neg_lo:[1,0,0] neg_hi:[1,0,0]
	v_cvt_pk_bf16_f32 v28, v28, v29
	v_cvt_pk_bf16_f32 v29, v26, v27
	ds_write_b64 v186, v[28:29] offset:3808
	ds_read_b128 a[48:51], v1
	ds_read_b128 a[52:55], v1 offset:64
	ds_read_b128 a[56:59], v1 offset:128
	ds_read_b128 a[60:63], v1 offset:192
	v_lshl_add_u64 v[26:27], v[130:131], 0, s[26:27]
	v_add_co_u32_e32 v28, vcc, s7, v26
	s_nop 1
	v_addc_co_u32_e32 v29, vcc, 0, v27, vcc
	global_load_dwordx4 v[86:89], v[26:27], off nt
	global_load_dwordx4 v[82:85], v[28:29], off nt
	v_add_co_u32_e32 v28, vcc, s36, v26
	s_nop 1
	v_addc_co_u32_e32 v29, vcc, 0, v27, vcc
	v_add_co_u32_e32 v30, vcc, s37, v26
	s_nop 1
	v_addc_co_u32_e32 v31, vcc, 0, v27, vcc
	global_load_dwordx4 v[78:81], v[28:29], off nt
	global_load_dwordx4 v[58:61], v[30:31], off nt
	v_add_co_u32_e32 v28, vcc, s38, v26
	s_nop 1
	v_addc_co_u32_e32 v29, vcc, 0, v27, vcc
	v_add_co_u32_e32 v30, vcc, s39, v26
	s_nop 1
	v_addc_co_u32_e32 v31, vcc, 0, v27, vcc
	global_load_dwordx4 v[46:49], v[28:29], off nt
	global_load_dwordx4 v[42:45], v[30:31], off nt
	v_add_co_u32_e32 v28, vcc, s41, v26
	s_nop 1
	v_addc_co_u32_e32 v29, vcc, 0, v27, vcc
	v_add_co_u32_e32 v26, vcc, s42, v26
	s_nop 1
	v_addc_co_u32_e32 v27, vcc, 0, v27, vcc
	global_load_dwordx4 v[30:33], v[28:29], off nt
	s_nop 0
	global_load_dwordx4 v[26:29], v[26:27], off nt
	v_mov_b32_e32 v62, v197
	s_waitcnt vmcnt(23)
	s_waitcnt vmcnt(22)
	s_waitcnt vmcnt(21)
	s_waitcnt vmcnt(20)
	s_waitcnt vmcnt(19)
	s_waitcnt vmcnt(18)
	s_waitcnt vmcnt(17)
	s_waitcnt vmcnt(16)
	ds_read_b32 v62, v187 offset:64
	s_waitcnt lgkmcnt(0)
	v_pk_fma_f32 v[64:65], v[62:63], v[110:111], 0 op_sel_hi:[0,1,0] neg_lo:[1,0,0] neg_hi:[1,0,0]
	v_pk_fma_f32 v[62:63], v[62:63], v[112:113], 0 op_sel_hi:[0,1,0] neg_lo:[1,0,0] neg_hi:[1,0,0]
	v_cvt_pk_bf16_f32 v64, v64, v65
	v_cvt_pk_bf16_f32 v65, v62, v63
	ds_write_b64 v186, v[64:65]
	ds_read_b32 v62, v187 offset:72
	s_waitcnt lgkmcnt(0)
	v_pk_fma_f32 v[64:65], v[62:63], v[90:91], 0 op_sel_hi:[0,1,0] neg_lo:[1,0,0] neg_hi:[1,0,0]
	v_pk_fma_f32 v[62:63], v[62:63], v[92:93], 0 op_sel_hi:[0,1,0] neg_lo:[1,0,0] neg_hi:[1,0,0]
	v_cvt_pk_bf16_f32 v64, v64, v65
	v_cvt_pk_bf16_f32 v65, v62, v63
	ds_write_b64 v186, v[64:65] offset:544
	ds_read_b32 v62, v187 offset:80
	s_waitcnt lgkmcnt(0)
	v_pk_fma_f32 v[64:65], v[62:63], v[70:71], 0 op_sel_hi:[0,1,0] neg_lo:[1,0,0] neg_hi:[1,0,0]
	v_pk_fma_f32 v[62:63], v[62:63], v[72:73], 0 op_sel_hi:[0,1,0] neg_lo:[1,0,0] neg_hi:[1,0,0]
	v_cvt_pk_bf16_f32 v64, v64, v65
	v_cvt_pk_bf16_f32 v65, v62, v63
	ds_write_b64 v186, v[64:65] offset:1088
	ds_read_b32 v62, v187 offset:88
	s_waitcnt lgkmcnt(0)
	v_pk_fma_f32 v[50:51], v[62:63], v[50:51], 0 op_sel_hi:[0,1,0] neg_lo:[1,0,0] neg_hi:[1,0,0]
	v_pk_fma_f32 v[52:53], v[62:63], v[52:53], 0 op_sel_hi:[0,1,0] neg_lo:[1,0,0] neg_hi:[1,0,0]
	v_cvt_pk_bf16_f32 v50, v50, v51
	v_cvt_pk_bf16_f32 v51, v52, v53
	ds_write_b64 v186, v[50:51] offset:1632
	ds_read_b32 v50, v187 offset:96
	s_waitcnt lgkmcnt(0)
	v_pk_fma_f32 v[34:35], v[50:51], v[34:35], 0 op_sel_hi:[0,1,0] neg_lo:[1,0,0] neg_hi:[1,0,0]
	v_pk_fma_f32 v[36:37], v[50:51], v[36:37], 0 op_sel_hi:[0,1,0] neg_lo:[1,0,0] neg_hi:[1,0,0]
	v_cvt_pk_bf16_f32 v34, v34, v35
	v_cvt_pk_bf16_f32 v35, v36, v37
	ds_write_b64 v186, v[34:35] offset:2176
	ds_read_b32 v34, v187 offset:104
	s_waitcnt lgkmcnt(0)
	v_pk_fma_f32 v[22:23], v[34:35], v[22:23], 0 op_sel_hi:[0,1,0] neg_lo:[1,0,0] neg_hi:[1,0,0]
	v_pk_fma_f32 v[24:25], v[34:35], v[24:25], 0 op_sel_hi:[0,1,0] neg_lo:[1,0,0] neg_hi:[1,0,0]
	v_cvt_pk_bf16_f32 v22, v22, v23
	v_cvt_pk_bf16_f32 v23, v24, v25
	ds_write_b64 v186, v[22:23] offset:2720
	ds_read_b32 v22, v187 offset:112
	s_waitcnt lgkmcnt(0)
	v_pk_fma_f32 v[14:15], v[22:23], v[14:15], 0 op_sel_hi:[0,1,0] neg_lo:[1,0,0] neg_hi:[1,0,0]
	v_pk_fma_f32 v[16:17], v[22:23], v[16:17], 0 op_sel_hi:[0,1,0] neg_lo:[1,0,0] neg_hi:[1,0,0]
	v_cvt_pk_bf16_f32 v14, v14, v15
	v_cvt_pk_bf16_f32 v15, v16, v17
	ds_write_b64 v186, v[14:15] offset:3264
	ds_read_b32 v14, v187 offset:120
	s_waitcnt lgkmcnt(0)
	v_pk_fma_f32 v[6:7], v[14:15], v[6:7], 0 op_sel_hi:[0,1,0] neg_lo:[1,0,0] neg_hi:[1,0,0]
	v_pk_fma_f32 v[8:9], v[14:15], v[8:9], 0 op_sel_hi:[0,1,0] neg_lo:[1,0,0] neg_hi:[1,0,0]
	v_cvt_pk_bf16_f32 v6, v6, v7
	v_cvt_pk_bf16_f32 v7, v8, v9
	ds_write_b64 v186, v[6:7] offset:3808
	ds_read_b128 a[64:67], v1
	ds_read_b128 a[68:71], v1 offset:64
	ds_read_b128 a[72:75], v1 offset:128
	ds_read_b128 a[76:79], v1 offset:192
	v_lshl_add_u64 v[6:7], v[150:151], 0, s[26:27]
	v_lshl_add_u64 v[8:9], v[152:153], 0, s[26:27]
	v_lshl_add_u64 v[14:15], v[156:157], 0, s[26:27]
	v_lshl_add_u64 v[16:17], v[158:159], 0, s[26:27]
	v_lshl_add_u64 v[22:23], v[160:161], 0, s[26:27]
	v_lshl_add_u64 v[24:25], v[162:163], 0, s[26:27]
	v_lshl_add_u64 v[70:71], v[164:165], 0, s[26:27]
	v_lshl_add_u64 v[72:73], v[166:167], 0, s[26:27]
	global_load_dwordx4 v[110:113], v[6:7], off nt
	global_load_dwordx4 v[98:101], v[8:9], off nt
	global_load_dwordx4 v[62:65], v[14:15], off nt
	global_load_dwordx4 v[50:53], v[16:17], off nt
	global_load_dwordx4 v[34:37], v[22:23], off nt
	s_nop 0
	global_load_dwordx4 v[22:25], v[24:25], off nt
	s_nop 0
	global_load_dwordx4 v[14:17], v[70:71], off nt
	global_load_dwordx4 v[6:9], v[72:73], off nt
	s_waitcnt vmcnt(23)
	s_waitcnt vmcnt(22)
	s_waitcnt vmcnt(21)
	s_waitcnt vmcnt(20)
	s_waitcnt vmcnt(19)
	s_waitcnt vmcnt(18)
	s_waitcnt vmcnt(17)
	s_waitcnt vmcnt(16)
	ds_read_b32 v70, v187 offset:128
	s_waitcnt lgkmcnt(0)
	v_pk_fma_f32 v[72:73], v[70:71], v[106:107], 0 op_sel_hi:[0,1,0] neg_lo:[1,0,0] neg_hi:[1,0,0]
	v_pk_fma_f32 v[70:71], v[70:71], v[108:109], 0 op_sel_hi:[0,1,0] neg_lo:[1,0,0] neg_hi:[1,0,0]
	v_cvt_pk_bf16_f32 v72, v72, v73
	v_cvt_pk_bf16_f32 v73, v70, v71
	ds_write_b64 v186, v[72:73]
	ds_read_b32 v70, v187 offset:136
	s_waitcnt lgkmcnt(0)
	v_pk_fma_f32 v[72:73], v[70:71], v[94:95], 0 op_sel_hi:[0,1,0] neg_lo:[1,0,0] neg_hi:[1,0,0]
	v_pk_fma_f32 v[70:71], v[70:71], v[96:97], 0 op_sel_hi:[0,1,0] neg_lo:[1,0,0] neg_hi:[1,0,0]
	v_cvt_pk_bf16_f32 v72, v72, v73
	v_cvt_pk_bf16_f32 v73, v70, v71
	ds_write_b64 v186, v[72:73] offset:544
	ds_read_b32 v70, v187 offset:144
	s_waitcnt lgkmcnt(0)
	v_pk_fma_f32 v[66:67], v[70:71], v[66:67], 0 op_sel_hi:[0,1,0] neg_lo:[1,0,0] neg_hi:[1,0,0]
	v_pk_fma_f32 v[68:69], v[70:71], v[68:69], 0 op_sel_hi:[0,1,0] neg_lo:[1,0,0] neg_hi:[1,0,0]
	v_cvt_pk_bf16_f32 v66, v66, v67
	v_cvt_pk_bf16_f32 v67, v68, v69
	ds_write_b64 v186, v[66:67] offset:1088
	ds_read_b32 v66, v187 offset:152
	s_waitcnt lgkmcnt(0)
	v_pk_fma_f32 v[54:55], v[66:67], v[54:55], 0 op_sel_hi:[0,1,0] neg_lo:[1,0,0] neg_hi:[1,0,0]
	v_pk_fma_f32 v[56:57], v[66:67], v[56:57], 0 op_sel_hi:[0,1,0] neg_lo:[1,0,0] neg_hi:[1,0,0]
	v_cvt_pk_bf16_f32 v54, v54, v55
	v_cvt_pk_bf16_f32 v55, v56, v57
	ds_write_b64 v186, v[54:55] offset:1632
	ds_read_b32 v54, v187 offset:160
	s_waitcnt lgkmcnt(0)
	v_pk_fma_f32 v[38:39], v[54:55], v[38:39], 0 op_sel_hi:[0,1,0] neg_lo:[1,0,0] neg_hi:[1,0,0]
	v_pk_fma_f32 v[40:41], v[54:55], v[40:41], 0 op_sel_hi:[0,1,0] neg_lo:[1,0,0] neg_hi:[1,0,0]
	v_cvt_pk_bf16_f32 v38, v38, v39
	v_cvt_pk_bf16_f32 v39, v40, v41
	ds_write_b64 v186, v[38:39] offset:2176
	ds_read_b32 v38, v187 offset:168
	s_waitcnt lgkmcnt(0)
	v_pk_fma_f32 v[18:19], v[38:39], v[18:19], 0 op_sel_hi:[0,1,0] neg_lo:[1,0,0] neg_hi:[1,0,0]
	v_pk_fma_f32 v[20:21], v[38:39], v[20:21], 0 op_sel_hi:[0,1,0] neg_lo:[1,0,0] neg_hi:[1,0,0]
	v_cvt_pk_bf16_f32 v18, v18, v19
	v_cvt_pk_bf16_f32 v19, v20, v21
	ds_write_b64 v186, v[18:19] offset:2720
	ds_read_b32 v18, v187 offset:176
	s_waitcnt lgkmcnt(0)
	v_pk_fma_f32 v[10:11], v[18:19], v[10:11], 0 op_sel_hi:[0,1,0] neg_lo:[1,0,0] neg_hi:[1,0,0]
	v_pk_fma_f32 v[12:13], v[18:19], v[12:13], 0 op_sel_hi:[0,1,0] neg_lo:[1,0,0] neg_hi:[1,0,0]
	v_cvt_pk_bf16_f32 v10, v10, v11
	v_cvt_pk_bf16_f32 v11, v12, v13
	ds_write_b64 v186, v[10:11] offset:3264
	ds_read_b32 v10, v187 offset:184
	s_waitcnt lgkmcnt(0)
	v_pk_fma_f32 v[2:3], v[10:11], v[2:3], 0 op_sel_hi:[0,1,0] neg_lo:[1,0,0] neg_hi:[1,0,0]
	v_pk_fma_f32 v[4:5], v[10:11], v[4:5], 0 op_sel_hi:[0,1,0] neg_lo:[1,0,0] neg_hi:[1,0,0]
	v_cvt_pk_bf16_f32 v2, v2, v3
	v_cvt_pk_bf16_f32 v3, v4, v5
	ds_write_b64 v186, v[2:3] offset:3808
	ds_read_b128 a[80:83], v1
	ds_read_b128 a[84:87], v1 offset:64
	ds_read_b128 a[88:91], v1 offset:128
	ds_read_b128 a[92:95], v1 offset:192
	v_lshl_add_u64 v[2:3], v[168:169], 0, s[26:27]
	v_lshl_add_u64 v[4:5], v[170:171], 0, s[26:27]
	v_lshl_add_u64 v[10:11], v[172:173], 0, s[26:27]
	v_lshl_add_u64 v[12:13], v[174:175], 0, s[26:27]
	v_lshl_add_u64 v[18:19], v[176:177], 0, s[26:27]
	v_lshl_add_u64 v[20:21], v[178:179], 0, s[26:27]
	v_lshl_add_u64 v[66:67], v[180:181], 0, s[26:27]
	v_lshl_add_u64 v[68:69], v[182:183], 0, s[26:27]
	global_load_dwordx4 v[106:109], v[2:3], off nt
	global_load_dwordx4 v[94:97], v[4:5], off nt
	global_load_dwordx4 v[74:77], v[10:11], off nt
	global_load_dwordx4 v[54:57], v[12:13], off nt
	global_load_dwordx4 v[38:41], v[18:19], off nt
	s_nop 0
	global_load_dwordx4 v[18:21], v[20:21], off nt
	s_nop 0
	global_load_dwordx4 v[10:13], v[66:67], off nt
	global_load_dwordx4 v[2:5], v[68:69], off nt
	v_mov_b32_e32 v66, v196
	s_waitcnt vmcnt(23)
	s_waitcnt vmcnt(22)
	s_waitcnt vmcnt(21)
	s_waitcnt vmcnt(20)
	s_waitcnt vmcnt(19)
	s_waitcnt vmcnt(18)
	s_waitcnt vmcnt(17)
	s_waitcnt vmcnt(16)
	ds_read_b32 v66, v187
	s_waitcnt lgkmcnt(0)
	v_pk_fma_f32 v[68:69], v[66:67], v[86:87], 0 op_sel_hi:[0,1,0] neg_lo:[1,0,0] neg_hi:[1,0,0]
	v_pk_fma_f32 v[66:67], v[66:67], v[88:89], 0 op_sel_hi:[0,1,0] neg_lo:[1,0,0] neg_hi:[1,0,0]
	v_cvt_pk_bf16_f32 v68, v68, v69
	v_cvt_pk_bf16_f32 v69, v66, v67
	ds_write_b64 v186, v[68:69]
	ds_read_b32 v66, v187 offset:8
	s_waitcnt lgkmcnt(0)
	v_pk_fma_f32 v[68:69], v[66:67], v[82:83], 0 op_sel_hi:[0,1,0] neg_lo:[1,0,0] neg_hi:[1,0,0]
	v_pk_fma_f32 v[66:67], v[66:67], v[84:85], 0 op_sel_hi:[0,1,0] neg_lo:[1,0,0] neg_hi:[1,0,0]
	v_cvt_pk_bf16_f32 v68, v68, v69
	v_cvt_pk_bf16_f32 v69, v66, v67
	ds_write_b64 v186, v[68:69] offset:544
	ds_read_b32 v66, v187 offset:16
	s_waitcnt lgkmcnt(0)
	v_pk_fma_f32 v[68:69], v[66:67], v[78:79], 0 op_sel_hi:[0,1,0] neg_lo:[1,0,0] neg_hi:[1,0,0]
	v_pk_fma_f32 v[66:67], v[66:67], v[80:81], 0 op_sel_hi:[0,1,0] neg_lo:[1,0,0] neg_hi:[1,0,0]
	v_cvt_pk_bf16_f32 v68, v68, v69
	v_cvt_pk_bf16_f32 v69, v66, v67
	ds_write_b64 v186, v[68:69] offset:1088
	ds_read_b32 v66, v187 offset:24
	s_waitcnt lgkmcnt(0)
	v_pk_fma_f32 v[58:59], v[66:67], v[58:59], 0 op_sel_hi:[0,1,0] neg_lo:[1,0,0] neg_hi:[1,0,0]
	v_pk_fma_f32 v[60:61], v[66:67], v[60:61], 0 op_sel_hi:[0,1,0] neg_lo:[1,0,0] neg_hi:[1,0,0]
	v_cvt_pk_bf16_f32 v58, v58, v59
	v_cvt_pk_bf16_f32 v59, v60, v61
	ds_write_b64 v186, v[58:59] offset:1632
	ds_read_b32 v58, v187 offset:32
	s_waitcnt lgkmcnt(0)
	v_pk_fma_f32 v[46:47], v[58:59], v[46:47], 0 op_sel_hi:[0,1,0] neg_lo:[1,0,0] neg_hi:[1,0,0]
	v_pk_fma_f32 v[48:49], v[58:59], v[48:49], 0 op_sel_hi:[0,1,0] neg_lo:[1,0,0] neg_hi:[1,0,0]
	v_cvt_pk_bf16_f32 v46, v46, v47
	v_cvt_pk_bf16_f32 v47, v48, v49
	ds_write_b64 v186, v[46:47] offset:2176
	ds_read_b32 v46, v187 offset:40
	s_waitcnt lgkmcnt(0)
	v_pk_fma_f32 v[42:43], v[46:47], v[42:43], 0 op_sel_hi:[0,1,0] neg_lo:[1,0,0] neg_hi:[1,0,0]
	v_pk_fma_f32 v[44:45], v[46:47], v[44:45], 0 op_sel_hi:[0,1,0] neg_lo:[1,0,0] neg_hi:[1,0,0]
	v_cvt_pk_bf16_f32 v42, v42, v43
	v_cvt_pk_bf16_f32 v43, v44, v45
	ds_write_b64 v186, v[42:43] offset:2720
	ds_read_b32 v42, v187 offset:48
	s_waitcnt lgkmcnt(0)
	v_pk_fma_f32 v[30:31], v[42:43], v[30:31], 0 op_sel_hi:[0,1,0] neg_lo:[1,0,0] neg_hi:[1,0,0]
	v_pk_fma_f32 v[32:33], v[42:43], v[32:33], 0 op_sel_hi:[0,1,0] neg_lo:[1,0,0] neg_hi:[1,0,0]
	v_cvt_pk_bf16_f32 v30, v30, v31
	v_cvt_pk_bf16_f32 v31, v32, v33
	ds_write_b64 v186, v[30:31] offset:3264
	ds_read_b32 v30, v187 offset:56
	s_waitcnt lgkmcnt(0)
	v_pk_fma_f32 v[26:27], v[30:31], v[26:27], 0 op_sel_hi:[0,1,0] neg_lo:[1,0,0] neg_hi:[1,0,0]
	v_pk_fma_f32 v[28:29], v[30:31], v[28:29], 0 op_sel_hi:[0,1,0] neg_lo:[1,0,0] neg_hi:[1,0,0]
	v_cvt_pk_bf16_f32 v26, v26, v27
	v_cvt_pk_bf16_f32 v27, v28, v29
	ds_write_b64 v186, v[26:27] offset:3808
	ds_read_b128 a[96:99], v1
	ds_read_b128 a[100:103], v1 offset:64
	ds_read_b128 a[104:107], v1 offset:128
	ds_read_b128 a[108:111], v1 offset:192
	v_lshl_add_u64 v[26:27], v[130:131], 0, s[24:25]
	v_add_co_u32_e32 v28, vcc, s7, v26
	s_nop 1
	v_addc_co_u32_e32 v29, vcc, 0, v27, vcc
	global_load_dwordx4 v[102:105], v[26:27], off nt
	global_load_dwordx4 v[90:93], v[28:29], off nt
	v_add_co_u32_e32 v28, vcc, s36, v26
	s_nop 1
	v_addc_co_u32_e32 v29, vcc, 0, v27, vcc
	v_add_co_u32_e32 v30, vcc, s37, v26
	s_nop 1
	v_addc_co_u32_e32 v31, vcc, 0, v27, vcc
	global_load_dwordx4 v[86:89], v[28:29], off nt
	global_load_dwordx4 v[70:73], v[30:31], off nt
	v_add_co_u32_e32 v28, vcc, s38, v26
	s_nop 1
	v_addc_co_u32_e32 v29, vcc, 0, v27, vcc
	v_add_co_u32_e32 v30, vcc, s39, v26
	s_nop 1
	v_addc_co_u32_e32 v31, vcc, 0, v27, vcc
	global_load_dwordx4 v[66:69], v[28:29], off nt
	global_load_dwordx4 v[46:49], v[30:31], off nt
	v_add_co_u32_e32 v28, vcc, s41, v26
	s_nop 1
	v_addc_co_u32_e32 v29, vcc, 0, v27, vcc
	v_add_co_u32_e32 v26, vcc, s42, v26
	s_nop 1
	v_addc_co_u32_e32 v27, vcc, 0, v27, vcc
	global_load_dwordx4 v[42:45], v[28:29], off nt
	global_load_dwordx4 v[30:33], v[26:27], off nt
	v_mov_b32_e32 v26, v196
	s_waitcnt vmcnt(23)
	s_waitcnt vmcnt(22)
	s_waitcnt vmcnt(21)
	s_waitcnt vmcnt(20)
	s_waitcnt vmcnt(19)
	s_waitcnt vmcnt(18)
	s_waitcnt vmcnt(17)
	s_waitcnt vmcnt(16)
	ds_read_b32 v26, v187 offset:64
	s_waitcnt lgkmcnt(0)
	v_pk_fma_f32 v[28:29], v[26:27], v[110:111], 0 op_sel_hi:[0,1,0] neg_lo:[1,0,0] neg_hi:[1,0,0]
	v_pk_fma_f32 v[26:27], v[26:27], v[112:113], 0 op_sel_hi:[0,1,0] neg_lo:[1,0,0] neg_hi:[1,0,0]
	v_cvt_pk_bf16_f32 v28, v28, v29
	v_cvt_pk_bf16_f32 v29, v26, v27
	ds_write_b64 v186, v[28:29]
	ds_read_b32 v26, v187 offset:72
	s_waitcnt lgkmcnt(0)
	v_pk_fma_f32 v[28:29], v[26:27], v[98:99], 0 op_sel_hi:[0,1,0] neg_lo:[1,0,0] neg_hi:[1,0,0]
	v_pk_fma_f32 v[26:27], v[26:27], v[100:101], 0 op_sel_hi:[0,1,0] neg_lo:[1,0,0] neg_hi:[1,0,0]
	v_cvt_pk_bf16_f32 v28, v28, v29
	v_cvt_pk_bf16_f32 v29, v26, v27
	ds_write_b64 v186, v[28:29] offset:544
	ds_read_b32 v26, v187 offset:80
	s_waitcnt lgkmcnt(0)
	v_pk_fma_f32 v[28:29], v[26:27], v[62:63], 0 op_sel_hi:[0,1,0] neg_lo:[1,0,0] neg_hi:[1,0,0]
	v_pk_fma_f32 v[26:27], v[26:27], v[64:65], 0 op_sel_hi:[0,1,0] neg_lo:[1,0,0] neg_hi:[1,0,0]
	v_cvt_pk_bf16_f32 v28, v28, v29
	v_cvt_pk_bf16_f32 v29, v26, v27
	ds_write_b64 v186, v[28:29] offset:1088
	ds_read_b32 v26, v187 offset:88
	s_waitcnt lgkmcnt(0)
	v_pk_fma_f32 v[28:29], v[26:27], v[50:51], 0 op_sel_hi:[0,1,0] neg_lo:[1,0,0] neg_hi:[1,0,0]
	v_pk_fma_f32 v[26:27], v[26:27], v[52:53], 0 op_sel_hi:[0,1,0] neg_lo:[1,0,0] neg_hi:[1,0,0]
	v_cvt_pk_bf16_f32 v28, v28, v29
	v_cvt_pk_bf16_f32 v29, v26, v27
	ds_write_b64 v186, v[28:29] offset:1632
	ds_read_b32 v26, v187 offset:96
	s_waitcnt lgkmcnt(0)
	v_pk_fma_f32 v[28:29], v[26:27], v[34:35], 0 op_sel_hi:[0,1,0] neg_lo:[1,0,0] neg_hi:[1,0,0]
	v_pk_fma_f32 v[26:27], v[26:27], v[36:37], 0 op_sel_hi:[0,1,0] neg_lo:[1,0,0] neg_hi:[1,0,0]
	v_cvt_pk_bf16_f32 v28, v28, v29
	v_cvt_pk_bf16_f32 v29, v26, v27
	ds_write_b64 v186, v[28:29] offset:2176
	ds_read_b32 v26, v187 offset:104
	s_waitcnt lgkmcnt(0)
	v_pk_fma_f32 v[22:23], v[26:27], v[22:23], 0 op_sel_hi:[0,1,0] neg_lo:[1,0,0] neg_hi:[1,0,0]
	v_pk_fma_f32 v[24:25], v[26:27], v[24:25], 0 op_sel_hi:[0,1,0] neg_lo:[1,0,0] neg_hi:[1,0,0]
	v_cvt_pk_bf16_f32 v22, v22, v23
	v_cvt_pk_bf16_f32 v23, v24, v25
	ds_write_b64 v186, v[22:23] offset:2720
	ds_read_b32 v22, v187 offset:112
	s_waitcnt lgkmcnt(0)
	v_pk_fma_f32 v[14:15], v[22:23], v[14:15], 0 op_sel_hi:[0,1,0] neg_lo:[1,0,0] neg_hi:[1,0,0]
	v_pk_fma_f32 v[16:17], v[22:23], v[16:17], 0 op_sel_hi:[0,1,0] neg_lo:[1,0,0] neg_hi:[1,0,0]
	v_cvt_pk_bf16_f32 v14, v14, v15
	v_cvt_pk_bf16_f32 v15, v16, v17
	ds_write_b64 v186, v[14:15] offset:3264
	ds_read_b32 v14, v187 offset:120
	s_waitcnt lgkmcnt(0)
	v_pk_fma_f32 v[6:7], v[14:15], v[6:7], 0 op_sel_hi:[0,1,0] neg_lo:[1,0,0] neg_hi:[1,0,0]
	v_pk_fma_f32 v[8:9], v[14:15], v[8:9], 0 op_sel_hi:[0,1,0] neg_lo:[1,0,0] neg_hi:[1,0,0]
	v_cvt_pk_bf16_f32 v6, v6, v7
	v_cvt_pk_bf16_f32 v7, v8, v9
	ds_write_b64 v186, v[6:7] offset:3808
	ds_read_b128 a[112:115], v1
	ds_read_b128 a[116:119], v1 offset:64
	ds_read_b128 a[120:123], v1 offset:128
	ds_read_b128 a[124:127], v1 offset:192
	v_lshl_add_u64 v[6:7], v[150:151], 0, s[24:25]
	v_lshl_add_u64 v[8:9], v[152:153], 0, s[24:25]
	v_lshl_add_u64 v[14:15], v[156:157], 0, s[24:25]
	v_lshl_add_u64 v[16:17], v[158:159], 0, s[24:25]
	v_lshl_add_u64 v[22:23], v[160:161], 0, s[24:25]
	v_lshl_add_u64 v[24:25], v[162:163], 0, s[24:25]
	v_lshl_add_u64 v[26:27], v[164:165], 0, s[24:25]
	v_lshl_add_u64 v[28:29], v[166:167], 0, s[24:25]
	global_load_dwordx4 v[110:113], v[6:7], off nt
	global_load_dwordx4 v[98:101], v[8:9], off nt
	global_load_dwordx4 v[78:81], v[14:15], off nt
	global_load_dwordx4 v[58:61], v[16:17], off nt
	global_load_dwordx4 v[34:37], v[22:23], off nt
	s_nop 0
	global_load_dwordx4 v[22:25], v[24:25], off nt
	s_nop 0
	global_load_dwordx4 v[14:17], v[26:27], off nt
	global_load_dwordx4 v[6:9], v[28:29], off nt
	s_waitcnt vmcnt(23)
	s_waitcnt vmcnt(22)
	s_waitcnt vmcnt(21)
	s_waitcnt vmcnt(20)
	s_waitcnt vmcnt(19)
	s_waitcnt vmcnt(18)
	s_waitcnt vmcnt(17)
	s_waitcnt vmcnt(16)
	ds_read_b32 v26, v187 offset:128
	s_waitcnt lgkmcnt(0)
	v_pk_fma_f32 v[28:29], v[26:27], v[106:107], 0 op_sel_hi:[0,1,0] neg_lo:[1,0,0] neg_hi:[1,0,0]
	v_pk_fma_f32 v[26:27], v[26:27], v[108:109], 0 op_sel_hi:[0,1,0] neg_lo:[1,0,0] neg_hi:[1,0,0]
	v_cvt_pk_bf16_f32 v28, v28, v29
	v_cvt_pk_bf16_f32 v29, v26, v27
	ds_write_b64 v186, v[28:29]
	ds_read_b32 v26, v187 offset:136
	s_waitcnt lgkmcnt(0)
	v_pk_fma_f32 v[28:29], v[26:27], v[94:95], 0 op_sel_hi:[0,1,0] neg_lo:[1,0,0] neg_hi:[1,0,0]
	v_pk_fma_f32 v[26:27], v[26:27], v[96:97], 0 op_sel_hi:[0,1,0] neg_lo:[1,0,0] neg_hi:[1,0,0]
	v_cvt_pk_bf16_f32 v28, v28, v29
	v_cvt_pk_bf16_f32 v29, v26, v27
	ds_write_b64 v186, v[28:29] offset:544
	ds_read_b32 v26, v187 offset:144
	s_waitcnt lgkmcnt(0)
	v_pk_fma_f32 v[28:29], v[26:27], v[74:75], 0 op_sel_hi:[0,1,0] neg_lo:[1,0,0] neg_hi:[1,0,0]
	v_pk_fma_f32 v[26:27], v[26:27], v[76:77], 0 op_sel_hi:[0,1,0] neg_lo:[1,0,0] neg_hi:[1,0,0]
	v_cvt_pk_bf16_f32 v28, v28, v29
	v_cvt_pk_bf16_f32 v29, v26, v27
	ds_write_b64 v186, v[28:29] offset:1088
	ds_read_b32 v26, v187 offset:152
	s_waitcnt lgkmcnt(0)
	v_pk_fma_f32 v[28:29], v[26:27], v[54:55], 0 op_sel_hi:[0,1,0] neg_lo:[1,0,0] neg_hi:[1,0,0]
	v_pk_fma_f32 v[26:27], v[26:27], v[56:57], 0 op_sel_hi:[0,1,0] neg_lo:[1,0,0] neg_hi:[1,0,0]
	v_cvt_pk_bf16_f32 v28, v28, v29
	v_cvt_pk_bf16_f32 v29, v26, v27
	ds_write_b64 v186, v[28:29] offset:1632
	ds_read_b32 v26, v187 offset:160
	s_waitcnt lgkmcnt(0)
	v_pk_fma_f32 v[28:29], v[26:27], v[38:39], 0 op_sel_hi:[0,1,0] neg_lo:[1,0,0] neg_hi:[1,0,0]
	v_pk_fma_f32 v[26:27], v[26:27], v[40:41], 0 op_sel_hi:[0,1,0] neg_lo:[1,0,0] neg_hi:[1,0,0]
	v_cvt_pk_bf16_f32 v28, v28, v29
	v_cvt_pk_bf16_f32 v29, v26, v27
	ds_write_b64 v186, v[28:29] offset:2176
	ds_read_b32 v26, v187 offset:168
	s_waitcnt lgkmcnt(0)
	v_pk_fma_f32 v[18:19], v[26:27], v[18:19], 0 op_sel_hi:[0,1,0] neg_lo:[1,0,0] neg_hi:[1,0,0]
	v_pk_fma_f32 v[20:21], v[26:27], v[20:21], 0 op_sel_hi:[0,1,0] neg_lo:[1,0,0] neg_hi:[1,0,0]
	v_cvt_pk_bf16_f32 v18, v18, v19
	v_cvt_pk_bf16_f32 v19, v20, v21
	ds_write_b64 v186, v[18:19] offset:2720
	ds_read_b32 v18, v187 offset:176
	s_waitcnt lgkmcnt(0)
	v_pk_fma_f32 v[10:11], v[18:19], v[10:11], 0 op_sel_hi:[0,1,0] neg_lo:[1,0,0] neg_hi:[1,0,0]
	v_pk_fma_f32 v[12:13], v[18:19], v[12:13], 0 op_sel_hi:[0,1,0] neg_lo:[1,0,0] neg_hi:[1,0,0]
	v_cvt_pk_bf16_f32 v10, v10, v11
	v_cvt_pk_bf16_f32 v11, v12, v13
	ds_write_b64 v186, v[10:11] offset:3264
	ds_read_b32 v10, v187 offset:184
	s_waitcnt lgkmcnt(0)
	v_pk_fma_f32 v[2:3], v[10:11], v[2:3], 0 op_sel_hi:[0,1,0] neg_lo:[1,0,0] neg_hi:[1,0,0]
	v_pk_fma_f32 v[4:5], v[10:11], v[4:5], 0 op_sel_hi:[0,1,0] neg_lo:[1,0,0] neg_hi:[1,0,0]
	v_cvt_pk_bf16_f32 v2, v2, v3
	v_cvt_pk_bf16_f32 v3, v4, v5
	ds_write_b64 v186, v[2:3] offset:3808
	ds_read_b128 a[128:131], v1
	ds_read_b128 a[132:135], v1 offset:64
	ds_read_b128 a[136:139], v1 offset:128
	ds_read_b128 a[140:143], v1 offset:192
	v_lshl_add_u64 v[2:3], v[168:169], 0, s[24:25]
	v_lshl_add_u64 v[4:5], v[170:171], 0, s[24:25]
	v_lshl_add_u64 v[10:11], v[172:173], 0, s[24:25]
	v_lshl_add_u64 v[12:13], v[174:175], 0, s[24:25]
	v_lshl_add_u64 v[18:19], v[176:177], 0, s[24:25]
	v_lshl_add_u64 v[20:21], v[178:179], 0, s[24:25]
	v_lshl_add_u64 v[50:51], v[180:181], 0, s[24:25]
	v_lshl_add_u64 v[52:53], v[182:183], 0, s[24:25]
	global_load_dwordx4 v[114:117], v[2:3], off nt
	global_load_dwordx4 v[94:97], v[4:5], off nt
	global_load_dwordx4 v[82:85], v[10:11], off nt
	global_load_dwordx4 v[62:65], v[12:13], off nt
	global_load_dwordx4 v[38:41], v[18:19], off nt
	global_load_dwordx4 v[26:29], v[20:21], off nt
	s_nop 0
	global_load_dwordx4 v[10:13], v[50:51], off nt
	global_load_dwordx4 v[2:5], v[52:53], off nt
	v_mov_b32_e32 v18, v195
	s_waitcnt vmcnt(23)
	s_waitcnt vmcnt(22)
	s_waitcnt vmcnt(21)
	s_waitcnt vmcnt(20)
	s_waitcnt vmcnt(19)
	s_waitcnt vmcnt(18)
	s_waitcnt vmcnt(17)
	s_waitcnt vmcnt(16)
	ds_read_b32 v18, v187
	s_waitcnt lgkmcnt(0)
	v_pk_fma_f32 v[20:21], v[18:19], v[102:103], 0 op_sel_hi:[0,1,0] neg_lo:[1,0,0] neg_hi:[1,0,0]
	v_pk_fma_f32 v[18:19], v[18:19], v[104:105], 0 op_sel_hi:[0,1,0] neg_lo:[1,0,0] neg_hi:[1,0,0]
	v_cvt_pk_bf16_f32 v20, v20, v21
	v_cvt_pk_bf16_f32 v21, v18, v19
	ds_write_b64 v186, v[20:21]
	ds_read_b32 v18, v187 offset:8
	s_waitcnt lgkmcnt(0)
	v_pk_fma_f32 v[20:21], v[18:19], v[90:91], 0 op_sel_hi:[0,1,0] neg_lo:[1,0,0] neg_hi:[1,0,0]
	v_pk_fma_f32 v[18:19], v[18:19], v[92:93], 0 op_sel_hi:[0,1,0] neg_lo:[1,0,0] neg_hi:[1,0,0]
	v_cvt_pk_bf16_f32 v20, v20, v21
	v_cvt_pk_bf16_f32 v21, v18, v19
	ds_write_b64 v186, v[20:21] offset:544
	ds_read_b32 v18, v187 offset:16
	s_waitcnt lgkmcnt(0)
	v_pk_fma_f32 v[20:21], v[18:19], v[86:87], 0 op_sel_hi:[0,1,0] neg_lo:[1,0,0] neg_hi:[1,0,0]
	v_pk_fma_f32 v[18:19], v[18:19], v[88:89], 0 op_sel_hi:[0,1,0] neg_lo:[1,0,0] neg_hi:[1,0,0]
	v_cvt_pk_bf16_f32 v20, v20, v21
	v_cvt_pk_bf16_f32 v21, v18, v19
	ds_write_b64 v186, v[20:21] offset:1088
	ds_read_b32 v18, v187 offset:24
	s_waitcnt lgkmcnt(0)
	v_pk_fma_f32 v[20:21], v[18:19], v[70:71], 0 op_sel_hi:[0,1,0] neg_lo:[1,0,0] neg_hi:[1,0,0]
	v_pk_fma_f32 v[18:19], v[18:19], v[72:73], 0 op_sel_hi:[0,1,0] neg_lo:[1,0,0] neg_hi:[1,0,0]
	v_cvt_pk_bf16_f32 v20, v20, v21
	v_cvt_pk_bf16_f32 v21, v18, v19
	ds_write_b64 v186, v[20:21] offset:1632
	ds_read_b32 v18, v187 offset:32
	s_waitcnt lgkmcnt(0)
	v_pk_fma_f32 v[20:21], v[18:19], v[66:67], 0 op_sel_hi:[0,1,0] neg_lo:[1,0,0] neg_hi:[1,0,0]
	v_pk_fma_f32 v[18:19], v[18:19], v[68:69], 0 op_sel_hi:[0,1,0] neg_lo:[1,0,0] neg_hi:[1,0,0]
	v_cvt_pk_bf16_f32 v20, v20, v21
	v_cvt_pk_bf16_f32 v21, v18, v19
	ds_write_b64 v186, v[20:21] offset:2176
	ds_read_b32 v18, v187 offset:40
	s_waitcnt lgkmcnt(0)
	v_pk_fma_f32 v[20:21], v[18:19], v[46:47], 0 op_sel_hi:[0,1,0] neg_lo:[1,0,0] neg_hi:[1,0,0]
	v_pk_fma_f32 v[18:19], v[18:19], v[48:49], 0 op_sel_hi:[0,1,0] neg_lo:[1,0,0] neg_hi:[1,0,0]
	v_cvt_pk_bf16_f32 v20, v20, v21
	v_cvt_pk_bf16_f32 v21, v18, v19
	ds_write_b64 v186, v[20:21] offset:2720
	ds_read_b32 v18, v187 offset:48
	s_waitcnt lgkmcnt(0)
	v_pk_fma_f32 v[20:21], v[18:19], v[42:43], 0 op_sel_hi:[0,1,0] neg_lo:[1,0,0] neg_hi:[1,0,0]
	v_pk_fma_f32 v[18:19], v[18:19], v[44:45], 0 op_sel_hi:[0,1,0] neg_lo:[1,0,0] neg_hi:[1,0,0]
	v_cvt_pk_bf16_f32 v20, v20, v21
	v_cvt_pk_bf16_f32 v21, v18, v19
	ds_write_b64 v186, v[20:21] offset:3264
	ds_read_b32 v18, v187 offset:56
	s_waitcnt lgkmcnt(0)
	v_pk_fma_f32 v[20:21], v[18:19], v[30:31], 0 op_sel_hi:[0,1,0] neg_lo:[1,0,0] neg_hi:[1,0,0]
	v_pk_fma_f32 v[18:19], v[18:19], v[32:33], 0 op_sel_hi:[0,1,0] neg_lo:[1,0,0] neg_hi:[1,0,0]
	v_cvt_pk_bf16_f32 v20, v20, v21
	v_cvt_pk_bf16_f32 v21, v18, v19
	ds_write_b64 v186, v[20:21] offset:3808
	ds_read_b128 a[144:147], v1
	ds_read_b128 a[148:151], v1 offset:64
	ds_read_b128 a[152:155], v1 offset:128
	ds_read_b128 a[156:159], v1 offset:192
	v_lshl_add_u64 v[18:19], v[130:131], 0, s[22:23]
	v_add_co_u32_e32 v20, vcc, s7, v18
	s_nop 1
	v_addc_co_u32_e32 v21, vcc, 0, v19, vcc
	global_load_dwordx4 v[106:109], v[18:19], off nt
	global_load_dwordx4 v[90:93], v[20:21], off nt
	v_add_co_u32_e32 v20, vcc, s36, v18
	s_nop 1
	v_addc_co_u32_e32 v21, vcc, 0, v19, vcc
	v_add_co_u32_e32 v30, vcc, s37, v18
	s_nop 1
	v_addc_co_u32_e32 v31, vcc, 0, v19, vcc
	global_load_dwordx4 v[86:89], v[20:21], off nt
	global_load_dwordx4 v[74:77], v[30:31], off nt
	v_add_co_u32_e32 v20, vcc, s38, v18
	s_nop 1
	v_addc_co_u32_e32 v21, vcc, 0, v19, vcc
	v_add_co_u32_e32 v30, vcc, s39, v18
	s_nop 1
	v_addc_co_u32_e32 v31, vcc, 0, v19, vcc
	global_load_dwordx4 v[70:73], v[20:21], off nt
	global_load_dwordx4 v[54:57], v[30:31], off nt
	v_add_co_u32_e32 v20, vcc, s41, v18
	s_nop 1
	v_addc_co_u32_e32 v21, vcc, 0, v19, vcc
	v_add_co_u32_e32 v18, vcc, s42, v18
	s_nop 1
	v_addc_co_u32_e32 v19, vcc, 0, v19, vcc
	global_load_dwordx4 v[50:53], v[20:21], off nt
	global_load_dwordx4 v[46:49], v[18:19], off nt
	v_mov_b32_e32 v18, v195
	s_waitcnt vmcnt(23)
	s_waitcnt vmcnt(22)
	s_waitcnt vmcnt(21)
	s_waitcnt vmcnt(20)
	s_waitcnt vmcnt(19)
	s_waitcnt vmcnt(18)
	s_waitcnt vmcnt(17)
	s_waitcnt vmcnt(16)
	ds_read_b32 v18, v187 offset:64
	s_waitcnt lgkmcnt(0)
	v_pk_fma_f32 v[20:21], v[18:19], v[110:111], 0 op_sel_hi:[0,1,0] neg_lo:[1,0,0] neg_hi:[1,0,0]
	v_pk_fma_f32 v[18:19], v[18:19], v[112:113], 0 op_sel_hi:[0,1,0] neg_lo:[1,0,0] neg_hi:[1,0,0]
	v_cvt_pk_bf16_f32 v20, v20, v21
	v_cvt_pk_bf16_f32 v21, v18, v19
	ds_write_b64 v186, v[20:21]
	ds_read_b32 v18, v187 offset:72
	s_waitcnt lgkmcnt(0)
	v_pk_fma_f32 v[20:21], v[18:19], v[98:99], 0 op_sel_hi:[0,1,0] neg_lo:[1,0,0] neg_hi:[1,0,0]
	v_pk_fma_f32 v[18:19], v[18:19], v[100:101], 0 op_sel_hi:[0,1,0] neg_lo:[1,0,0] neg_hi:[1,0,0]
	v_cvt_pk_bf16_f32 v20, v20, v21
	v_cvt_pk_bf16_f32 v21, v18, v19
	ds_write_b64 v186, v[20:21] offset:544
	ds_read_b32 v18, v187 offset:80
	s_waitcnt lgkmcnt(0)
	v_pk_fma_f32 v[20:21], v[18:19], v[78:79], 0 op_sel_hi:[0,1,0] neg_lo:[1,0,0] neg_hi:[1,0,0]
	v_pk_fma_f32 v[18:19], v[18:19], v[80:81], 0 op_sel_hi:[0,1,0] neg_lo:[1,0,0] neg_hi:[1,0,0]
	v_cvt_pk_bf16_f32 v20, v20, v21
	v_cvt_pk_bf16_f32 v21, v18, v19
	ds_write_b64 v186, v[20:21] offset:1088
	ds_read_b32 v18, v187 offset:88
	s_waitcnt lgkmcnt(0)
	v_pk_fma_f32 v[20:21], v[18:19], v[58:59], 0 op_sel_hi:[0,1,0] neg_lo:[1,0,0] neg_hi:[1,0,0]
	v_pk_fma_f32 v[18:19], v[18:19], v[60:61], 0 op_sel_hi:[0,1,0] neg_lo:[1,0,0] neg_hi:[1,0,0]
	v_cvt_pk_bf16_f32 v20, v20, v21
	v_cvt_pk_bf16_f32 v21, v18, v19
	ds_write_b64 v186, v[20:21] offset:1632
	ds_read_b32 v18, v187 offset:96
	s_waitcnt lgkmcnt(0)
	v_pk_fma_f32 v[20:21], v[18:19], v[34:35], 0 op_sel_hi:[0,1,0] neg_lo:[1,0,0] neg_hi:[1,0,0]
	v_pk_fma_f32 v[18:19], v[18:19], v[36:37], 0 op_sel_hi:[0,1,0] neg_lo:[1,0,0] neg_hi:[1,0,0]
	v_cvt_pk_bf16_f32 v20, v20, v21
	v_cvt_pk_bf16_f32 v21, v18, v19
	ds_write_b64 v186, v[20:21] offset:2176
	ds_read_b32 v18, v187 offset:104
	s_waitcnt lgkmcnt(0)
	v_pk_fma_f32 v[20:21], v[18:19], v[22:23], 0 op_sel_hi:[0,1,0] neg_lo:[1,0,0] neg_hi:[1,0,0]
	v_pk_fma_f32 v[18:19], v[18:19], v[24:25], 0 op_sel_hi:[0,1,0] neg_lo:[1,0,0] neg_hi:[1,0,0]
	v_cvt_pk_bf16_f32 v20, v20, v21
	v_cvt_pk_bf16_f32 v21, v18, v19
	ds_write_b64 v186, v[20:21] offset:2720
	ds_read_b32 v18, v187 offset:112
	s_waitcnt lgkmcnt(0)
	v_pk_fma_f32 v[14:15], v[18:19], v[14:15], 0 op_sel_hi:[0,1,0] neg_lo:[1,0,0] neg_hi:[1,0,0]
	v_pk_fma_f32 v[16:17], v[18:19], v[16:17], 0 op_sel_hi:[0,1,0] neg_lo:[1,0,0] neg_hi:[1,0,0]
	v_cvt_pk_bf16_f32 v14, v14, v15
	v_cvt_pk_bf16_f32 v15, v16, v17
	ds_write_b64 v186, v[14:15] offset:3264
	ds_read_b32 v14, v187 offset:120
	s_waitcnt lgkmcnt(0)
	v_pk_fma_f32 v[6:7], v[14:15], v[6:7], 0 op_sel_hi:[0,1,0] neg_lo:[1,0,0] neg_hi:[1,0,0]
	v_pk_fma_f32 v[8:9], v[14:15], v[8:9], 0 op_sel_hi:[0,1,0] neg_lo:[1,0,0] neg_hi:[1,0,0]
	v_cvt_pk_bf16_f32 v6, v6, v7
	v_cvt_pk_bf16_f32 v7, v8, v9
	ds_write_b64 v186, v[6:7] offset:3808
	ds_read_b128 a[160:163], v1
	ds_read_b128 a[164:167], v1 offset:64
	ds_read_b128 a[168:171], v1 offset:128
	ds_read_b128 a[172:175], v1 offset:192
	v_lshl_add_u64 v[6:7], v[150:151], 0, s[22:23]
	v_lshl_add_u64 v[18:19], v[160:161], 0, s[22:23]
	v_lshl_add_u64 v[20:21], v[162:163], 0, s[22:23]
	v_lshl_add_u64 v[22:23], v[164:165], 0, s[22:23]
	v_lshl_add_u64 v[8:9], v[152:153], 0, s[22:23]
	v_lshl_add_u64 v[14:15], v[156:157], 0, s[22:23]
	v_lshl_add_u64 v[16:17], v[158:159], 0, s[22:23]
	v_lshl_add_u64 v[34:35], v[166:167], 0, s[22:23]
	global_load_dwordx4 v[110:113], v[6:7], off nt
	global_load_dwordx4 v[98:101], v[8:9], off nt
	global_load_dwordx4 v[78:81], v[14:15], off nt
	global_load_dwordx4 v[66:69], v[16:17], off nt
	global_load_dwordx4 v[58:61], v[18:19], off nt
	global_load_dwordx4 v[30:33], v[20:21], off nt
	s_nop 0
	global_load_dwordx4 v[22:25], v[22:23], off nt
	s_nop 0
	global_load_dwordx4 v[18:21], v[34:35], off nt
	s_waitcnt vmcnt(23)
	s_waitcnt vmcnt(22)
	s_waitcnt vmcnt(21)
	s_waitcnt vmcnt(20)
	s_waitcnt vmcnt(19)
	s_waitcnt vmcnt(18)
	s_waitcnt vmcnt(17)
	s_waitcnt vmcnt(16)
	ds_read_b32 v6, v187 offset:128
	s_waitcnt lgkmcnt(0)
	v_pk_fma_f32 v[8:9], v[6:7], v[114:115], 0 op_sel_hi:[0,1,0] neg_lo:[1,0,0] neg_hi:[1,0,0]
	v_pk_fma_f32 v[6:7], v[6:7], v[116:117], 0 op_sel_hi:[0,1,0] neg_lo:[1,0,0] neg_hi:[1,0,0]
	v_cvt_pk_bf16_f32 v8, v8, v9
	v_cvt_pk_bf16_f32 v9, v6, v7
	ds_write_b64 v186, v[8:9]
	ds_read_b32 v6, v187 offset:136
	s_waitcnt lgkmcnt(0)
	v_pk_fma_f32 v[8:9], v[6:7], v[94:95], 0 op_sel_hi:[0,1,0] neg_lo:[1,0,0] neg_hi:[1,0,0]
	v_pk_fma_f32 v[6:7], v[6:7], v[96:97], 0 op_sel_hi:[0,1,0] neg_lo:[1,0,0] neg_hi:[1,0,0]
	v_cvt_pk_bf16_f32 v8, v8, v9
	v_cvt_pk_bf16_f32 v9, v6, v7
	ds_write_b64 v186, v[8:9] offset:544
	ds_read_b32 v6, v187 offset:144
	s_waitcnt lgkmcnt(0)
	v_pk_fma_f32 v[8:9], v[6:7], v[82:83], 0 op_sel_hi:[0,1,0] neg_lo:[1,0,0] neg_hi:[1,0,0]
	v_pk_fma_f32 v[6:7], v[6:7], v[84:85], 0 op_sel_hi:[0,1,0] neg_lo:[1,0,0] neg_hi:[1,0,0]
	v_cvt_pk_bf16_f32 v8, v8, v9
	v_cvt_pk_bf16_f32 v9, v6, v7
	ds_write_b64 v186, v[8:9] offset:1088
	ds_read_b32 v6, v187 offset:152
	s_waitcnt lgkmcnt(0)
	v_pk_fma_f32 v[8:9], v[6:7], v[62:63], 0 op_sel_hi:[0,1,0] neg_lo:[1,0,0] neg_hi:[1,0,0]
	v_pk_fma_f32 v[6:7], v[6:7], v[64:65], 0 op_sel_hi:[0,1,0] neg_lo:[1,0,0] neg_hi:[1,0,0]
	v_cvt_pk_bf16_f32 v8, v8, v9
	v_cvt_pk_bf16_f32 v9, v6, v7
	ds_write_b64 v186, v[8:9] offset:1632
	ds_read_b32 v6, v187 offset:160
	s_waitcnt lgkmcnt(0)
	v_pk_fma_f32 v[8:9], v[6:7], v[38:39], 0 op_sel_hi:[0,1,0] neg_lo:[1,0,0] neg_hi:[1,0,0]
	v_pk_fma_f32 v[6:7], v[6:7], v[40:41], 0 op_sel_hi:[0,1,0] neg_lo:[1,0,0] neg_hi:[1,0,0]
	v_cvt_pk_bf16_f32 v8, v8, v9
	v_cvt_pk_bf16_f32 v9, v6, v7
	ds_write_b64 v186, v[8:9] offset:2176
	ds_read_b32 v6, v187 offset:168
	s_waitcnt lgkmcnt(0)
	v_pk_fma_f32 v[8:9], v[6:7], v[26:27], 0 op_sel_hi:[0,1,0] neg_lo:[1,0,0] neg_hi:[1,0,0]
	v_pk_fma_f32 v[6:7], v[6:7], v[28:29], 0 op_sel_hi:[0,1,0] neg_lo:[1,0,0] neg_hi:[1,0,0]
	v_cvt_pk_bf16_f32 v8, v8, v9
	v_cvt_pk_bf16_f32 v9, v6, v7
	ds_write_b64 v186, v[8:9] offset:2720
	ds_read_b32 v6, v187 offset:176
	s_waitcnt lgkmcnt(0)
	v_pk_fma_f32 v[8:9], v[6:7], v[10:11], 0 op_sel_hi:[0,1,0] neg_lo:[1,0,0] neg_hi:[1,0,0]
	v_pk_fma_f32 v[6:7], v[6:7], v[12:13], 0 op_sel_hi:[0,1,0] neg_lo:[1,0,0] neg_hi:[1,0,0]
	v_cvt_pk_bf16_f32 v8, v8, v9
	v_cvt_pk_bf16_f32 v9, v6, v7
	ds_write_b64 v186, v[8:9] offset:3264
	ds_read_b32 v6, v187 offset:184
	s_waitcnt lgkmcnt(0)
	v_pk_fma_f32 v[2:3], v[6:7], v[2:3], 0 op_sel_hi:[0,1,0] neg_lo:[1,0,0] neg_hi:[1,0,0]
	v_pk_fma_f32 v[4:5], v[6:7], v[4:5], 0 op_sel_hi:[0,1,0] neg_lo:[1,0,0] neg_hi:[1,0,0]
	v_cvt_pk_bf16_f32 v2, v2, v3
	v_cvt_pk_bf16_f32 v3, v4, v5
	ds_write_b64 v186, v[2:3] offset:3808
	ds_read_b128 a[176:179], v1
	ds_read_b128 a[180:183], v1 offset:64
	ds_read_b128 a[184:187], v1 offset:128
	ds_read_b128 a[188:191], v1 offset:192
	v_lshl_add_u64 v[2:3], v[168:169], 0, s[22:23]
	v_lshl_add_u64 v[4:5], v[170:171], 0, s[22:23]
	v_lshl_add_u64 v[6:7], v[172:173], 0, s[22:23]
	v_lshl_add_u64 v[8:9], v[174:175], 0, s[22:23]
	v_lshl_add_u64 v[10:11], v[176:177], 0, s[22:23]
	v_lshl_add_u64 v[12:13], v[178:179], 0, s[22:23]
	v_lshl_add_u64 v[14:15], v[180:181], 0, s[22:23]
	v_lshl_add_u64 v[16:17], v[182:183], 0, s[22:23]
	global_load_dwordx4 v[114:117], v[2:3], off nt
	global_load_dwordx4 v[102:105], v[4:5], off nt
	global_load_dwordx4 v[94:97], v[6:7], off nt
	global_load_dwordx4 v[82:85], v[8:9], off nt
	global_load_dwordx4 v[62:65], v[10:11], off nt
	global_load_dwordx4 v[42:45], v[12:13], off nt
	global_load_dwordx4 v[38:41], v[14:15], off nt
	global_load_dwordx4 v[34:37], v[16:17], off nt
	v_mov_b32_e32 v2, v194
	s_waitcnt vmcnt(23)
	s_waitcnt vmcnt(22)
	s_waitcnt vmcnt(21)
	s_waitcnt vmcnt(20)
	s_waitcnt vmcnt(19)
	s_waitcnt vmcnt(18)
	s_waitcnt vmcnt(17)
	s_waitcnt vmcnt(16)
	ds_read_b32 v2, v187
	s_waitcnt lgkmcnt(0)
	v_pk_fma_f32 v[4:5], v[2:3], v[106:107], 0 op_sel_hi:[0,1,0] neg_lo:[1,0,0] neg_hi:[1,0,0]
	v_pk_fma_f32 v[2:3], v[2:3], v[108:109], 0 op_sel_hi:[0,1,0] neg_lo:[1,0,0] neg_hi:[1,0,0]
	v_cvt_pk_bf16_f32 v4, v4, v5
	v_cvt_pk_bf16_f32 v5, v2, v3
	ds_write_b64 v186, v[4:5]
	ds_read_b32 v2, v187 offset:8
	s_waitcnt lgkmcnt(0)
	v_pk_fma_f32 v[4:5], v[2:3], v[90:91], 0 op_sel_hi:[0,1,0] neg_lo:[1,0,0] neg_hi:[1,0,0]
	v_pk_fma_f32 v[2:3], v[2:3], v[92:93], 0 op_sel_hi:[0,1,0] neg_lo:[1,0,0] neg_hi:[1,0,0]
	v_cvt_pk_bf16_f32 v4, v4, v5
	v_cvt_pk_bf16_f32 v5, v2, v3
	ds_write_b64 v186, v[4:5] offset:544
	ds_read_b32 v2, v187 offset:16
	s_waitcnt lgkmcnt(0)
	v_pk_fma_f32 v[4:5], v[2:3], v[86:87], 0 op_sel_hi:[0,1,0] neg_lo:[1,0,0] neg_hi:[1,0,0]
	v_pk_fma_f32 v[2:3], v[2:3], v[88:89], 0 op_sel_hi:[0,1,0] neg_lo:[1,0,0] neg_hi:[1,0,0]
	v_cvt_pk_bf16_f32 v4, v4, v5
	v_cvt_pk_bf16_f32 v5, v2, v3
	ds_write_b64 v186, v[4:5] offset:1088
	ds_read_b32 v2, v187 offset:24
	s_waitcnt lgkmcnt(0)
	v_pk_fma_f32 v[4:5], v[2:3], v[74:75], 0 op_sel_hi:[0,1,0] neg_lo:[1,0,0] neg_hi:[1,0,0]
	v_pk_fma_f32 v[2:3], v[2:3], v[76:77], 0 op_sel_hi:[0,1,0] neg_lo:[1,0,0] neg_hi:[1,0,0]
	v_cvt_pk_bf16_f32 v4, v4, v5
	v_cvt_pk_bf16_f32 v5, v2, v3
	ds_write_b64 v186, v[4:5] offset:1632
	ds_read_b32 v2, v187 offset:32
	s_waitcnt lgkmcnt(0)
	v_pk_fma_f32 v[4:5], v[2:3], v[70:71], 0 op_sel_hi:[0,1,0] neg_lo:[1,0,0] neg_hi:[1,0,0]
	v_pk_fma_f32 v[2:3], v[2:3], v[72:73], 0 op_sel_hi:[0,1,0] neg_lo:[1,0,0] neg_hi:[1,0,0]
	v_cvt_pk_bf16_f32 v4, v4, v5
	v_cvt_pk_bf16_f32 v5, v2, v3
	ds_write_b64 v186, v[4:5] offset:2176
	ds_read_b32 v2, v187 offset:40
	s_waitcnt lgkmcnt(0)
	v_pk_fma_f32 v[4:5], v[2:3], v[54:55], 0 op_sel_hi:[0,1,0] neg_lo:[1,0,0] neg_hi:[1,0,0]
	v_pk_fma_f32 v[2:3], v[2:3], v[56:57], 0 op_sel_hi:[0,1,0] neg_lo:[1,0,0] neg_hi:[1,0,0]
	v_cvt_pk_bf16_f32 v4, v4, v5
	v_cvt_pk_bf16_f32 v5, v2, v3
	ds_write_b64 v186, v[4:5] offset:2720
	ds_read_b32 v2, v187 offset:48
	s_waitcnt lgkmcnt(0)
	v_pk_fma_f32 v[4:5], v[2:3], v[50:51], 0 op_sel_hi:[0,1,0] neg_lo:[1,0,0] neg_hi:[1,0,0]
	v_pk_fma_f32 v[2:3], v[2:3], v[52:53], 0 op_sel_hi:[0,1,0] neg_lo:[1,0,0] neg_hi:[1,0,0]
	v_cvt_pk_bf16_f32 v4, v4, v5
	v_cvt_pk_bf16_f32 v5, v2, v3
	ds_write_b64 v186, v[4:5] offset:3264
	ds_read_b32 v2, v187 offset:56
	s_waitcnt lgkmcnt(0)
	v_pk_fma_f32 v[4:5], v[2:3], v[46:47], 0 op_sel_hi:[0,1,0] neg_lo:[1,0,0] neg_hi:[1,0,0]
	v_pk_fma_f32 v[2:3], v[2:3], v[48:49], 0 op_sel_hi:[0,1,0] neg_lo:[1,0,0] neg_hi:[1,0,0]
	v_cvt_pk_bf16_f32 v4, v4, v5
	v_cvt_pk_bf16_f32 v5, v2, v3
	ds_write_b64 v186, v[4:5] offset:3808
	ds_read_b128 a[192:195], v1
	ds_read_b128 a[196:199], v1 offset:64
	ds_read_b128 a[200:203], v1 offset:128
	ds_read_b128 a[204:207], v1 offset:192
	v_lshl_add_u64 v[118:119], v[130:131], 0, s[20:21]
	v_add_co_u32_e32 v126, vcc, s7, v118
	s_nop 1
	v_addc_co_u32_e32 v127, vcc, 0, v119, vcc
	v_add_co_u32_e32 v128, vcc, s36, v118
	global_load_dwordx4 v[90:93], v[118:119], off nt
	global_load_dwordx4 v[86:89], v[126:127], off nt
	v_addc_co_u32_e32 v129, vcc, 0, v119, vcc
	v_add_co_u32_e32 v134, vcc, s37, v118
	s_nop 1
	v_addc_co_u32_e32 v135, vcc, 0, v119, vcc
	v_add_co_u32_e32 v136, vcc, s38, v118
	global_load_dwordx4 v[54:57], v[128:129], off nt
	global_load_dwordx4 v[50:53], v[134:135], off nt
	v_addc_co_u32_e32 v137, vcc, 0, v119, vcc
	v_add_co_u32_e32 v138, vcc, s39, v118
	s_nop 1
	v_addc_co_u32_e32 v139, vcc, 0, v119, vcc
	v_add_co_u32_e32 v140, vcc, s41, v118
	global_load_dwordx4 v[14:17], v[136:137], off nt
	global_load_dwordx4 v[10:13], v[138:139], off nt
	v_addc_co_u32_e32 v141, vcc, 0, v119, vcc
	v_add_co_u32_e32 v142, vcc, s42, v118
	s_nop 1
	v_addc_co_u32_e32 v143, vcc, 0, v119, vcc
	global_load_dwordx4 v[6:9], v[140:141], off nt
	global_load_dwordx4 v[2:5], v[142:143], off nt
	v_mov_b32_e32 v26, v194
	s_waitcnt vmcnt(23)
	s_waitcnt vmcnt(22)
	s_waitcnt vmcnt(21)
	s_waitcnt vmcnt(20)
	s_waitcnt vmcnt(19)
	s_waitcnt vmcnt(18)
	s_waitcnt vmcnt(17)
	s_waitcnt vmcnt(16)
	ds_read_b32 v26, v187 offset:64
	s_waitcnt lgkmcnt(0)
	v_pk_fma_f32 v[28:29], v[26:27], v[110:111], 0 op_sel_hi:[0,1,0] neg_lo:[1,0,0] neg_hi:[1,0,0]
	v_pk_fma_f32 v[26:27], v[26:27], v[112:113], 0 op_sel_hi:[0,1,0] neg_lo:[1,0,0] neg_hi:[1,0,0]
	v_cvt_pk_bf16_f32 v28, v28, v29
	v_cvt_pk_bf16_f32 v29, v26, v27
	ds_write_b64 v186, v[28:29]
	ds_read_b32 v26, v187 offset:72
	s_waitcnt lgkmcnt(0)
	v_pk_fma_f32 v[28:29], v[26:27], v[98:99], 0 op_sel_hi:[0,1,0] neg_lo:[1,0,0] neg_hi:[1,0,0]
	v_pk_fma_f32 v[26:27], v[26:27], v[100:101], 0 op_sel_hi:[0,1,0] neg_lo:[1,0,0] neg_hi:[1,0,0]
	v_cvt_pk_bf16_f32 v28, v28, v29
	v_cvt_pk_bf16_f32 v29, v26, v27
	ds_write_b64 v186, v[28:29] offset:544
	ds_read_b32 v26, v187 offset:80
	s_waitcnt lgkmcnt(0)
	v_pk_fma_f32 v[28:29], v[26:27], v[78:79], 0 op_sel_hi:[0,1,0] neg_lo:[1,0,0] neg_hi:[1,0,0]
	v_pk_fma_f32 v[26:27], v[26:27], v[80:81], 0 op_sel_hi:[0,1,0] neg_lo:[1,0,0] neg_hi:[1,0,0]
	v_cvt_pk_bf16_f32 v28, v28, v29
	v_cvt_pk_bf16_f32 v29, v26, v27
	ds_write_b64 v186, v[28:29] offset:1088
	ds_read_b32 v26, v187 offset:88
	s_waitcnt lgkmcnt(0)
	v_pk_fma_f32 v[28:29], v[26:27], v[66:67], 0 op_sel_hi:[0,1,0] neg_lo:[1,0,0] neg_hi:[1,0,0]
	v_pk_fma_f32 v[26:27], v[26:27], v[68:69], 0 op_sel_hi:[0,1,0] neg_lo:[1,0,0] neg_hi:[1,0,0]
	v_cvt_pk_bf16_f32 v28, v28, v29
	v_cvt_pk_bf16_f32 v29, v26, v27
	ds_write_b64 v186, v[28:29] offset:1632
	ds_read_b32 v26, v187 offset:96
	s_waitcnt lgkmcnt(0)
	v_pk_fma_f32 v[28:29], v[26:27], v[58:59], 0 op_sel_hi:[0,1,0] neg_lo:[1,0,0] neg_hi:[1,0,0]
	v_pk_fma_f32 v[26:27], v[26:27], v[60:61], 0 op_sel_hi:[0,1,0] neg_lo:[1,0,0] neg_hi:[1,0,0]
	v_cvt_pk_bf16_f32 v28, v28, v29
	v_cvt_pk_bf16_f32 v29, v26, v27
	ds_write_b64 v186, v[28:29] offset:2176
	ds_read_b32 v26, v187 offset:104
	s_waitcnt lgkmcnt(0)
	v_pk_fma_f32 v[28:29], v[26:27], v[30:31], 0 op_sel_hi:[0,1,0] neg_lo:[1,0,0] neg_hi:[1,0,0]
	v_pk_fma_f32 v[26:27], v[26:27], v[32:33], 0 op_sel_hi:[0,1,0] neg_lo:[1,0,0] neg_hi:[1,0,0]
	v_cvt_pk_bf16_f32 v28, v28, v29
	v_cvt_pk_bf16_f32 v29, v26, v27
	ds_write_b64 v186, v[28:29] offset:2720
	ds_read_b32 v26, v187 offset:112
	s_waitcnt lgkmcnt(0)
	v_pk_fma_f32 v[22:23], v[26:27], v[22:23], 0 op_sel_hi:[0,1,0] neg_lo:[1,0,0] neg_hi:[1,0,0]
	v_pk_fma_f32 v[24:25], v[26:27], v[24:25], 0 op_sel_hi:[0,1,0] neg_lo:[1,0,0] neg_hi:[1,0,0]
	v_cvt_pk_bf16_f32 v22, v22, v23
	v_cvt_pk_bf16_f32 v23, v24, v25
	ds_write_b64 v186, v[22:23] offset:3264
	ds_read_b32 v22, v187 offset:120
	s_waitcnt lgkmcnt(0)
	v_pk_fma_f32 v[18:19], v[22:23], v[18:19], 0 op_sel_hi:[0,1,0] neg_lo:[1,0,0] neg_hi:[1,0,0]
	v_pk_fma_f32 v[20:21], v[22:23], v[20:21], 0 op_sel_hi:[0,1,0] neg_lo:[1,0,0] neg_hi:[1,0,0]
	v_cvt_pk_bf16_f32 v18, v18, v19
	v_cvt_pk_bf16_f32 v19, v20, v21
	ds_write_b64 v186, v[18:19] offset:3808
	ds_read_b128 a[208:211], v1
	ds_read_b128 a[212:215], v1 offset:64
	ds_read_b128 a[216:219], v1 offset:128
	ds_read_b128 a[220:223], v1 offset:192
	v_lshl_add_u64 v[18:19], v[150:151], 0, s[20:21]
	v_lshl_add_u64 v[20:21], v[152:153], 0, s[20:21]
	v_lshl_add_u64 v[22:23], v[156:157], 0, s[20:21]
	v_lshl_add_u64 v[24:25], v[158:159], 0, s[20:21]
	v_lshl_add_u64 v[26:27], v[160:161], 0, s[20:21]
	v_lshl_add_u64 v[28:29], v[162:163], 0, s[20:21]
	v_lshl_add_u64 v[46:47], v[164:165], 0, s[20:21]
	v_lshl_add_u64 v[48:49], v[166:167], 0, s[20:21]
	global_load_dwordx4 v[78:81], v[18:19], off nt
	global_load_dwordx4 v[74:77], v[20:21], off nt
	global_load_dwordx4 v[70:73], v[22:23], off nt
	global_load_dwordx4 v[66:69], v[24:25], off nt
	global_load_dwordx4 v[30:33], v[26:27], off nt
	s_nop 0
	global_load_dwordx4 v[26:29], v[28:29], off nt
	s_nop 0
	global_load_dwordx4 v[22:25], v[46:47], off nt
	global_load_dwordx4 v[18:21], v[48:49], off nt
	s_waitcnt vmcnt(23)
	s_waitcnt vmcnt(22)
	s_waitcnt vmcnt(21)
	s_waitcnt vmcnt(20)
	s_waitcnt vmcnt(19)
	s_waitcnt vmcnt(18)
	s_waitcnt vmcnt(17)
	s_waitcnt vmcnt(16)
	ds_read_b32 v46, v187 offset:128
	s_waitcnt lgkmcnt(0)
	v_pk_fma_f32 v[48:49], v[46:47], v[114:115], 0 op_sel_hi:[0,1,0] neg_lo:[1,0,0] neg_hi:[1,0,0]
	v_pk_fma_f32 v[46:47], v[46:47], v[116:117], 0 op_sel_hi:[0,1,0] neg_lo:[1,0,0] neg_hi:[1,0,0]
	v_cvt_pk_bf16_f32 v48, v48, v49
	v_cvt_pk_bf16_f32 v49, v46, v47
	ds_write_b64 v186, v[48:49]
	ds_read_b32 v46, v187 offset:136
	s_waitcnt lgkmcnt(0)
	v_pk_fma_f32 v[48:49], v[46:47], v[102:103], 0 op_sel_hi:[0,1,0] neg_lo:[1,0,0] neg_hi:[1,0,0]
	v_pk_fma_f32 v[46:47], v[46:47], v[104:105], 0 op_sel_hi:[0,1,0] neg_lo:[1,0,0] neg_hi:[1,0,0]
	v_cvt_pk_bf16_f32 v48, v48, v49
	v_cvt_pk_bf16_f32 v49, v46, v47
	ds_write_b64 v186, v[48:49] offset:544
	ds_read_b32 v46, v187 offset:144
	s_waitcnt lgkmcnt(0)
	v_pk_fma_f32 v[48:49], v[46:47], v[94:95], 0 op_sel_hi:[0,1,0] neg_lo:[1,0,0] neg_hi:[1,0,0]
	v_pk_fma_f32 v[46:47], v[46:47], v[96:97], 0 op_sel_hi:[0,1,0] neg_lo:[1,0,0] neg_hi:[1,0,0]
	v_cvt_pk_bf16_f32 v48, v48, v49
	v_cvt_pk_bf16_f32 v49, v46, v47
	ds_write_b64 v186, v[48:49] offset:1088
	ds_read_b32 v46, v187 offset:152
	s_waitcnt lgkmcnt(0)
	v_pk_fma_f32 v[48:49], v[46:47], v[82:83], 0 op_sel_hi:[0,1,0] neg_lo:[1,0,0] neg_hi:[1,0,0]
	v_pk_fma_f32 v[46:47], v[46:47], v[84:85], 0 op_sel_hi:[0,1,0] neg_lo:[1,0,0] neg_hi:[1,0,0]
	v_cvt_pk_bf16_f32 v48, v48, v49
	v_cvt_pk_bf16_f32 v49, v46, v47
	ds_write_b64 v186, v[48:49] offset:1632
	ds_read_b32 v46, v187 offset:160
	s_waitcnt lgkmcnt(0)
	v_pk_fma_f32 v[48:49], v[46:47], v[62:63], 0 op_sel_hi:[0,1,0] neg_lo:[1,0,0] neg_hi:[1,0,0]
	v_pk_fma_f32 v[46:47], v[46:47], v[64:65], 0 op_sel_hi:[0,1,0] neg_lo:[1,0,0] neg_hi:[1,0,0]
	v_cvt_pk_bf16_f32 v48, v48, v49
	v_cvt_pk_bf16_f32 v49, v46, v47
	ds_write_b64 v186, v[48:49] offset:2176
	ds_read_b32 v46, v187 offset:168
	s_waitcnt lgkmcnt(0)
	v_pk_fma_f32 v[42:43], v[46:47], v[42:43], 0 op_sel_hi:[0,1,0] neg_lo:[1,0,0] neg_hi:[1,0,0]
	v_pk_fma_f32 v[44:45], v[46:47], v[44:45], 0 op_sel_hi:[0,1,0] neg_lo:[1,0,0] neg_hi:[1,0,0]
	v_cvt_pk_bf16_f32 v42, v42, v43
	v_cvt_pk_bf16_f32 v43, v44, v45
	ds_write_b64 v186, v[42:43] offset:2720
	ds_read_b32 v42, v187 offset:176
	s_waitcnt lgkmcnt(0)
	v_pk_fma_f32 v[38:39], v[42:43], v[38:39], 0 op_sel_hi:[0,1,0] neg_lo:[1,0,0] neg_hi:[1,0,0]
	v_pk_fma_f32 v[40:41], v[42:43], v[40:41], 0 op_sel_hi:[0,1,0] neg_lo:[1,0,0] neg_hi:[1,0,0]
	v_cvt_pk_bf16_f32 v38, v38, v39
	v_cvt_pk_bf16_f32 v39, v40, v41
	ds_write_b64 v186, v[38:39] offset:3264
	ds_read_b32 v38, v187 offset:184
	s_waitcnt lgkmcnt(0)
	v_pk_fma_f32 v[34:35], v[38:39], v[34:35], 0 op_sel_hi:[0,1,0] neg_lo:[1,0,0] neg_hi:[1,0,0]
	v_pk_fma_f32 v[36:37], v[38:39], v[36:37], 0 op_sel_hi:[0,1,0] neg_lo:[1,0,0] neg_hi:[1,0,0]
	v_cvt_pk_bf16_f32 v34, v34, v35
	v_cvt_pk_bf16_f32 v35, v36, v37
	ds_write_b64 v186, v[34:35] offset:3808
	ds_read_b128 a[224:227], v1
	ds_read_b128 a[228:231], v1 offset:64
	ds_read_b128 a[232:235], v1 offset:128
	ds_read_b128 a[236:239], v1 offset:192
	v_lshl_add_u64 v[34:35], v[168:169], 0, s[20:21]
	v_lshl_add_u64 v[36:37], v[170:171], 0, s[20:21]
	v_lshl_add_u64 v[38:39], v[172:173], 0, s[20:21]
	v_lshl_add_u64 v[40:41], v[174:175], 0, s[20:21]
	v_lshl_add_u64 v[42:43], v[176:177], 0, s[20:21]
	v_lshl_add_u64 v[44:45], v[178:179], 0, s[20:21]
	v_lshl_add_u64 v[58:59], v[180:181], 0, s[20:21]
	v_lshl_add_u64 v[60:61], v[182:183], 0, s[20:21]
	global_load_dwordx4 v[122:125], v[34:35], off nt
	global_load_dwordx4 v[106:109], v[36:37], off nt
	global_load_dwordx4 v[94:97], v[38:39], off nt
	global_load_dwordx4 v[82:85], v[40:41], off nt
	global_load_dwordx4 v[46:49], v[42:43], off nt
	s_nop 0
	global_load_dwordx4 v[42:45], v[44:45], off nt
	s_nop 0
	global_load_dwordx4 v[38:41], v[58:59], off nt
	global_load_dwordx4 v[34:37], v[60:61], off nt
	v_mov_b32_e32 v98, v133
	s_waitcnt vmcnt(23)
	s_waitcnt vmcnt(22)
	s_waitcnt vmcnt(21)
	s_waitcnt vmcnt(20)
	s_waitcnt vmcnt(19)
	s_waitcnt vmcnt(18)
	s_waitcnt vmcnt(17)
	s_waitcnt vmcnt(16)
	ds_read_b32 v58, v187
	v_add_u32_e32 v99, 1, v98
	v_cmp_eq_u32_e32 vcc, v98, v132
	s_nop 1
	v_cndmask_b32_e64 v60, 0, 1.0, vcc
	v_cmp_eq_u32_e32 vcc, v99, v132
	s_nop 1
	v_cndmask_b32_e64 v61, 0, 1.0, vcc
	s_waitcnt lgkmcnt(0)
	v_pk_fma_f32 v[62:63], v[58:59], v[90:91], v[60:61] op_sel_hi:[0,1,1] neg_lo:[1,0,0] neg_hi:[1,0,0]
	v_add_u32_e32 v90, 3, v98
	v_add_u32_e32 v91, 2, v98
	v_cmp_eq_u32_e32 vcc, v90, v132
	v_cvt_pk_bf16_f32 v62, v62, v63
	s_nop 0
	v_cndmask_b32_e64 v65, 0, 1.0, vcc
	v_cmp_eq_u32_e32 vcc, v91, v132
	s_nop 1
	v_cndmask_b32_e64 v64, 0, 1.0, vcc
	v_pk_fma_f32 v[58:59], v[58:59], v[92:93], v[64:65] op_sel_hi:[0,1,1] neg_lo:[1,0,0] neg_hi:[1,0,0]
	v_cvt_pk_bf16_f32 v63, v58, v59
	ds_write_b64 v186, v[62:63]
	ds_read_b32 v58, v187 offset:8
	v_cmp_eq_u32_e32 vcc, v98, v193
	s_nop 1
	v_cndmask_b32_e64 v62, 0, 1.0, vcc
	v_cmp_eq_u32_e32 vcc, v99, v193
	s_nop 1
	v_cndmask_b32_e64 v63, 0, 1.0, vcc
	v_cmp_eq_u32_e32 vcc, v90, v193
	s_waitcnt lgkmcnt(0)
	v_pk_fma_f32 v[62:63], v[58:59], v[86:87], v[62:63] op_sel_hi:[0,1,1] neg_lo:[1,0,0] neg_hi:[1,0,0]
	v_cvt_pk_bf16_f32 v62, v62, v63
	v_cndmask_b32_e64 v61, 0, 1.0, vcc
	v_pk_fma_f32 v[58:59], v[58:59], v[88:89], v[60:61] op_sel_hi:[0,1,1] neg_lo:[1,0,0] neg_hi:[1,0,0]
	v_cvt_pk_bf16_f32 v63, v58, v59
	ds_write_b64 v186, v[62:63] offset:544
	ds_read_b32 v58, v187 offset:16
	v_cmp_eq_u32_e32 vcc, v98, v192
	s_nop 1
	v_cndmask_b32_e64 v60, 0, 1.0, vcc
	v_cmp_eq_u32_e32 vcc, v99, v192
	s_nop 1
	v_cndmask_b32_e64 v61, 0, 1.0, vcc
	v_cmp_eq_u32_e32 vcc, v90, v192
	s_waitcnt lgkmcnt(0)
	v_pk_fma_f32 v[54:55], v[58:59], v[54:55], v[60:61] op_sel_hi:[0,1,1] neg_lo:[1,0,0] neg_hi:[1,0,0]
	v_cvt_pk_bf16_f32 v54, v54, v55
	v_cndmask_b32_e64 v61, 0, 1.0, vcc
	v_cmp_eq_u32_e32 vcc, v91, v192
	s_nop 1
	v_cndmask_b32_e64 v60, 0, 1.0, vcc
	v_pk_fma_f32 v[56:57], v[58:59], v[56:57], v[60:61] op_sel_hi:[0,1,1] neg_lo:[1,0,0] neg_hi:[1,0,0]
	v_cvt_pk_bf16_f32 v55, v56, v57
	ds_write_b64 v186, v[54:55] offset:1088
	ds_read_b32 v54, v187 offset:24
	v_cmp_eq_u32_e32 vcc, v98, v190
	s_nop 1
	v_cndmask_b32_e64 v56, 0, 1.0, vcc
	v_cmp_eq_u32_e32 vcc, v99, v190
	s_nop 1
	v_cndmask_b32_e64 v57, 0, 1.0, vcc
	v_cmp_eq_u32_e32 vcc, v90, v190
	s_waitcnt lgkmcnt(0)
	v_pk_fma_f32 v[50:51], v[54:55], v[50:51], v[56:57] op_sel_hi:[0,1,1] neg_lo:[1,0,0] neg_hi:[1,0,0]
	v_cvt_pk_bf16_f32 v50, v50, v51
	v_cndmask_b32_e64 v57, 0, 1.0, vcc
	v_cmp_eq_u32_e32 vcc, v91, v190
	s_nop 1
	v_cndmask_b32_e64 v56, 0, 1.0, vcc
	v_pk_fma_f32 v[52:53], v[54:55], v[52:53], v[56:57] op_sel_hi:[0,1,1] neg_lo:[1,0,0] neg_hi:[1,0,0]
	v_cvt_pk_bf16_f32 v51, v52, v53
	ds_write_b64 v186, v[50:51] offset:1632
	ds_read_b32 v50, v187 offset:32
	v_cmp_eq_u32_e32 vcc, v98, v149
	s_nop 1
	v_cndmask_b32_e64 v52, 0, 1.0, vcc
	v_cmp_eq_u32_e32 vcc, v99, v149
	s_nop 1
	v_cndmask_b32_e64 v53, 0, 1.0, vcc
	v_cmp_eq_u32_e32 vcc, v90, v149
	s_waitcnt lgkmcnt(0)
	v_pk_fma_f32 v[14:15], v[50:51], v[14:15], v[52:53] op_sel_hi:[0,1,1] neg_lo:[1,0,0] neg_hi:[1,0,0]
	v_cvt_pk_bf16_f32 v14, v14, v15
	v_cndmask_b32_e64 v53, 0, 1.0, vcc
	v_cmp_eq_u32_e32 vcc, v91, v149
	s_nop 1
	v_cndmask_b32_e64 v52, 0, 1.0, vcc
	v_pk_fma_f32 v[16:17], v[50:51], v[16:17], v[52:53] op_sel_hi:[0,1,1] neg_lo:[1,0,0] neg_hi:[1,0,0]
	v_cvt_pk_bf16_f32 v15, v16, v17
	ds_write_b64 v186, v[14:15] offset:2176
	ds_read_b32 v14, v187 offset:40
	v_cmp_eq_u32_e32 vcc, v98, v148
	s_nop 1
	v_cndmask_b32_e64 v16, 0, 1.0, vcc
	v_cmp_eq_u32_e32 vcc, v99, v148
	s_nop 1
	v_cndmask_b32_e64 v17, 0, 1.0, vcc
	v_cmp_eq_u32_e32 vcc, v90, v148
	s_waitcnt lgkmcnt(0)
	v_pk_fma_f32 v[10:11], v[14:15], v[10:11], v[16:17] op_sel_hi:[0,1,1] neg_lo:[1,0,0] neg_hi:[1,0,0]
	v_cvt_pk_bf16_f32 v10, v10, v11
	v_cndmask_b32_e64 v17, 0, 1.0, vcc
	v_cmp_eq_u32_e32 vcc, v91, v148
	s_nop 1
	v_cndmask_b32_e64 v16, 0, 1.0, vcc
	v_pk_fma_f32 v[12:13], v[14:15], v[12:13], v[16:17] op_sel_hi:[0,1,1] neg_lo:[1,0,0] neg_hi:[1,0,0]
	v_cvt_pk_bf16_f32 v11, v12, v13
	ds_write_b64 v186, v[10:11] offset:2720
	ds_read_b32 v10, v187 offset:48
	v_cmp_eq_u32_e32 vcc, v98, v147
	s_nop 1
	v_cndmask_b32_e64 v12, 0, 1.0, vcc
	v_cmp_eq_u32_e32 vcc, v99, v147
	s_nop 1
	v_cndmask_b32_e64 v13, 0, 1.0, vcc
	v_cmp_eq_u32_e32 vcc, v90, v147
	s_waitcnt lgkmcnt(0)
	v_pk_fma_f32 v[6:7], v[10:11], v[6:7], v[12:13] op_sel_hi:[0,1,1] neg_lo:[1,0,0] neg_hi:[1,0,0]
	v_cvt_pk_bf16_f32 v6, v6, v7
	v_cndmask_b32_e64 v13, 0, 1.0, vcc
	v_cmp_eq_u32_e32 vcc, v91, v147
	s_nop 1
	v_cndmask_b32_e64 v12, 0, 1.0, vcc
	v_pk_fma_f32 v[8:9], v[10:11], v[8:9], v[12:13] op_sel_hi:[0,1,1] neg_lo:[1,0,0] neg_hi:[1,0,0]
	v_cvt_pk_bf16_f32 v7, v8, v9
	ds_write_b64 v186, v[6:7] offset:3264
	ds_read_b32 v6, v187 offset:56
	v_cmp_eq_u32_e32 vcc, v98, v146
	s_nop 1
	v_cndmask_b32_e64 v8, 0, 1.0, vcc
	v_cmp_eq_u32_e32 vcc, v99, v146
	s_nop 1
	v_cndmask_b32_e64 v9, 0, 1.0, vcc
	v_cmp_eq_u32_e32 vcc, v90, v146
	s_waitcnt lgkmcnt(0)
	v_pk_fma_f32 v[2:3], v[6:7], v[2:3], v[8:9] op_sel_hi:[0,1,1] neg_lo:[1,0,0] neg_hi:[1,0,0]
	v_cvt_pk_bf16_f32 v2, v2, v3
	v_cndmask_b32_e64 v9, 0, 1.0, vcc
	v_cmp_eq_u32_e32 vcc, v91, v146
	s_nop 1
	v_cndmask_b32_e64 v8, 0, 1.0, vcc
	v_pk_fma_f32 v[4:5], v[6:7], v[4:5], v[8:9] op_sel_hi:[0,1,1] neg_lo:[1,0,0] neg_hi:[1,0,0]
	v_cvt_pk_bf16_f32 v3, v4, v5
	ds_write_b64 v186, v[2:3] offset:3808
	ds_read_b128 v[2:5], v1
	ds_read_b128 v[6:9], v1 offset:64
	ds_read_b128 v[10:13], v1 offset:128
	ds_read_b128 v[14:17], v1 offset:192
	global_load_dwordx4 v[118:121], v[118:119], off offset:512 nt
	s_nop 0
	global_load_dwordx4 v[110:113], v[126:127], off offset:512 nt
	global_load_dwordx4 v[98:101], v[128:129], off offset:512 nt
	global_load_dwordx4 v[86:89], v[134:135], off offset:512 nt
	global_load_dwordx4 v[62:65], v[136:137], off offset:512 nt
	global_load_dwordx4 v[58:61], v[138:139], off offset:512 nt
	global_load_dwordx4 v[54:57], v[140:141], off offset:512 nt
	global_load_dwordx4 v[50:53], v[142:143], off offset:512 nt
	v_mov_b32_e32 v91, v133
	s_waitcnt vmcnt(23)
	s_waitcnt vmcnt(22)
	s_waitcnt vmcnt(21)
	s_waitcnt vmcnt(20)
	s_waitcnt vmcnt(19)
	s_waitcnt vmcnt(18)
	s_waitcnt vmcnt(17)
	s_waitcnt vmcnt(16)
	ds_read_b32 v90, v187 offset:64
	v_or_b32_e32 v138, 16, v132
	v_add_u32_e32 v102, 1, v91
	v_cmp_eq_u32_e32 vcc, v91, v138
	v_add_u32_e32 v103, 3, v91
	v_add_u32_e32 v104, 2, v91
	v_cndmask_b32_e64 v92, 0, 1.0, vcc
	v_cmp_eq_u32_e32 vcc, v102, v138
	v_or_b32_e32 v139, 18, v132
	v_or_b32_e32 v140, 20, v132
	v_cndmask_b32_e64 v93, 0, 1.0, vcc
	v_cmp_eq_u32_e32 vcc, v103, v138
	s_waitcnt lgkmcnt(0)
	v_pk_fma_f32 v[78:79], v[90:91], v[78:79], v[92:93] op_sel_hi:[0,1,1] neg_lo:[1,0,0] neg_hi:[1,0,0]
	v_cvt_pk_bf16_f32 v78, v78, v79
	v_cndmask_b32_e64 v93, 0, 1.0, vcc
	v_cmp_eq_u32_e32 vcc, v104, v138
	v_or_b32_e32 v141, 22, v132
	v_or_b32_e32 v142, 24, v132
	v_cndmask_b32_e64 v92, 0, 1.0, vcc
	v_pk_fma_f32 v[80:81], v[90:91], v[80:81], v[92:93] op_sel_hi:[0,1,1] neg_lo:[1,0,0] neg_hi:[1,0,0]
	v_cvt_pk_bf16_f32 v79, v80, v81
	ds_write_b64 v186, v[78:79]
	ds_read_b32 v78, v187 offset:72
	v_cmp_eq_u32_e32 vcc, v91, v139
	v_or_b32_e32 v143, 26, v132
	v_or_b32_e32 v144, 28, v132
	v_cndmask_b32_e64 v80, 0, 1.0, vcc
	v_cmp_eq_u32_e32 vcc, v102, v139
	v_or_b32_e32 v145, 30, v132
	s_nop 0
	v_cndmask_b32_e64 v81, 0, 1.0, vcc
	v_cmp_eq_u32_e32 vcc, v103, v139
	s_waitcnt lgkmcnt(0)
	v_pk_fma_f32 v[74:75], v[78:79], v[74:75], v[80:81] op_sel_hi:[0,1,1] neg_lo:[1,0,0] neg_hi:[1,0,0]
	v_cvt_pk_bf16_f32 v74, v74, v75
	v_cndmask_b32_e64 v81, 0, 1.0, vcc
	v_cmp_eq_u32_e32 vcc, v104, v139
	s_nop 1
	v_cndmask_b32_e64 v80, 0, 1.0, vcc
	v_pk_fma_f32 v[76:77], v[78:79], v[76:77], v[80:81] op_sel_hi:[0,1,1] neg_lo:[1,0,0] neg_hi:[1,0,0]
	v_cvt_pk_bf16_f32 v75, v76, v77
	ds_write_b64 v186, v[74:75] offset:544
	ds_read_b32 v74, v187 offset:80
	v_cmp_eq_u32_e32 vcc, v91, v140
	s_nop 1
	v_cndmask_b32_e64 v76, 0, 1.0, vcc
	v_cmp_eq_u32_e32 vcc, v102, v140
	s_nop 1
	v_cndmask_b32_e64 v77, 0, 1.0, vcc
	v_cmp_eq_u32_e32 vcc, v103, v140
	s_waitcnt lgkmcnt(0)
	v_pk_fma_f32 v[70:71], v[74:75], v[70:71], v[76:77] op_sel_hi:[0,1,1] neg_lo:[1,0,0] neg_hi:[1,0,0]
	v_cvt_pk_bf16_f32 v70, v70, v71
	v_cndmask_b32_e64 v77, 0, 1.0, vcc
	v_cmp_eq_u32_e32 vcc, v104, v140
	s_nop 1
	v_cndmask_b32_e64 v76, 0, 1.0, vcc
	v_pk_fma_f32 v[72:73], v[74:75], v[72:73], v[76:77] op_sel_hi:[0,1,1] neg_lo:[1,0,0] neg_hi:[1,0,0]
	v_cvt_pk_bf16_f32 v71, v72, v73
	ds_write_b64 v186, v[70:71] offset:1088
	ds_read_b32 v70, v187 offset:88
	v_cmp_eq_u32_e32 vcc, v91, v141
	s_nop 1
	v_cndmask_b32_e64 v72, 0, 1.0, vcc
	v_cmp_eq_u32_e32 vcc, v102, v141
	s_nop 1
	v_cndmask_b32_e64 v73, 0, 1.0, vcc
	v_cmp_eq_u32_e32 vcc, v103, v141
	s_waitcnt lgkmcnt(0)
	v_pk_fma_f32 v[66:67], v[70:71], v[66:67], v[72:73] op_sel_hi:[0,1,1] neg_lo:[1,0,0] neg_hi:[1,0,0]
	v_cvt_pk_bf16_f32 v66, v66, v67
	v_cndmask_b32_e64 v73, 0, 1.0, vcc
	v_cmp_eq_u32_e32 vcc, v104, v141
	s_nop 1
	v_cndmask_b32_e64 v72, 0, 1.0, vcc
	v_pk_fma_f32 v[68:69], v[70:71], v[68:69], v[72:73] op_sel_hi:[0,1,1] neg_lo:[1,0,0] neg_hi:[1,0,0]
	v_cvt_pk_bf16_f32 v67, v68, v69
	ds_write_b64 v186, v[66:67] offset:1632
	ds_read_b32 v66, v187 offset:96
	v_cmp_eq_u32_e32 vcc, v91, v142
	s_nop 1
	v_cndmask_b32_e64 v68, 0, 1.0, vcc
	v_cmp_eq_u32_e32 vcc, v102, v142
	s_nop 1
	v_cndmask_b32_e64 v69, 0, 1.0, vcc
	v_cmp_eq_u32_e32 vcc, v103, v142
	s_waitcnt lgkmcnt(0)
	v_pk_fma_f32 v[30:31], v[66:67], v[30:31], v[68:69] op_sel_hi:[0,1,1] neg_lo:[1,0,0] neg_hi:[1,0,0]
	v_cvt_pk_bf16_f32 v30, v30, v31
	v_cndmask_b32_e64 v69, 0, 1.0, vcc
	v_cmp_eq_u32_e32 vcc, v104, v142
	s_nop 1
	v_cndmask_b32_e64 v68, 0, 1.0, vcc
	v_pk_fma_f32 v[32:33], v[66:67], v[32:33], v[68:69] op_sel_hi:[0,1,1] neg_lo:[1,0,0] neg_hi:[1,0,0]
	v_cvt_pk_bf16_f32 v31, v32, v33
	ds_write_b64 v186, v[30:31] offset:2176
	ds_read_b32 v30, v187 offset:104
	v_cmp_eq_u32_e32 vcc, v91, v143
	s_nop 1
	v_cndmask_b32_e64 v32, 0, 1.0, vcc
	v_cmp_eq_u32_e32 vcc, v102, v143
	s_nop 1
	v_cndmask_b32_e64 v33, 0, 1.0, vcc
	v_cmp_eq_u32_e32 vcc, v103, v143
	s_waitcnt lgkmcnt(0)
	v_pk_fma_f32 v[26:27], v[30:31], v[26:27], v[32:33] op_sel_hi:[0,1,1] neg_lo:[1,0,0] neg_hi:[1,0,0]
	v_cvt_pk_bf16_f32 v26, v26, v27
	v_cndmask_b32_e64 v33, 0, 1.0, vcc
	v_cmp_eq_u32_e32 vcc, v104, v143
	s_nop 1
	v_cndmask_b32_e64 v32, 0, 1.0, vcc
	v_pk_fma_f32 v[28:29], v[30:31], v[28:29], v[32:33] op_sel_hi:[0,1,1] neg_lo:[1,0,0] neg_hi:[1,0,0]
	v_cvt_pk_bf16_f32 v27, v28, v29
	ds_write_b64 v186, v[26:27] offset:2720
	ds_read_b32 v26, v187 offset:112
	v_cmp_eq_u32_e32 vcc, v91, v144
	s_nop 1
	v_cndmask_b32_e64 v28, 0, 1.0, vcc
	v_cmp_eq_u32_e32 vcc, v102, v144
	s_nop 1
	v_cndmask_b32_e64 v29, 0, 1.0, vcc
	v_cmp_eq_u32_e32 vcc, v103, v144
	s_waitcnt lgkmcnt(0)
	v_pk_fma_f32 v[22:23], v[26:27], v[22:23], v[28:29] op_sel_hi:[0,1,1] neg_lo:[1,0,0] neg_hi:[1,0,0]
	v_cvt_pk_bf16_f32 v22, v22, v23
	v_cndmask_b32_e64 v29, 0, 1.0, vcc
	v_cmp_eq_u32_e32 vcc, v104, v144
	s_nop 1
	v_cndmask_b32_e64 v28, 0, 1.0, vcc
	v_pk_fma_f32 v[24:25], v[26:27], v[24:25], v[28:29] op_sel_hi:[0,1,1] neg_lo:[1,0,0] neg_hi:[1,0,0]
	v_cvt_pk_bf16_f32 v23, v24, v25
	ds_write_b64 v186, v[22:23] offset:3264
	ds_read_b32 v22, v187 offset:120
	v_cmp_eq_u32_e32 vcc, v91, v145
	s_nop 1
	v_cndmask_b32_e64 v24, 0, 1.0, vcc
	v_cmp_eq_u32_e32 vcc, v102, v145
	s_nop 1
	v_cndmask_b32_e64 v25, 0, 1.0, vcc
	v_cmp_eq_u32_e32 vcc, v103, v145
	s_waitcnt lgkmcnt(0)
	v_pk_fma_f32 v[18:19], v[22:23], v[18:19], v[24:25] op_sel_hi:[0,1,1] neg_lo:[1,0,0] neg_hi:[1,0,0]
	v_cvt_pk_bf16_f32 v18, v18, v19
	v_cndmask_b32_e64 v25, 0, 1.0, vcc
	v_cmp_eq_u32_e32 vcc, v104, v145
	s_nop 1
	v_cndmask_b32_e64 v24, 0, 1.0, vcc
	v_pk_fma_f32 v[20:21], v[22:23], v[20:21], v[24:25] op_sel_hi:[0,1,1] neg_lo:[1,0,0] neg_hi:[1,0,0]
	v_cvt_pk_bf16_f32 v19, v20, v21
	ds_write_b64 v186, v[18:19] offset:3808
	ds_read_b128 v[18:21], v1
	ds_read_b128 v[22:25], v1 offset:64
	ds_read_b128 v[26:29], v1 offset:128
	ds_read_b128 v[30:33], v1 offset:192
	v_lshl_add_u64 v[66:67], v[150:151], 0, s[8:9]
	v_lshl_add_u64 v[68:69], v[152:153], 0, s[8:9]
	v_lshl_add_u64 v[70:71], v[156:157], 0, s[8:9]
	v_lshl_add_u64 v[72:73], v[158:159], 0, s[8:9]
	v_lshl_add_u64 v[74:75], v[160:161], 0, s[8:9]
	v_lshl_add_u64 v[76:77], v[162:163], 0, s[8:9]
	v_lshl_add_u64 v[134:135], v[164:165], 0, s[8:9]
	v_lshl_add_u64 v[136:137], v[166:167], 0, s[8:9]
	global_load_dwordx4 v[126:129], v[66:67], off nt
	global_load_dwordx4 v[114:117], v[68:69], off nt
	global_load_dwordx4 v[102:105], v[70:71], off nt
	global_load_dwordx4 v[90:93], v[72:73], off nt
	global_load_dwordx4 v[78:81], v[74:75], off nt
	s_nop 0
	global_load_dwordx4 v[74:77], v[76:77], off nt
	s_nop 0
	global_load_dwordx4 v[70:73], v[134:135], off nt
	global_load_dwordx4 v[66:69], v[136:137], off nt
	s_waitcnt vmcnt(23)
	s_waitcnt vmcnt(22)
	s_waitcnt vmcnt(21)
	s_waitcnt vmcnt(20)
	s_waitcnt vmcnt(19)
	s_waitcnt vmcnt(18)
	s_waitcnt vmcnt(17)
	s_waitcnt vmcnt(16)
	ds_read_b32 v134, v187 offset:128
	v_or_b32_e32 v194, 32, v132
	v_add_u32_e32 v135, 1, v133
	v_cmp_eq_u32_e32 vcc, v133, v194
	v_add_u32_e32 v202, 3, v133
	v_add_u32_e32 v203, 2, v133
	v_cndmask_b32_e64 v136, 0, 1.0, vcc
	v_cmp_eq_u32_e32 vcc, v135, v194
	v_or_b32_e32 v195, 34, v132
	v_or_b32_e32 v196, 36, v132
	v_cndmask_b32_e64 v137, 0, 1.0, vcc
	v_cmp_eq_u32_e32 vcc, v202, v194
	s_waitcnt lgkmcnt(0)
	v_pk_fma_f32 v[122:123], v[134:135], v[122:123], v[136:137] op_sel_hi:[0,1,1] neg_lo:[1,0,0] neg_hi:[1,0,0]
	v_cvt_pk_bf16_f32 v122, v122, v123
	v_cndmask_b32_e64 v137, 0, 1.0, vcc
	v_cmp_eq_u32_e32 vcc, v203, v194
	v_or_b32_e32 v197, 38, v132
	v_or_b32_e32 v198, 40, v132
	v_cndmask_b32_e64 v136, 0, 1.0, vcc
	v_pk_fma_f32 v[124:125], v[134:135], v[124:125], v[136:137] op_sel_hi:[0,1,1] neg_lo:[1,0,0] neg_hi:[1,0,0]
	v_cvt_pk_bf16_f32 v123, v124, v125
	ds_write_b64 v186, v[122:123]
	ds_read_b32 v122, v187 offset:136
	v_cmp_eq_u32_e32 vcc, v133, v195
	v_or_b32_e32 v199, 42, v132
	v_or_b32_e32 v200, 44, v132
	v_cndmask_b32_e64 v124, 0, 1.0, vcc
	v_cmp_eq_u32_e32 vcc, v135, v195
	v_or_b32_e32 v201, 46, v132
	s_nop 0
	v_cndmask_b32_e64 v125, 0, 1.0, vcc
	v_cmp_eq_u32_e32 vcc, v202, v195
	s_waitcnt lgkmcnt(0)
	v_pk_fma_f32 v[106:107], v[122:123], v[106:107], v[124:125] op_sel_hi:[0,1,1] neg_lo:[1,0,0] neg_hi:[1,0,0]
	v_cvt_pk_bf16_f32 v106, v106, v107
	v_cndmask_b32_e64 v125, 0, 1.0, vcc
	v_cmp_eq_u32_e32 vcc, v203, v195
	s_nop 1
	v_cndmask_b32_e64 v124, 0, 1.0, vcc
	v_pk_fma_f32 v[108:109], v[122:123], v[108:109], v[124:125] op_sel_hi:[0,1,1] neg_lo:[1,0,0] neg_hi:[1,0,0]
	v_cvt_pk_bf16_f32 v107, v108, v109
	ds_write_b64 v186, v[106:107] offset:544
	ds_read_b32 v106, v187 offset:144
	v_cmp_eq_u32_e32 vcc, v133, v196
	s_nop 1
	v_cndmask_b32_e64 v108, 0, 1.0, vcc
	v_cmp_eq_u32_e32 vcc, v135, v196
	s_nop 1
	v_cndmask_b32_e64 v109, 0, 1.0, vcc
	v_cmp_eq_u32_e32 vcc, v202, v196
	s_waitcnt lgkmcnt(0)
	v_pk_fma_f32 v[94:95], v[106:107], v[94:95], v[108:109] op_sel_hi:[0,1,1] neg_lo:[1,0,0] neg_hi:[1,0,0]
	v_cvt_pk_bf16_f32 v94, v94, v95
	v_cndmask_b32_e64 v109, 0, 1.0, vcc
	v_cmp_eq_u32_e32 vcc, v203, v196
	s_nop 1
	v_cndmask_b32_e64 v108, 0, 1.0, vcc
	v_pk_fma_f32 v[96:97], v[106:107], v[96:97], v[108:109] op_sel_hi:[0,1,1] neg_lo:[1,0,0] neg_hi:[1,0,0]
	v_cvt_pk_bf16_f32 v95, v96, v97
	ds_write_b64 v186, v[94:95] offset:1088
	ds_read_b32 v94, v187 offset:152
	v_cmp_eq_u32_e32 vcc, v133, v197
	s_nop 1
	v_cndmask_b32_e64 v96, 0, 1.0, vcc
	v_cmp_eq_u32_e32 vcc, v135, v197
	s_nop 1
	v_cndmask_b32_e64 v97, 0, 1.0, vcc
	v_cmp_eq_u32_e32 vcc, v202, v197
	s_waitcnt lgkmcnt(0)
	v_pk_fma_f32 v[82:83], v[94:95], v[82:83], v[96:97] op_sel_hi:[0,1,1] neg_lo:[1,0,0] neg_hi:[1,0,0]
	v_cvt_pk_bf16_f32 v82, v82, v83
	v_cndmask_b32_e64 v97, 0, 1.0, vcc
	v_cmp_eq_u32_e32 vcc, v203, v197
	s_nop 1
	v_cndmask_b32_e64 v96, 0, 1.0, vcc
	v_pk_fma_f32 v[84:85], v[94:95], v[84:85], v[96:97] op_sel_hi:[0,1,1] neg_lo:[1,0,0] neg_hi:[1,0,0]
	v_cvt_pk_bf16_f32 v83, v84, v85
	ds_write_b64 v186, v[82:83] offset:1632
	ds_read_b32 v82, v187 offset:160
	v_cmp_eq_u32_e32 vcc, v133, v198
	s_nop 1
	v_cndmask_b32_e64 v84, 0, 1.0, vcc
	v_cmp_eq_u32_e32 vcc, v135, v198
	s_nop 1
	v_cndmask_b32_e64 v85, 0, 1.0, vcc
	v_cmp_eq_u32_e32 vcc, v202, v198
	s_waitcnt lgkmcnt(0)
	v_pk_fma_f32 v[46:47], v[82:83], v[46:47], v[84:85] op_sel_hi:[0,1,1] neg_lo:[1,0,0] neg_hi:[1,0,0]
	v_cvt_pk_bf16_f32 v46, v46, v47
	v_cndmask_b32_e64 v85, 0, 1.0, vcc
	v_cmp_eq_u32_e32 vcc, v203, v198
	s_nop 1
	v_cndmask_b32_e64 v84, 0, 1.0, vcc
	v_pk_fma_f32 v[48:49], v[82:83], v[48:49], v[84:85] op_sel_hi:[0,1,1] neg_lo:[1,0,0] neg_hi:[1,0,0]
	v_cvt_pk_bf16_f32 v47, v48, v49
	ds_write_b64 v186, v[46:47] offset:2176
	ds_read_b32 v46, v187 offset:168
	v_cmp_eq_u32_e32 vcc, v133, v199
	s_nop 1
	v_cndmask_b32_e64 v48, 0, 1.0, vcc
	v_cmp_eq_u32_e32 vcc, v135, v199
	s_nop 1
	v_cndmask_b32_e64 v49, 0, 1.0, vcc
	v_cmp_eq_u32_e32 vcc, v202, v199
	s_waitcnt lgkmcnt(0)
	v_pk_fma_f32 v[42:43], v[46:47], v[42:43], v[48:49] op_sel_hi:[0,1,1] neg_lo:[1,0,0] neg_hi:[1,0,0]
	v_cvt_pk_bf16_f32 v42, v42, v43
	v_cndmask_b32_e64 v49, 0, 1.0, vcc
	v_cmp_eq_u32_e32 vcc, v203, v199
	s_nop 1
	v_cndmask_b32_e64 v48, 0, 1.0, vcc
	v_pk_fma_f32 v[44:45], v[46:47], v[44:45], v[48:49] op_sel_hi:[0,1,1] neg_lo:[1,0,0] neg_hi:[1,0,0]
	v_cvt_pk_bf16_f32 v43, v44, v45
	ds_write_b64 v186, v[42:43] offset:2720
	ds_read_b32 v42, v187 offset:176
	v_cmp_eq_u32_e32 vcc, v133, v200
	s_nop 1
	v_cndmask_b32_e64 v44, 0, 1.0, vcc
	v_cmp_eq_u32_e32 vcc, v135, v200
	s_nop 1
	v_cndmask_b32_e64 v45, 0, 1.0, vcc
	v_cmp_eq_u32_e32 vcc, v202, v200
	s_waitcnt lgkmcnt(0)
	v_pk_fma_f32 v[38:39], v[42:43], v[38:39], v[44:45] op_sel_hi:[0,1,1] neg_lo:[1,0,0] neg_hi:[1,0,0]
	v_cvt_pk_bf16_f32 v38, v38, v39
	v_cndmask_b32_e64 v45, 0, 1.0, vcc
	v_cmp_eq_u32_e32 vcc, v203, v200
	s_nop 1
	v_cndmask_b32_e64 v44, 0, 1.0, vcc
	v_pk_fma_f32 v[40:41], v[42:43], v[40:41], v[44:45] op_sel_hi:[0,1,1] neg_lo:[1,0,0] neg_hi:[1,0,0]
	v_cvt_pk_bf16_f32 v39, v40, v41
	ds_write_b64 v186, v[38:39] offset:3264
	ds_read_b32 v38, v187 offset:184
	v_cmp_eq_u32_e32 vcc, v133, v201
	s_nop 1
	v_cndmask_b32_e64 v40, 0, 1.0, vcc
	v_cmp_eq_u32_e32 vcc, v135, v201
	s_nop 1
	v_cndmask_b32_e64 v41, 0, 1.0, vcc
	v_cmp_eq_u32_e32 vcc, v202, v201
	s_waitcnt lgkmcnt(0)
	v_pk_fma_f32 v[34:35], v[38:39], v[34:35], v[40:41] op_sel_hi:[0,1,1] neg_lo:[1,0,0] neg_hi:[1,0,0]
	v_cvt_pk_bf16_f32 v34, v34, v35
	v_cndmask_b32_e64 v41, 0, 1.0, vcc
	v_cmp_eq_u32_e32 vcc, v203, v201
	s_nop 1
	v_cndmask_b32_e64 v40, 0, 1.0, vcc
	v_pk_fma_f32 v[36:37], v[38:39], v[36:37], v[40:41] op_sel_hi:[0,1,1] neg_lo:[1,0,0] neg_hi:[1,0,0]
	v_cvt_pk_bf16_f32 v35, v36, v37
	ds_write_b64 v186, v[34:35] offset:3808
	ds_read_b128 v[34:37], v1
	ds_read_b128 v[38:41], v1 offset:64
	ds_read_b128 v[42:45], v1 offset:128
	ds_read_b128 v[46:49], v1 offset:192
	v_mov_b32_e32 v106, v189
	s_waitcnt vmcnt(15)
	s_waitcnt vmcnt(14)
	s_waitcnt vmcnt(13)
	s_waitcnt vmcnt(12)
	s_waitcnt vmcnt(11)
	s_waitcnt vmcnt(10)
	s_waitcnt vmcnt(9)
	s_waitcnt vmcnt(8)
	ds_read_b32 v82, v187
	v_add_u32_e32 v107, 1, v106
	v_cmp_eq_u32_e32 vcc, v106, v132
	v_add_u32_e32 v108, 3, v106
	v_add_u32_e32 v109, 2, v106
	v_cndmask_b32_e64 v84, 0, 1.0, vcc
	v_cmp_eq_u32_e32 vcc, v107, v132
	s_nop 1
	v_cndmask_b32_e64 v85, 0, 1.0, vcc
	v_cmp_eq_u32_e32 vcc, v108, v132
	s_waitcnt lgkmcnt(0)
	v_pk_fma_f32 v[94:95], v[82:83], v[118:119], v[84:85] op_sel_hi:[0,1,1] neg_lo:[1,0,0] neg_hi:[1,0,0]
	v_cvt_pk_bf16_f32 v94, v94, v95
	v_cndmask_b32_e64 v97, 0, 1.0, vcc
	v_cmp_eq_u32_e32 vcc, v109, v132
	s_nop 1
	v_cndmask_b32_e64 v96, 0, 1.0, vcc
	v_pk_fma_f32 v[82:83], v[82:83], v[120:121], v[96:97] op_sel_hi:[0,1,1] neg_lo:[1,0,0] neg_hi:[1,0,0]
	v_cvt_pk_bf16_f32 v95, v82, v83
	ds_write_b64 v186, v[94:95]
	ds_read_b32 v82, v187 offset:8
	v_cmp_eq_u32_e32 vcc, v106, v193
	s_nop 1
	v_cndmask_b32_e64 v94, 0, 1.0, vcc
	v_cmp_eq_u32_e32 vcc, v107, v193
	s_nop 1
	v_cndmask_b32_e64 v95, 0, 1.0, vcc
	v_cmp_eq_u32_e32 vcc, v108, v193
	s_waitcnt lgkmcnt(0)
	v_pk_fma_f32 v[94:95], v[82:83], v[110:111], v[94:95] op_sel_hi:[0,1,1] neg_lo:[1,0,0] neg_hi:[1,0,0]
	v_cvt_pk_bf16_f32 v94, v94, v95
	v_cndmask_b32_e64 v85, 0, 1.0, vcc
	v_pk_fma_f32 v[82:83], v[82:83], v[112:113], v[84:85] op_sel_hi:[0,1,1] neg_lo:[1,0,0] neg_hi:[1,0,0]
	v_cvt_pk_bf16_f32 v95, v82, v83
	ds_write_b64 v186, v[94:95] offset:544
	ds_read_b32 v82, v187 offset:16
	v_cmp_eq_u32_e32 vcc, v106, v192
	s_nop 1
	v_cndmask_b32_e64 v84, 0, 1.0, vcc
	v_cmp_eq_u32_e32 vcc, v107, v192
	s_nop 1
	v_cndmask_b32_e64 v85, 0, 1.0, vcc
	v_cmp_eq_u32_e32 vcc, v108, v192
	s_waitcnt lgkmcnt(0)
	v_pk_fma_f32 v[84:85], v[82:83], v[98:99], v[84:85] op_sel_hi:[0,1,1] neg_lo:[1,0,0] neg_hi:[1,0,0]
	v_cvt_pk_bf16_f32 v84, v84, v85
	v_cndmask_b32_e64 v95, 0, 1.0, vcc
	v_cmp_eq_u32_e32 vcc, v109, v192
	s_nop 1
	v_cndmask_b32_e64 v94, 0, 1.0, vcc
	v_pk_fma_f32 v[82:83], v[82:83], v[100:101], v[94:95] op_sel_hi:[0,1,1] neg_lo:[1,0,0] neg_hi:[1,0,0]
	v_cvt_pk_bf16_f32 v85, v82, v83
	ds_write_b64 v186, v[84:85] offset:1088
	ds_read_b32 v82, v187 offset:24
	v_cmp_eq_u32_e32 vcc, v106, v190
	s_nop 1
	v_cndmask_b32_e64 v84, 0, 1.0, vcc
	v_cmp_eq_u32_e32 vcc, v107, v190
	s_nop 1
	v_cndmask_b32_e64 v85, 0, 1.0, vcc
	v_cmp_eq_u32_e32 vcc, v108, v190
	s_waitcnt lgkmcnt(0)
	v_pk_fma_f32 v[84:85], v[82:83], v[86:87], v[84:85] op_sel_hi:[0,1,1] neg_lo:[1,0,0] neg_hi:[1,0,0]
	v_cvt_pk_bf16_f32 v84, v84, v85
	v_cndmask_b32_e64 v87, 0, 1.0, vcc
	v_cmp_eq_u32_e32 vcc, v109, v190
	s_nop 1
	v_cndmask_b32_e64 v86, 0, 1.0, vcc
	v_pk_fma_f32 v[82:83], v[82:83], v[88:89], v[86:87] op_sel_hi:[0,1,1] neg_lo:[1,0,0] neg_hi:[1,0,0]
	v_cvt_pk_bf16_f32 v85, v82, v83
	ds_write_b64 v186, v[84:85] offset:1632
	ds_read_b32 v82, v187 offset:32
	v_cmp_eq_u32_e32 vcc, v106, v149
	s_nop 1
	v_cndmask_b32_e64 v84, 0, 1.0, vcc
	v_cmp_eq_u32_e32 vcc, v107, v149
	s_nop 1
	v_cndmask_b32_e64 v85, 0, 1.0, vcc
	v_cmp_eq_u32_e32 vcc, v108, v149
	s_waitcnt lgkmcnt(0)
	v_pk_fma_f32 v[62:63], v[82:83], v[62:63], v[84:85] op_sel_hi:[0,1,1] neg_lo:[1,0,0] neg_hi:[1,0,0]
	v_cvt_pk_bf16_f32 v62, v62, v63
	v_cndmask_b32_e64 v85, 0, 1.0, vcc
	v_cmp_eq_u32_e32 vcc, v109, v149
	s_nop 1
	v_cndmask_b32_e64 v84, 0, 1.0, vcc
	v_pk_fma_f32 v[64:65], v[82:83], v[64:65], v[84:85] op_sel_hi:[0,1,1] neg_lo:[1,0,0] neg_hi:[1,0,0]
	v_cvt_pk_bf16_f32 v63, v64, v65
	ds_write_b64 v186, v[62:63] offset:2176
	ds_read_b32 v62, v187 offset:40
	v_cmp_eq_u32_e32 vcc, v106, v148
	s_nop 1
	v_cndmask_b32_e64 v64, 0, 1.0, vcc
	v_cmp_eq_u32_e32 vcc, v107, v148
	s_nop 1
	v_cndmask_b32_e64 v65, 0, 1.0, vcc
	v_cmp_eq_u32_e32 vcc, v108, v148
	s_waitcnt lgkmcnt(0)
	v_pk_fma_f32 v[58:59], v[62:63], v[58:59], v[64:65] op_sel_hi:[0,1,1] neg_lo:[1,0,0] neg_hi:[1,0,0]
	v_cvt_pk_bf16_f32 v58, v58, v59
	v_cndmask_b32_e64 v65, 0, 1.0, vcc
	v_cmp_eq_u32_e32 vcc, v109, v148
	s_nop 1
	v_cndmask_b32_e64 v64, 0, 1.0, vcc
	v_pk_fma_f32 v[60:61], v[62:63], v[60:61], v[64:65] op_sel_hi:[0,1,1] neg_lo:[1,0,0] neg_hi:[1,0,0]
	v_cvt_pk_bf16_f32 v59, v60, v61
	ds_write_b64 v186, v[58:59] offset:2720
	ds_read_b32 v58, v187 offset:48
	v_cmp_eq_u32_e32 vcc, v106, v147
	s_nop 1
	v_cndmask_b32_e64 v60, 0, 1.0, vcc
	v_cmp_eq_u32_e32 vcc, v107, v147
	s_nop 1
	v_cndmask_b32_e64 v61, 0, 1.0, vcc
	v_cmp_eq_u32_e32 vcc, v108, v147
	s_waitcnt lgkmcnt(0)
	v_pk_fma_f32 v[54:55], v[58:59], v[54:55], v[60:61] op_sel_hi:[0,1,1] neg_lo:[1,0,0] neg_hi:[1,0,0]
	v_cvt_pk_bf16_f32 v54, v54, v55
	v_cndmask_b32_e64 v61, 0, 1.0, vcc
	v_cmp_eq_u32_e32 vcc, v109, v147
	s_nop 1
	v_cndmask_b32_e64 v60, 0, 1.0, vcc
	v_pk_fma_f32 v[56:57], v[58:59], v[56:57], v[60:61] op_sel_hi:[0,1,1] neg_lo:[1,0,0] neg_hi:[1,0,0]
	v_cvt_pk_bf16_f32 v55, v56, v57
	ds_write_b64 v186, v[54:55] offset:3264
	ds_read_b32 v54, v187 offset:56
	v_cmp_eq_u32_e32 vcc, v106, v146
	s_nop 1
	v_cndmask_b32_e64 v56, 0, 1.0, vcc
	v_cmp_eq_u32_e32 vcc, v107, v146
	s_nop 1
	v_cndmask_b32_e64 v57, 0, 1.0, vcc
	v_cmp_eq_u32_e32 vcc, v108, v146
	s_waitcnt lgkmcnt(0)
	v_pk_fma_f32 v[50:51], v[54:55], v[50:51], v[56:57] op_sel_hi:[0,1,1] neg_lo:[1,0,0] neg_hi:[1,0,0]
	v_cvt_pk_bf16_f32 v50, v50, v51
	v_cndmask_b32_e64 v57, 0, 1.0, vcc
	v_cmp_eq_u32_e32 vcc, v109, v146
	s_nop 1
	v_cndmask_b32_e64 v56, 0, 1.0, vcc
	v_pk_fma_f32 v[52:53], v[54:55], v[52:53], v[56:57] op_sel_hi:[0,1,1] neg_lo:[1,0,0] neg_hi:[1,0,0]
	v_cvt_pk_bf16_f32 v51, v52, v53
	ds_write_b64 v186, v[50:51] offset:3808
	ds_read_b128 v[50:53], v1
	ds_read_b128 v[54:57], v1 offset:64
	ds_read_b128 v[58:61], v1 offset:128
	ds_read_b128 v[62:65], v1 offset:192
	v_lshl_add_u64 v[82:83], v[168:169], 0, s[8:9]
	v_lshl_add_u64 v[84:85], v[170:171], 0, s[8:9]
	v_lshl_add_u64 v[86:87], v[172:173], 0, s[8:9]
	v_lshl_add_u64 v[88:89], v[174:175], 0, s[8:9]
	v_lshl_add_u64 v[94:95], v[176:177], 0, s[8:9]
	v_lshl_add_u64 v[96:97], v[178:179], 0, s[8:9]
	v_lshl_add_u64 v[122:123], v[180:181], 0, s[8:9]
	v_lshl_add_u64 v[124:125], v[182:183], 0, s[8:9]
	global_load_dwordx4 v[134:137], v[82:83], off nt
	global_load_dwordx4 v[118:121], v[84:85], off nt
	global_load_dwordx4 v[110:113], v[86:87], off nt
	global_load_dwordx4 v[106:109], v[88:89], off nt
	global_load_dwordx4 v[98:101], v[94:95], off nt
	s_nop 0
	global_load_dwordx4 v[94:97], v[96:97], off nt
	s_nop 0
	global_load_dwordx4 v[86:89], v[122:123], off nt
	global_load_dwordx4 v[82:85], v[124:125], off nt
	v_mov_b32_e32 v132, v189
	s_waitcnt vmcnt(15)
	s_waitcnt vmcnt(14)
	s_waitcnt vmcnt(13)
	s_waitcnt vmcnt(12)
	s_waitcnt vmcnt(11)
	s_waitcnt vmcnt(10)
	s_waitcnt vmcnt(9)
	s_waitcnt vmcnt(8)
	ds_read_b32 v122, v187 offset:64
	v_add_u32_e32 v133, 1, v132
	v_cmp_eq_u32_e32 vcc, v132, v138
	v_add_u32_e32 v146, 3, v132
	v_add_u32_e32 v147, 2, v132
	v_cndmask_b32_e64 v124, 0, 1.0, vcc
	v_cmp_eq_u32_e32 vcc, v133, v138
	s_nop 1
	v_cndmask_b32_e64 v125, 0, 1.0, vcc
	v_cmp_eq_u32_e32 vcc, v146, v138
	s_waitcnt lgkmcnt(0)
	v_pk_fma_f32 v[124:125], v[122:123], v[126:127], v[124:125] op_sel_hi:[0,1,1] neg_lo:[1,0,0] neg_hi:[1,0,0]
	v_cvt_pk_bf16_f32 v124, v124, v125
	v_cndmask_b32_e64 v127, 0, 1.0, vcc
	v_cmp_eq_u32_e32 vcc, v147, v138
	s_nop 1
	v_cndmask_b32_e64 v126, 0, 1.0, vcc
	v_pk_fma_f32 v[122:123], v[122:123], v[128:129], v[126:127] op_sel_hi:[0,1,1] neg_lo:[1,0,0] neg_hi:[1,0,0]
	v_cvt_pk_bf16_f32 v125, v122, v123
	ds_write_b64 v186, v[124:125]
	ds_read_b32 v122, v187 offset:72
	v_cmp_eq_u32_e32 vcc, v132, v139
	s_nop 1
	v_cndmask_b32_e64 v124, 0, 1.0, vcc
	v_cmp_eq_u32_e32 vcc, v133, v139
	s_nop 1
	v_cndmask_b32_e64 v125, 0, 1.0, vcc
	v_cmp_eq_u32_e32 vcc, v146, v139
	s_waitcnt lgkmcnt(0)
	v_pk_fma_f32 v[114:115], v[122:123], v[114:115], v[124:125] op_sel_hi:[0,1,1] neg_lo:[1,0,0] neg_hi:[1,0,0]
	v_cvt_pk_bf16_f32 v114, v114, v115
	v_cndmask_b32_e64 v125, 0, 1.0, vcc
	v_cmp_eq_u32_e32 vcc, v147, v139
	s_nop 1
	v_cndmask_b32_e64 v124, 0, 1.0, vcc
	v_pk_fma_f32 v[116:117], v[122:123], v[116:117], v[124:125] op_sel_hi:[0,1,1] neg_lo:[1,0,0] neg_hi:[1,0,0]
	v_cvt_pk_bf16_f32 v115, v116, v117
	ds_write_b64 v186, v[114:115] offset:544
	ds_read_b32 v114, v187 offset:80
	v_cmp_eq_u32_e32 vcc, v132, v140
	s_nop 1
	v_cndmask_b32_e64 v116, 0, 1.0, vcc
	v_cmp_eq_u32_e32 vcc, v133, v140
	s_nop 1
	v_cndmask_b32_e64 v117, 0, 1.0, vcc
	v_cmp_eq_u32_e32 vcc, v146, v140
	s_waitcnt lgkmcnt(0)
	v_pk_fma_f32 v[102:103], v[114:115], v[102:103], v[116:117] op_sel_hi:[0,1,1] neg_lo:[1,0,0] neg_hi:[1,0,0]
	v_cvt_pk_bf16_f32 v102, v102, v103
	v_cndmask_b32_e64 v117, 0, 1.0, vcc
	v_cmp_eq_u32_e32 vcc, v147, v140
	s_nop 1
	v_cndmask_b32_e64 v116, 0, 1.0, vcc
	v_pk_fma_f32 v[104:105], v[114:115], v[104:105], v[116:117] op_sel_hi:[0,1,1] neg_lo:[1,0,0] neg_hi:[1,0,0]
	v_cvt_pk_bf16_f32 v103, v104, v105
	ds_write_b64 v186, v[102:103] offset:1088
	ds_read_b32 v102, v187 offset:88
	v_cmp_eq_u32_e32 vcc, v132, v141
	s_nop 1
	v_cndmask_b32_e64 v104, 0, 1.0, vcc
	v_cmp_eq_u32_e32 vcc, v133, v141
	s_nop 1
	v_cndmask_b32_e64 v105, 0, 1.0, vcc
	v_cmp_eq_u32_e32 vcc, v146, v141
	s_waitcnt lgkmcnt(0)
	v_pk_fma_f32 v[90:91], v[102:103], v[90:91], v[104:105] op_sel_hi:[0,1,1] neg_lo:[1,0,0] neg_hi:[1,0,0]
	v_cvt_pk_bf16_f32 v90, v90, v91
	v_cndmask_b32_e64 v105, 0, 1.0, vcc
	v_cmp_eq_u32_e32 vcc, v147, v141
	s_nop 1
	v_cndmask_b32_e64 v104, 0, 1.0, vcc
	v_pk_fma_f32 v[92:93], v[102:103], v[92:93], v[104:105] op_sel_hi:[0,1,1] neg_lo:[1,0,0] neg_hi:[1,0,0]
	v_cvt_pk_bf16_f32 v91, v92, v93
	ds_write_b64 v186, v[90:91] offset:1632
	ds_read_b32 v90, v187 offset:96
	v_cmp_eq_u32_e32 vcc, v132, v142
	s_nop 1
	v_cndmask_b32_e64 v92, 0, 1.0, vcc
	v_cmp_eq_u32_e32 vcc, v133, v142
	s_nop 1
	v_cndmask_b32_e64 v93, 0, 1.0, vcc
	v_cmp_eq_u32_e32 vcc, v146, v142
	s_waitcnt lgkmcnt(0)
	v_pk_fma_f32 v[78:79], v[90:91], v[78:79], v[92:93] op_sel_hi:[0,1,1] neg_lo:[1,0,0] neg_hi:[1,0,0]
	v_cvt_pk_bf16_f32 v78, v78, v79
	v_cndmask_b32_e64 v93, 0, 1.0, vcc
	v_cmp_eq_u32_e32 vcc, v147, v142
	s_nop 1
	v_cndmask_b32_e64 v92, 0, 1.0, vcc
	v_pk_fma_f32 v[80:81], v[90:91], v[80:81], v[92:93] op_sel_hi:[0,1,1] neg_lo:[1,0,0] neg_hi:[1,0,0]
	v_cvt_pk_bf16_f32 v79, v80, v81
	ds_write_b64 v186, v[78:79] offset:2176
	ds_read_b32 v78, v187 offset:104
	v_cmp_eq_u32_e32 vcc, v132, v143
	s_nop 1
	v_cndmask_b32_e64 v80, 0, 1.0, vcc
	v_cmp_eq_u32_e32 vcc, v133, v143
	s_nop 1
	v_cndmask_b32_e64 v81, 0, 1.0, vcc
	v_cmp_eq_u32_e32 vcc, v146, v143
	s_waitcnt lgkmcnt(0)
	v_pk_fma_f32 v[74:75], v[78:79], v[74:75], v[80:81] op_sel_hi:[0,1,1] neg_lo:[1,0,0] neg_hi:[1,0,0]
	v_cvt_pk_bf16_f32 v74, v74, v75
	v_cndmask_b32_e64 v81, 0, 1.0, vcc
	v_cmp_eq_u32_e32 vcc, v147, v143
	s_nop 1
	v_cndmask_b32_e64 v80, 0, 1.0, vcc
	v_pk_fma_f32 v[76:77], v[78:79], v[76:77], v[80:81] op_sel_hi:[0,1,1] neg_lo:[1,0,0] neg_hi:[1,0,0]
	v_cvt_pk_bf16_f32 v75, v76, v77
	ds_write_b64 v186, v[74:75] offset:2720
	ds_read_b32 v74, v187 offset:112
	v_cmp_eq_u32_e32 vcc, v132, v144
	s_nop 1
	v_cndmask_b32_e64 v76, 0, 1.0, vcc
	v_cmp_eq_u32_e32 vcc, v133, v144
	s_nop 1
	v_cndmask_b32_e64 v77, 0, 1.0, vcc
	v_cmp_eq_u32_e32 vcc, v146, v144
	s_waitcnt lgkmcnt(0)
	v_pk_fma_f32 v[70:71], v[74:75], v[70:71], v[76:77] op_sel_hi:[0,1,1] neg_lo:[1,0,0] neg_hi:[1,0,0]
	v_cvt_pk_bf16_f32 v70, v70, v71
	v_cndmask_b32_e64 v77, 0, 1.0, vcc
	v_cmp_eq_u32_e32 vcc, v147, v144
	s_nop 1
	v_cndmask_b32_e64 v76, 0, 1.0, vcc
	v_pk_fma_f32 v[72:73], v[74:75], v[72:73], v[76:77] op_sel_hi:[0,1,1] neg_lo:[1,0,0] neg_hi:[1,0,0]
	v_cvt_pk_bf16_f32 v71, v72, v73
	ds_write_b64 v186, v[70:71] offset:3264
	ds_read_b32 v70, v187 offset:120
	v_cmp_eq_u32_e32 vcc, v132, v145
	s_nop 1
	v_cndmask_b32_e64 v72, 0, 1.0, vcc
	v_cmp_eq_u32_e32 vcc, v133, v145
	s_nop 1
	v_cndmask_b32_e64 v73, 0, 1.0, vcc
	v_cmp_eq_u32_e32 vcc, v146, v145
	s_waitcnt lgkmcnt(0)
	v_pk_fma_f32 v[66:67], v[70:71], v[66:67], v[72:73] op_sel_hi:[0,1,1] neg_lo:[1,0,0] neg_hi:[1,0,0]
	v_cvt_pk_bf16_f32 v66, v66, v67
	v_cndmask_b32_e64 v73, 0, 1.0, vcc
	v_cmp_eq_u32_e32 vcc, v147, v145
	s_nop 1
	v_cndmask_b32_e64 v72, 0, 1.0, vcc
	v_pk_fma_f32 v[68:69], v[70:71], v[68:69], v[72:73] op_sel_hi:[0,1,1] neg_lo:[1,0,0] neg_hi:[1,0,0]
	v_cvt_pk_bf16_f32 v67, v68, v69
	ds_write_b64 v186, v[66:67] offset:3808
	ds_read_b128 v[66:69], v1
	ds_read_b128 v[70:73], v1 offset:64
	ds_read_b128 v[74:77], v1 offset:128
	ds_read_b128 v[78:81], v1 offset:192
	v_lshl_add_u64 v[90:91], v[130:131], 0, s[0:1]
	v_add_co_u32_e32 v92, vcc, s7, v90
	s_nop 1
	v_addc_co_u32_e32 v93, vcc, 0, v91, vcc
	global_load_dwordx4 v[146:149], v[90:91], off nt
	global_load_dwordx4 v[142:145], v[92:93], off nt
	v_add_co_u32_e32 v92, vcc, s36, v90
	s_nop 1
	v_addc_co_u32_e32 v93, vcc, 0, v91, vcc
	v_add_co_u32_e32 v102, vcc, s37, v90
	s_nop 1
	v_addc_co_u32_e32 v103, vcc, 0, v91, vcc
	global_load_dwordx4 v[138:141], v[92:93], off nt
	global_load_dwordx4 v[130:133], v[102:103], off nt
	v_add_co_u32_e32 v92, vcc, s38, v90
	s_nop 1
	v_addc_co_u32_e32 v93, vcc, 0, v91, vcc
	v_add_co_u32_e32 v102, vcc, s39, v90
	s_nop 1
	v_addc_co_u32_e32 v103, vcc, 0, v91, vcc
	global_load_dwordx4 v[126:129], v[92:93], off nt
	global_load_dwordx4 v[122:125], v[102:103], off nt
	v_add_co_u32_e32 v92, vcc, s41, v90
	s_nop 1
	v_addc_co_u32_e32 v93, vcc, 0, v91, vcc
	v_add_co_u32_e32 v90, vcc, s42, v90
	s_nop 1
	v_addc_co_u32_e32 v91, vcc, 0, v91, vcc
	global_load_dwordx4 v[114:117], v[92:93], off nt
	global_load_dwordx4 v[102:105], v[90:91], off nt
	s_waitcnt vmcnt(15)
	s_waitcnt vmcnt(14)
	s_waitcnt vmcnt(13)
	s_waitcnt vmcnt(12)
	s_waitcnt vmcnt(11)
	s_waitcnt vmcnt(10)
	s_waitcnt vmcnt(9)
	s_waitcnt vmcnt(8)
	ds_read_b32 v90, v187 offset:128
	v_add_u32_e32 v190, 1, v189
	v_cmp_eq_u32_e32 vcc, v189, v194
	v_add_u32_e32 v192, 3, v189
	v_add_u32_e32 v193, 2, v189
	v_cndmask_b32_e64 v92, 0, 1.0, vcc
	v_cmp_eq_u32_e32 vcc, v190, v194
	s_nop 1
	v_cndmask_b32_e64 v93, 0, 1.0, vcc
	v_cmp_eq_u32_e32 vcc, v192, v194
	s_waitcnt lgkmcnt(0)
	v_pk_fma_f32 v[92:93], v[90:91], v[134:135], v[92:93] op_sel_hi:[0,1,1] neg_lo:[1,0,0] neg_hi:[1,0,0]
	v_cvt_pk_bf16_f32 v92, v92, v93
	v_cndmask_b32_e64 v135, 0, 1.0, vcc
	v_cmp_eq_u32_e32 vcc, v193, v194
	s_nop 1
	v_cndmask_b32_e64 v134, 0, 1.0, vcc
	v_pk_fma_f32 v[90:91], v[90:91], v[136:137], v[134:135] op_sel_hi:[0,1,1] neg_lo:[1,0,0] neg_hi:[1,0,0]
	v_cvt_pk_bf16_f32 v93, v90, v91
	ds_write_b64 v186, v[92:93]
	ds_read_b32 v90, v187 offset:136
	v_cmp_eq_u32_e32 vcc, v189, v195
	s_nop 1
	v_cndmask_b32_e64 v92, 0, 1.0, vcc
	v_cmp_eq_u32_e32 vcc, v190, v195
	s_nop 1
	v_cndmask_b32_e64 v93, 0, 1.0, vcc
	v_cmp_eq_u32_e32 vcc, v192, v195
	s_waitcnt lgkmcnt(0)
	v_pk_fma_f32 v[92:93], v[90:91], v[118:119], v[92:93] op_sel_hi:[0,1,1] neg_lo:[1,0,0] neg_hi:[1,0,0]
	v_cvt_pk_bf16_f32 v92, v92, v93
	v_cndmask_b32_e64 v119, 0, 1.0, vcc
	v_cmp_eq_u32_e32 vcc, v193, v195
	s_nop 1
	v_cndmask_b32_e64 v118, 0, 1.0, vcc
	v_pk_fma_f32 v[90:91], v[90:91], v[120:121], v[118:119] op_sel_hi:[0,1,1] neg_lo:[1,0,0] neg_hi:[1,0,0]
	v_cvt_pk_bf16_f32 v93, v90, v91
	ds_write_b64 v186, v[92:93] offset:544
	ds_read_b32 v90, v187 offset:144
	v_cmp_eq_u32_e32 vcc, v189, v196
	s_nop 1
	v_cndmask_b32_e64 v92, 0, 1.0, vcc
	v_cmp_eq_u32_e32 vcc, v190, v196
	s_nop 1
	v_cndmask_b32_e64 v93, 0, 1.0, vcc
	v_cmp_eq_u32_e32 vcc, v192, v196
	s_waitcnt lgkmcnt(0)
	v_pk_fma_f32 v[92:93], v[90:91], v[110:111], v[92:93] op_sel_hi:[0,1,1] neg_lo:[1,0,0] neg_hi:[1,0,0]
	v_cvt_pk_bf16_f32 v92, v92, v93
	v_cndmask_b32_e64 v111, 0, 1.0, vcc
	v_cmp_eq_u32_e32 vcc, v193, v196
	s_nop 1
	v_cndmask_b32_e64 v110, 0, 1.0, vcc
	v_pk_fma_f32 v[90:91], v[90:91], v[112:113], v[110:111] op_sel_hi:[0,1,1] neg_lo:[1,0,0] neg_hi:[1,0,0]
	v_cvt_pk_bf16_f32 v93, v90, v91
	ds_write_b64 v186, v[92:93] offset:1088
	ds_read_b32 v90, v187 offset:152
	v_cmp_eq_u32_e32 vcc, v189, v197
	s_nop 1
	v_cndmask_b32_e64 v92, 0, 1.0, vcc
	v_cmp_eq_u32_e32 vcc, v190, v197
	s_nop 1
	v_cndmask_b32_e64 v93, 0, 1.0, vcc
	v_cmp_eq_u32_e32 vcc, v192, v197
	s_waitcnt lgkmcnt(0)
	v_pk_fma_f32 v[92:93], v[90:91], v[106:107], v[92:93] op_sel_hi:[0,1,1] neg_lo:[1,0,0] neg_hi:[1,0,0]
	v_cvt_pk_bf16_f32 v92, v92, v93
	v_cndmask_b32_e64 v107, 0, 1.0, vcc
	v_cmp_eq_u32_e32 vcc, v193, v197
	s_nop 1
	v_cndmask_b32_e64 v106, 0, 1.0, vcc
	v_pk_fma_f32 v[90:91], v[90:91], v[108:109], v[106:107] op_sel_hi:[0,1,1] neg_lo:[1,0,0] neg_hi:[1,0,0]
	v_cvt_pk_bf16_f32 v93, v90, v91
	ds_write_b64 v186, v[92:93] offset:1632
	ds_read_b32 v90, v187 offset:160
	v_cmp_eq_u32_e32 vcc, v189, v198
	s_nop 1
	v_cndmask_b32_e64 v92, 0, 1.0, vcc
	v_cmp_eq_u32_e32 vcc, v190, v198
	s_nop 1
	v_cndmask_b32_e64 v93, 0, 1.0, vcc
	v_cmp_eq_u32_e32 vcc, v192, v198
	s_waitcnt lgkmcnt(0)
	v_pk_fma_f32 v[92:93], v[90:91], v[98:99], v[92:93] op_sel_hi:[0,1,1] neg_lo:[1,0,0] neg_hi:[1,0,0]
	v_cvt_pk_bf16_f32 v92, v92, v93
	v_cndmask_b32_e64 v99, 0, 1.0, vcc
	v_cmp_eq_u32_e32 vcc, v193, v198
	s_nop 1
	v_cndmask_b32_e64 v98, 0, 1.0, vcc
	v_pk_fma_f32 v[90:91], v[90:91], v[100:101], v[98:99] op_sel_hi:[0,1,1] neg_lo:[1,0,0] neg_hi:[1,0,0]
	v_cvt_pk_bf16_f32 v93, v90, v91
	ds_write_b64 v186, v[92:93] offset:2176
	ds_read_b32 v90, v187 offset:168
	v_cmp_eq_u32_e32 vcc, v189, v199
	s_nop 1
	v_cndmask_b32_e64 v92, 0, 1.0, vcc
	v_cmp_eq_u32_e32 vcc, v190, v199
	s_nop 1
	v_cndmask_b32_e64 v93, 0, 1.0, vcc
	v_cmp_eq_u32_e32 vcc, v192, v199
	s_waitcnt lgkmcnt(0)
	v_pk_fma_f32 v[92:93], v[90:91], v[94:95], v[92:93] op_sel_hi:[0,1,1] neg_lo:[1,0,0] neg_hi:[1,0,0]
	v_cvt_pk_bf16_f32 v92, v92, v93
	v_cndmask_b32_e64 v95, 0, 1.0, vcc
	v_cmp_eq_u32_e32 vcc, v193, v199
	s_nop 1
	v_cndmask_b32_e64 v94, 0, 1.0, vcc
	v_pk_fma_f32 v[90:91], v[90:91], v[96:97], v[94:95] op_sel_hi:[0,1,1] neg_lo:[1,0,0] neg_hi:[1,0,0]
	v_cvt_pk_bf16_f32 v93, v90, v91
	ds_write_b64 v186, v[92:93] offset:2720
	ds_read_b32 v90, v187 offset:176
	v_cmp_eq_u32_e32 vcc, v189, v200
	s_nop 1
	v_cndmask_b32_e64 v92, 0, 1.0, vcc
	v_cmp_eq_u32_e32 vcc, v190, v200
	s_nop 1
	v_cndmask_b32_e64 v93, 0, 1.0, vcc
	v_cmp_eq_u32_e32 vcc, v192, v200
	s_waitcnt lgkmcnt(0)
	v_pk_fma_f32 v[86:87], v[90:91], v[86:87], v[92:93] op_sel_hi:[0,1,1] neg_lo:[1,0,0] neg_hi:[1,0,0]
	v_cvt_pk_bf16_f32 v86, v86, v87
	v_cndmask_b32_e64 v93, 0, 1.0, vcc
	v_cmp_eq_u32_e32 vcc, v193, v200
	s_nop 1
	v_cndmask_b32_e64 v92, 0, 1.0, vcc
	v_pk_fma_f32 v[88:89], v[90:91], v[88:89], v[92:93] op_sel_hi:[0,1,1] neg_lo:[1,0,0] neg_hi:[1,0,0]
	v_cvt_pk_bf16_f32 v87, v88, v89
	ds_write_b64 v186, v[86:87] offset:3264
	ds_read_b32 v86, v187 offset:184
	v_cmp_eq_u32_e32 vcc, v189, v201
	s_nop 1
	v_cndmask_b32_e64 v88, 0, 1.0, vcc
	v_cmp_eq_u32_e32 vcc, v190, v201
	s_nop 1
	v_cndmask_b32_e64 v89, 0, 1.0, vcc
	v_cmp_eq_u32_e32 vcc, v192, v201
	s_waitcnt lgkmcnt(0)
	v_pk_fma_f32 v[82:83], v[86:87], v[82:83], v[88:89] op_sel_hi:[0,1,1] neg_lo:[1,0,0] neg_hi:[1,0,0]
	v_cvt_pk_bf16_f32 v82, v82, v83
	v_cndmask_b32_e64 v89, 0, 1.0, vcc
	v_cmp_eq_u32_e32 vcc, v193, v201
	s_nop 1
	v_cndmask_b32_e64 v88, 0, 1.0, vcc
	v_pk_fma_f32 v[84:85], v[86:87], v[84:85], v[88:89] op_sel_hi:[0,1,1] neg_lo:[1,0,0] neg_hi:[1,0,0]
	v_cvt_pk_bf16_f32 v83, v84, v85
	ds_write_b64 v186, v[82:83] offset:3808
	ds_read_b128 v[82:85], v1
	ds_read_b128 v[86:89], v1 offset:64
	ds_read_b128 v[90:93], v1 offset:128
	ds_read_b128 v[94:97], v1 offset:192
	v_lshl_add_u64 v[98:99], v[150:151], 0, s[0:1]
	v_lshl_add_u64 v[192:193], v[164:165], 0, s[0:1]
	v_lshl_add_u64 v[196:197], v[166:167], 0, s[0:1]
	v_lshl_add_u64 v[100:101], v[152:153], 0, s[0:1]
	v_lshl_add_u64 v[106:107], v[156:157], 0, s[0:1]
	v_lshl_add_u64 v[108:109], v[158:159], 0, s[0:1]
	v_lshl_add_u64 v[110:111], v[160:161], 0, s[0:1]
	v_lshl_add_u64 v[112:113], v[162:163], 0, s[0:1]
	global_load_dwordx4 v[118:121], v[98:99], off nt
	global_load_dwordx4 v[134:137], v[100:101], off nt
	global_load_dwordx4 v[150:153], v[106:107], off nt
	global_load_dwordx4 v[156:159], v[108:109], off nt
	global_load_dwordx4 v[160:163], v[110:111], off nt
	global_load_dwordx4 v[164:167], v[112:113], off nt
	s_nop 0
	global_load_dwordx4 v[192:195], v[192:193], off nt
	s_nop 0
	global_load_dwordx4 v[196:199], v[196:197], off nt
	v_mov_b32_e32 v98, v188
	s_waitcnt vmcnt(15)
	s_waitcnt vmcnt(14)
	s_waitcnt vmcnt(13)
	s_waitcnt vmcnt(12)
	s_waitcnt vmcnt(11)
	s_waitcnt vmcnt(10)
	s_waitcnt vmcnt(9)
	s_waitcnt vmcnt(8)
	ds_read_b32 v98, v187
	s_waitcnt lgkmcnt(0)
	v_pk_fma_f32 v[100:101], v[98:99], v[146:147], 0 op_sel_hi:[0,1,0] neg_lo:[1,0,0] neg_hi:[1,0,0]
	v_pk_fma_f32 v[98:99], v[98:99], v[148:149], 0 op_sel_hi:[0,1,0] neg_lo:[1,0,0] neg_hi:[1,0,0]
	v_cvt_pk_bf16_f32 v100, v100, v101
	v_cvt_pk_bf16_f32 v101, v98, v99
	ds_write_b64 v186, v[100:101]
	ds_read_b32 v98, v187 offset:8
	s_waitcnt lgkmcnt(0)
	v_pk_fma_f32 v[100:101], v[98:99], v[142:143], 0 op_sel_hi:[0,1,0] neg_lo:[1,0,0] neg_hi:[1,0,0]
	v_pk_fma_f32 v[98:99], v[98:99], v[144:145], 0 op_sel_hi:[0,1,0] neg_lo:[1,0,0] neg_hi:[1,0,0]
	v_cvt_pk_bf16_f32 v100, v100, v101
	v_cvt_pk_bf16_f32 v101, v98, v99
	ds_write_b64 v186, v[100:101] offset:544
	ds_read_b32 v98, v187 offset:16
	s_waitcnt lgkmcnt(0)
	v_pk_fma_f32 v[100:101], v[98:99], v[138:139], 0 op_sel_hi:[0,1,0] neg_lo:[1,0,0] neg_hi:[1,0,0]
	v_pk_fma_f32 v[98:99], v[98:99], v[140:141], 0 op_sel_hi:[0,1,0] neg_lo:[1,0,0] neg_hi:[1,0,0]
	v_cvt_pk_bf16_f32 v100, v100, v101
	v_cvt_pk_bf16_f32 v101, v98, v99
	ds_write_b64 v186, v[100:101] offset:1088
	ds_read_b32 v98, v187 offset:24
	s_waitcnt lgkmcnt(0)
	v_pk_fma_f32 v[100:101], v[98:99], v[130:131], 0 op_sel_hi:[0,1,0] neg_lo:[1,0,0] neg_hi:[1,0,0]
	v_pk_fma_f32 v[98:99], v[98:99], v[132:133], 0 op_sel_hi:[0,1,0] neg_lo:[1,0,0] neg_hi:[1,0,0]
	v_cvt_pk_bf16_f32 v100, v100, v101
	v_cvt_pk_bf16_f32 v101, v98, v99
	ds_write_b64 v186, v[100:101] offset:1632
	ds_read_b32 v98, v187 offset:32
	s_waitcnt lgkmcnt(0)
	v_pk_fma_f32 v[100:101], v[98:99], v[126:127], 0 op_sel_hi:[0,1,0] neg_lo:[1,0,0] neg_hi:[1,0,0]
	v_pk_fma_f32 v[98:99], v[98:99], v[128:129], 0 op_sel_hi:[0,1,0] neg_lo:[1,0,0] neg_hi:[1,0,0]
	v_cvt_pk_bf16_f32 v100, v100, v101
	v_cvt_pk_bf16_f32 v101, v98, v99
	ds_write_b64 v186, v[100:101] offset:2176
	ds_read_b32 v98, v187 offset:40
	s_waitcnt lgkmcnt(0)
	v_pk_fma_f32 v[100:101], v[98:99], v[122:123], 0 op_sel_hi:[0,1,0] neg_lo:[1,0,0] neg_hi:[1,0,0]
	v_pk_fma_f32 v[98:99], v[98:99], v[124:125], 0 op_sel_hi:[0,1,0] neg_lo:[1,0,0] neg_hi:[1,0,0]
	v_cvt_pk_bf16_f32 v100, v100, v101
	v_cvt_pk_bf16_f32 v101, v98, v99
	ds_write_b64 v186, v[100:101] offset:2720
	ds_read_b32 v98, v187 offset:48
	s_waitcnt lgkmcnt(0)
	v_pk_fma_f32 v[100:101], v[98:99], v[114:115], 0 op_sel_hi:[0,1,0] neg_lo:[1,0,0] neg_hi:[1,0,0]
	v_pk_fma_f32 v[98:99], v[98:99], v[116:117], 0 op_sel_hi:[0,1,0] neg_lo:[1,0,0] neg_hi:[1,0,0]
	v_cvt_pk_bf16_f32 v100, v100, v101
	v_cvt_pk_bf16_f32 v101, v98, v99
	ds_write_b64 v186, v[100:101] offset:3264
	ds_read_b32 v98, v187 offset:56
	s_waitcnt lgkmcnt(0)
	v_pk_fma_f32 v[100:101], v[98:99], v[102:103], 0 op_sel_hi:[0,1,0] neg_lo:[1,0,0] neg_hi:[1,0,0]
	v_pk_fma_f32 v[98:99], v[98:99], v[104:105], 0 op_sel_hi:[0,1,0] neg_lo:[1,0,0] neg_hi:[1,0,0]
	v_cvt_pk_bf16_f32 v100, v100, v101
	v_cvt_pk_bf16_f32 v101, v98, v99
	ds_write_b64 v186, v[100:101] offset:3808
	ds_read_b128 v[98:101], v1
	ds_read_b128 v[102:105], v1 offset:64
	ds_read_b128 v[106:109], v1 offset:128
	ds_read_b128 v[110:113], v1 offset:192
	v_lshl_add_u64 v[114:115], v[168:169], 0, s[0:1]
	v_lshl_add_u64 v[126:127], v[176:177], 0, s[0:1]
	v_lshl_add_u64 v[176:177], v[180:181], 0, s[0:1]
	v_lshl_add_u64 v[180:181], v[182:183], 0, s[0:1]
	v_lshl_add_u64 v[116:117], v[170:171], 0, s[0:1]
	v_lshl_add_u64 v[122:123], v[172:173], 0, s[0:1]
	v_lshl_add_u64 v[124:125], v[174:175], 0, s[0:1]
	v_lshl_add_u64 v[128:129], v[178:179], 0, s[0:1]
	global_load_dwordx4 v[130:133], v[114:115], off nt
	global_load_dwordx4 v[138:141], v[116:117], off nt
	global_load_dwordx4 v[142:145], v[122:123], off nt
	global_load_dwordx4 v[146:149], v[124:125], off nt
	global_load_dwordx4 v[168:171], v[126:127], off nt
	global_load_dwordx4 v[172:175], v[128:129], off nt
	s_nop 0
	global_load_dwordx4 v[176:179], v[176:177], off nt
	s_nop 0
	global_load_dwordx4 v[180:183], v[180:181], off nt
	v_mov_b32_e32 v114, v188
	s_waitcnt vmcnt(15)
	s_waitcnt vmcnt(14)
	s_waitcnt vmcnt(13)
	s_waitcnt vmcnt(12)
	s_waitcnt vmcnt(11)
	s_waitcnt vmcnt(10)
	s_waitcnt vmcnt(9)
	s_waitcnt vmcnt(8)
	ds_read_b32 v114, v187 offset:64
	s_waitcnt lgkmcnt(0)
	v_pk_fma_f32 v[116:117], v[114:115], v[118:119], 0 op_sel_hi:[0,1,0] neg_lo:[1,0,0] neg_hi:[1,0,0]
	v_pk_fma_f32 v[114:115], v[114:115], v[120:121], 0 op_sel_hi:[0,1,0] neg_lo:[1,0,0] neg_hi:[1,0,0]
	v_cvt_pk_bf16_f32 v116, v116, v117
	v_cvt_pk_bf16_f32 v117, v114, v115
	ds_write_b64 v186, v[116:117]
	ds_read_b32 v114, v187 offset:72
	s_waitcnt lgkmcnt(0)
	v_pk_fma_f32 v[116:117], v[114:115], v[134:135], 0 op_sel_hi:[0,1,0] neg_lo:[1,0,0] neg_hi:[1,0,0]
	v_pk_fma_f32 v[114:115], v[114:115], v[136:137], 0 op_sel_hi:[0,1,0] neg_lo:[1,0,0] neg_hi:[1,0,0]
	v_cvt_pk_bf16_f32 v116, v116, v117
	v_cvt_pk_bf16_f32 v117, v114, v115
	ds_write_b64 v186, v[116:117] offset:544
	ds_read_b32 v114, v187 offset:80
	s_waitcnt lgkmcnt(0)
	v_pk_fma_f32 v[116:117], v[114:115], v[150:151], 0 op_sel_hi:[0,1,0] neg_lo:[1,0,0] neg_hi:[1,0,0]
	v_pk_fma_f32 v[114:115], v[114:115], v[152:153], 0 op_sel_hi:[0,1,0] neg_lo:[1,0,0] neg_hi:[1,0,0]
	v_cvt_pk_bf16_f32 v116, v116, v117
	v_cvt_pk_bf16_f32 v117, v114, v115
	ds_write_b64 v186, v[116:117] offset:1088
	ds_read_b32 v114, v187 offset:88
	s_waitcnt lgkmcnt(0)
	v_pk_fma_f32 v[116:117], v[114:115], v[156:157], 0 op_sel_hi:[0,1,0] neg_lo:[1,0,0] neg_hi:[1,0,0]
	v_pk_fma_f32 v[114:115], v[114:115], v[158:159], 0 op_sel_hi:[0,1,0] neg_lo:[1,0,0] neg_hi:[1,0,0]
	v_cvt_pk_bf16_f32 v116, v116, v117
	v_cvt_pk_bf16_f32 v117, v114, v115
	ds_write_b64 v186, v[116:117] offset:1632
	ds_read_b32 v114, v187 offset:96
	s_waitcnt lgkmcnt(0)
	v_pk_fma_f32 v[116:117], v[114:115], v[160:161], 0 op_sel_hi:[0,1,0] neg_lo:[1,0,0] neg_hi:[1,0,0]
	v_pk_fma_f32 v[114:115], v[114:115], v[162:163], 0 op_sel_hi:[0,1,0] neg_lo:[1,0,0] neg_hi:[1,0,0]
	v_cvt_pk_bf16_f32 v116, v116, v117
	v_cvt_pk_bf16_f32 v117, v114, v115
	ds_write_b64 v186, v[116:117] offset:2176
	ds_read_b32 v114, v187 offset:104
	s_waitcnt lgkmcnt(0)
	v_pk_fma_f32 v[116:117], v[114:115], v[164:165], 0 op_sel_hi:[0,1,0] neg_lo:[1,0,0] neg_hi:[1,0,0]
	v_pk_fma_f32 v[114:115], v[114:115], v[166:167], 0 op_sel_hi:[0,1,0] neg_lo:[1,0,0] neg_hi:[1,0,0]
	v_cvt_pk_bf16_f32 v116, v116, v117
	v_cvt_pk_bf16_f32 v117, v114, v115
	ds_write_b64 v186, v[116:117] offset:2720
	ds_read_b32 v114, v187 offset:112
	s_waitcnt lgkmcnt(0)
	v_pk_fma_f32 v[116:117], v[114:115], v[192:193], 0 op_sel_hi:[0,1,0] neg_lo:[1,0,0] neg_hi:[1,0,0]
	v_pk_fma_f32 v[114:115], v[114:115], v[194:195], 0 op_sel_hi:[0,1,0] neg_lo:[1,0,0] neg_hi:[1,0,0]
	v_cvt_pk_bf16_f32 v116, v116, v117
	v_cvt_pk_bf16_f32 v117, v114, v115
	ds_write_b64 v186, v[116:117] offset:3264
	ds_read_b32 v114, v187 offset:120
	s_waitcnt lgkmcnt(0)
	v_pk_fma_f32 v[116:117], v[114:115], v[196:197], 0 op_sel_hi:[0,1,0] neg_lo:[1,0,0] neg_hi:[1,0,0]
	v_pk_fma_f32 v[114:115], v[114:115], v[198:199], 0 op_sel_hi:[0,1,0] neg_lo:[1,0,0] neg_hi:[1,0,0]
	v_cvt_pk_bf16_f32 v116, v116, v117
	v_cvt_pk_bf16_f32 v117, v114, v115
	ds_write_b64 v186, v[116:117] offset:3808
	ds_read_b128 v[114:117], v1
	ds_read_b128 v[118:121], v1 offset:64
	ds_read_b128 v[122:125], v1 offset:128
	ds_read_b128 v[126:129], v1 offset:192
	s_waitcnt vmcnt(7)
	s_waitcnt vmcnt(6)
	s_waitcnt vmcnt(5)
	s_waitcnt vmcnt(4)
	s_waitcnt vmcnt(3)
	s_waitcnt vmcnt(2)
	s_waitcnt vmcnt(1)
	s_waitcnt vmcnt(0)
	ds_read_b32 v134, v187 offset:128
	s_waitcnt lgkmcnt(0)
	v_pk_fma_f32 v[130:131], v[134:135], v[130:131], 0 op_sel_hi:[0,1,0] neg_lo:[1,0,0] neg_hi:[1,0,0]
	v_pk_fma_f32 v[132:133], v[134:135], v[132:133], 0 op_sel_hi:[0,1,0] neg_lo:[1,0,0] neg_hi:[1,0,0]
	v_cvt_pk_bf16_f32 v130, v130, v131
	v_cvt_pk_bf16_f32 v131, v132, v133
	ds_write_b64 v186, v[130:131]
	ds_read_b32 v130, v187 offset:136
	s_waitcnt lgkmcnt(0)
	v_pk_fma_f32 v[132:133], v[130:131], v[138:139], 0 op_sel_hi:[0,1,0] neg_lo:[1,0,0] neg_hi:[1,0,0]
	v_pk_fma_f32 v[130:131], v[130:131], v[140:141], 0 op_sel_hi:[0,1,0] neg_lo:[1,0,0] neg_hi:[1,0,0]
	v_cvt_pk_bf16_f32 v132, v132, v133
	v_cvt_pk_bf16_f32 v133, v130, v131
	ds_write_b64 v186, v[132:133] offset:544
	ds_read_b32 v130, v187 offset:144
	s_waitcnt lgkmcnt(0)
	v_pk_fma_f32 v[132:133], v[130:131], v[142:143], 0 op_sel_hi:[0,1,0] neg_lo:[1,0,0] neg_hi:[1,0,0]
	v_pk_fma_f32 v[130:131], v[130:131], v[144:145], 0 op_sel_hi:[0,1,0] neg_lo:[1,0,0] neg_hi:[1,0,0]
	v_cvt_pk_bf16_f32 v132, v132, v133
	v_cvt_pk_bf16_f32 v133, v130, v131
	ds_write_b64 v186, v[132:133] offset:1088
	ds_read_b32 v130, v187 offset:152
	s_waitcnt lgkmcnt(0)
	v_pk_fma_f32 v[132:133], v[130:131], v[146:147], 0 op_sel_hi:[0,1,0] neg_lo:[1,0,0] neg_hi:[1,0,0]
	v_pk_fma_f32 v[130:131], v[130:131], v[148:149], 0 op_sel_hi:[0,1,0] neg_lo:[1,0,0] neg_hi:[1,0,0]
	v_cvt_pk_bf16_f32 v132, v132, v133
	v_cvt_pk_bf16_f32 v133, v130, v131
	ds_write_b64 v186, v[132:133] offset:1632
	ds_read_b32 v130, v187 offset:160
	s_waitcnt lgkmcnt(0)
	v_pk_fma_f32 v[132:133], v[130:131], v[168:169], 0 op_sel_hi:[0,1,0] neg_lo:[1,0,0] neg_hi:[1,0,0]
	v_pk_fma_f32 v[130:131], v[130:131], v[170:171], 0 op_sel_hi:[0,1,0] neg_lo:[1,0,0] neg_hi:[1,0,0]
	v_cvt_pk_bf16_f32 v132, v132, v133
	v_cvt_pk_bf16_f32 v133, v130, v131
	ds_write_b64 v186, v[132:133] offset:2176
	ds_read_b32 v130, v187 offset:168
	s_waitcnt lgkmcnt(0)
	v_pk_fma_f32 v[132:133], v[130:131], v[172:173], 0 op_sel_hi:[0,1,0] neg_lo:[1,0,0] neg_hi:[1,0,0]
	v_pk_fma_f32 v[130:131], v[130:131], v[174:175], 0 op_sel_hi:[0,1,0] neg_lo:[1,0,0] neg_hi:[1,0,0]
	v_cvt_pk_bf16_f32 v132, v132, v133
	v_cvt_pk_bf16_f32 v133, v130, v131
	ds_write_b64 v186, v[132:133] offset:2720
	ds_read_b32 v130, v187 offset:176
	s_waitcnt lgkmcnt(0)
	v_pk_fma_f32 v[132:133], v[130:131], v[176:177], 0 op_sel_hi:[0,1,0] neg_lo:[1,0,0] neg_hi:[1,0,0]
	v_pk_fma_f32 v[130:131], v[130:131], v[178:179], 0 op_sel_hi:[0,1,0] neg_lo:[1,0,0] neg_hi:[1,0,0]
	v_cvt_pk_bf16_f32 v132, v132, v133
	v_cvt_pk_bf16_f32 v133, v130, v131
	ds_write_b64 v186, v[132:133] offset:3264
	ds_read_b32 v130, v187 offset:184
	s_waitcnt lgkmcnt(0)
	v_pk_fma_f32 v[132:133], v[130:131], v[180:181], 0 op_sel_hi:[0,1,0] neg_lo:[1,0,0] neg_hi:[1,0,0]
	v_pk_fma_f32 v[130:131], v[130:131], v[182:183], 0 op_sel_hi:[0,1,0] neg_lo:[1,0,0] neg_hi:[1,0,0]
	v_cvt_pk_bf16_f32 v132, v132, v133
	v_cvt_pk_bf16_f32 v133, v130, v131
	ds_write_b64 v186, v[132:133] offset:3808
	ds_read_b128 v[130:133], v1
	ds_read_b128 v[134:137], v1 offset:64
	ds_read_b128 v[138:141], v1 offset:128
	ds_read_b128 v[142:145], v1 offset:192
	s_ashr_i32 s7, s6, 31
	s_lshl_b64 s[0:1], s[6:7], 2
	s_add_u32 s0, s4, s0
	s_addc_u32 s1, s5, s1
	v_lshlrev_b32_e32 v1, 4, v0
	global_load_dwordx4 v[146:149], v1, s[0:1]
	s_add_i32 s20, s34, 1
	s_add_i32 s34, s34, -1
	v_or_b32_e32 v153, s10, v206
	s_xor_b32 s26, s3, 2
	s_lshl_b64 s[10:11], s[10:11], 3
	s_and_b32 s20, s20, 3
	s_and_b32 s27, s34, 3
	s_add_u32 s10, s14, s10
	s_addc_u32 s11, s15, s11
	s_lshl_b32 s42, s35, 2
	s_add_i32 s41, s42, 0x26a20
	s_add_i32 s42, s42, 0x26a00
	v_lshlrev_b32_e32 v190, 3, v206
	s_cmp_eq_u32 s35, 3
	v_lshlrev_b32_e32 v150, 3, v0
	v_and_b32_e32 v151, 1, v0
	v_lshl_add_u64 v[0:1], v[154:155], 3, s[14:15]
	v_lshl_add_u64 v[192:193], s[10:11], 0, v[190:191]
	s_cselect_b64 s[10:11], -1, 0
	s_lshl_b32 s14, s3, 2
	s_add_u32 s24, s16, s14
	v_or_b32_e32 v155, 0x20000, v150
	v_add_u32_e32 v156, 0x20880, v150
	v_lshlrev_b32_e32 v150, 1, v153
	s_addc_u32 s25, s17, 0
	s_lshl_b32 s43, s3, 9
	v_lshl_add_u32 v212, s26, 9, v150
	s_lshl_b32 s15, s26, 8
	s_add_i32 s26, s43, 0x200
	v_mov_b32_e32 v152, 0x880
	v_cmp_lt_u32_e64 s[0:1], 15, v206
	v_cmp_eq_u32_e32 vcc, 1, v151
	s_and_b32 s45, s26, 0x600
	s_add_i32 s26, s43, 0x500
	v_cndmask_b32_e32 v211, 0, v152, vcc
	s_and_b32 s56, s26, 0x700
	s_add_i32 s26, s43, 0x540
	v_lshl_add_u32 v213, s20, 9, v150
	v_lshl_add_u32 v214, s27, 9, v150
	s_and_b32 s57, s26, 0x740
	s_add_i32 s26, s43, 0x580
	s_and_b32 s58, s26, 0x780
	s_add_i32 s26, s43, 0x5c0
	s_and_b32 s59, s26, 0x7c0
	s_add_i32 s26, s43, 0x600
	s_and_b32 s60, s26, 0x600
	s_add_i32 s26, s43, 0x640
	s_and_b32 s61, s26, 0x640
	s_add_i32 s26, s43, 0x680
	s_and_b32 s62, s26, 0x680
	s_add_i32 s26, s43, 0x6c0
	s_and_b32 s63, s26, 0x6c0
	s_add_i32 s26, s43, 0x700
	s_and_b32 s64, s26, 0x700
	s_add_i32 s26, s43, 0x740
	s_and_b32 s65, s26, 0x740
	s_add_i32 s26, s43, 0x780
	s_lshl_b32 s14, s27, 8
	s_lshl_b32 s20, s20, 8
	s_add_i32 s27, s43, 0x240
	s_add_i32 s28, s43, 0x280
	s_add_i32 s29, s43, 0x2c0
	s_add_i32 s30, s43, 0x300
	s_add_i32 s31, s43, 0x340
	s_add_i32 s34, s43, 0x380
	s_add_i32 s35, s43, 0x3c0
	s_add_i32 s36, s43, 0x440
	s_add_i32 s37, s43, 0x480
	s_add_i32 s38, s43, 0x4c0
	s_and_b32 s66, s26, 0x780
	s_add_i32 s26, s43, 0x7c0
	s_mul_hi_i32 s23, s18, 0x65
	s_mul_i32 s22, s18, 0x65
	v_cmp_eq_u32_e64 s[4:5], 1, v185
	v_cmp_eq_u32_e64 s[6:7], 2, v185
	v_cmp_eq_u32_e64 s[8:9], 63, v206
	s_xor_b32 s44, s43, 0x400
	s_and_b32 s46, s27, 0x640
	s_and_b32 s47, s28, 0x680
	v_and_b32_e32 v248, 2, v206
	v_cmp_ne_u32_e32 vcc, 0, v248
	v_mov_b32_e32 v249, 0x44444444
	v_mov_b32_e32 v250, 0xeeeeeeee
	s_nop 1
	v_cndmask_b32_e32 v223, v249, v250, vcc
	v_lshrrev_b32_e32 v248, 4, v206
	v_lshl_add_u32 v248, v248, 4, 1
	v_add_u32_e32 v249, 0, v248
	v_cvt_f32_u32_e32 v249, v249
	v_add_u32_e32 v250, 1, v248
	v_cvt_f32_u32_e32 v250, v250
	v_cvt_pk_bf16_f32 v232, v249, v250
	v_add_u32_e32 v249, 2, v248
	v_cvt_f32_u32_e32 v249, v249
	v_add_u32_e32 v250, 3, v248
	v_cvt_f32_u32_e32 v250, v250
	v_cvt_pk_bf16_f32 v233, v249, v250
	v_add_u32_e32 v249, 4, v248
	v_cvt_f32_u32_e32 v249, v249
	v_add_u32_e32 v250, 5, v248
	v_cvt_f32_u32_e32 v250, v250
	v_cvt_pk_bf16_f32 v234, v249, v250
	v_add_u32_e32 v249, 6, v248
	v_cvt_f32_u32_e32 v249, v249
	v_add_u32_e32 v250, 7, v248
	v_cvt_f32_u32_e32 v250, v250
	v_cvt_pk_bf16_f32 v235, v249, v250
	v_add_u32_e32 v249, 8, v248
	v_cvt_f32_u32_e32 v249, v249
	v_add_u32_e32 v250, 9, v248
	v_cvt_f32_u32_e32 v250, v250
	v_cvt_pk_bf16_f32 v236, v249, v250
	v_add_u32_e32 v249, 10, v248
	v_cvt_f32_u32_e32 v249, v249
	v_add_u32_e32 v250, 11, v248
	v_cvt_f32_u32_e32 v250, v250
	v_cvt_pk_bf16_f32 v237, v249, v250
	v_add_u32_e32 v249, 12, v248
	v_cvt_f32_u32_e32 v249, v249
	v_add_u32_e32 v250, 13, v248
	v_cvt_f32_u32_e32 v250, v250
	v_cvt_pk_bf16_f32 v238, v249, v250
	v_add_u32_e32 v249, 14, v248
	v_cvt_f32_u32_e32 v249, v249
	v_add_u32_e32 v250, 15, v248
	v_cvt_f32_u32_e32 v250, v250
	v_cvt_pk_bf16_f32 v239, v249, v250
	v_and_b32_e32 v248, 15, v206
	v_lshrrev_b32_e32 v249, 2, v248
	v_and_b32_e32 v250, 1, v248
	v_lshl_add_u32 v249, v249, 1, v250
	v_and_b32_e32 v250, 3, v249
	v_lshrrev_b32_e32 v251, 4, v206
	v_cmp_eq_u32_e32 vcc, v250, v251
	v_lshrrev_b32_e32 v249, 2, v249
	v_cmp_ne_u32_e64 s[78:79], 0, v249
	v_mov_b32_e32 v250, 0x3f80
	v_mov_b32_e32 v251, 0x3f800000
	s_nop 1
	v_cndmask_b32_e64 v250, v250, v251, s[78:79]
	v_cndmask_b32_e32 v252, 0, v250, vcc
	s_lshr_b32 s77, s19, 15
	s_mulk_i32 s77, 0x1100
	s_add_i32 s77, s77, 0x22200
	v_lshrrev_b32_e32 v248, 4, v206
	v_and_b32_e32 v249, 1, v248
	v_lshrrev_b32_e32 v250, 1, v248
	v_lshlrev_b32_e32 v249, 6, v249
	v_lshl_add_u32 v253, v250, 1, v249
	v_and_b32_e32 v248, 15, v206
	v_cmp_eq_u32_e64 s[78:79], 0, v248
	v_mov_b32_e32 v244, v252
	v_mov_b32_e32 v245, 0
	v_mov_b32_e32 v246, 0
	v_mov_b32_e32 v247, 0
	v_mov_b64_e32 v[240:241], 0
	v_mov_b64_e32 v[242:243], 0
	s_nop 1
	v_smfmac_f32_16x16x64_bf16 v[240:243], v[244:247], v[232:239], v223
	s_nop 15
	s_nop 3
	s_and_saveexec_b64 s[80:81], s[78:79]
	v_cvt_u32_f32_e32 v248, v240
	v_add_u32_e32 v248, -1, v248
	v_lshl_add_u32 v248, v248, 2, s77
	v_add_u32_e32 v249, 0, v253
	ds_write_b32 v248, v249
	v_cvt_u32_f32_e32 v248, v241
	v_add_u32_e32 v248, -1, v248
	v_lshl_add_u32 v248, v248, 2, s77
	v_add_u32_e32 v249, 32, v253
	ds_write_b32 v248, v249
	v_cvt_u32_f32_e32 v248, v242
	v_add_u32_e32 v248, -1, v248
	v_lshl_add_u32 v248, v248, 2, s77
	v_add_u32_e32 v249, 16, v253
	ds_write_b32 v248, v249
	v_cvt_u32_f32_e32 v248, v243
	v_add_u32_e32 v248, -1, v248
	v_lshl_add_u32 v248, v248, 2, s77
	v_add_u32_e32 v249, 48, v253
	ds_write_b32 v248, v249
	s_or_b64 exec, exec, s[80:81]
	v_mov_b32_e32 v244, 0
	v_mov_b32_e32 v245, v252
	v_mov_b32_e32 v246, 0
	v_mov_b32_e32 v247, 0
	v_mov_b64_e32 v[240:241], 0
	v_mov_b64_e32 v[242:243], 0
	s_nop 1
	v_smfmac_f32_16x16x64_bf16 v[240:243], v[244:247], v[232:239], v223
	s_nop 15
	s_nop 3
	s_and_saveexec_b64 s[80:81], s[78:79]
	v_cvt_u32_f32_e32 v248, v240
	v_add_u32_e32 v248, -1, v248
	v_lshl_add_u32 v248, v248, 2, s77
	v_add_u32_e32 v249, 4, v253
	ds_write_b32 v248, v249
	v_cvt_u32_f32_e32 v248, v241
	v_add_u32_e32 v248, -1, v248
	v_lshl_add_u32 v248, v248, 2, s77
	v_add_u32_e32 v249, 36, v253
	ds_write_b32 v248, v249
	v_cvt_u32_f32_e32 v248, v242
	v_add_u32_e32 v248, -1, v248
	v_lshl_add_u32 v248, v248, 2, s77
	v_add_u32_e32 v249, 20, v253
	ds_write_b32 v248, v249
	v_cvt_u32_f32_e32 v248, v243
	v_add_u32_e32 v248, -1, v248
	v_lshl_add_u32 v248, v248, 2, s77
	v_add_u32_e32 v249, 52, v253
	ds_write_b32 v248, v249
	s_or_b64 exec, exec, s[80:81]
	v_mov_b32_e32 v244, 0
	v_mov_b32_e32 v245, 0
	v_mov_b32_e32 v246, v252
	v_mov_b32_e32 v247, 0
	v_mov_b64_e32 v[240:241], 0
	v_mov_b64_e32 v[242:243], 0
	s_nop 1
	v_smfmac_f32_16x16x64_bf16 v[240:243], v[244:247], v[232:239], v223
	s_nop 15
	s_nop 3
	s_and_saveexec_b64 s[80:81], s[78:79]
	v_cvt_u32_f32_e32 v248, v240
	v_add_u32_e32 v248, -1, v248
	v_lshl_add_u32 v248, v248, 2, s77
	v_add_u32_e32 v249, 8, v253
	ds_write_b32 v248, v249
	v_cvt_u32_f32_e32 v248, v241
	v_add_u32_e32 v248, -1, v248
	v_lshl_add_u32 v248, v248, 2, s77
	v_add_u32_e32 v249, 40, v253
	ds_write_b32 v248, v249
	v_cvt_u32_f32_e32 v248, v242
	v_add_u32_e32 v248, -1, v248
	v_lshl_add_u32 v248, v248, 2, s77
	v_add_u32_e32 v249, 24, v253
	ds_write_b32 v248, v249
	v_cvt_u32_f32_e32 v248, v243
	v_add_u32_e32 v248, -1, v248
	v_lshl_add_u32 v248, v248, 2, s77
	v_add_u32_e32 v249, 56, v253
	ds_write_b32 v248, v249
	s_or_b64 exec, exec, s[80:81]
	v_mov_b32_e32 v244, 0
	v_mov_b32_e32 v245, 0
	v_mov_b32_e32 v246, 0
	v_mov_b32_e32 v247, v252
	v_mov_b64_e32 v[240:241], 0
	v_mov_b64_e32 v[242:243], 0
	s_nop 1
	v_smfmac_f32_16x16x64_bf16 v[240:243], v[244:247], v[232:239], v223
	s_nop 15
	s_nop 3
	s_and_saveexec_b64 s[80:81], s[78:79]
	v_cvt_u32_f32_e32 v248, v240
	v_add_u32_e32 v248, -1, v248
	v_lshl_add_u32 v248, v248, 2, s77
	v_add_u32_e32 v249, 12, v253
	ds_write_b32 v248, v249
	v_cvt_u32_f32_e32 v248, v241
	v_add_u32_e32 v248, -1, v248
	v_lshl_add_u32 v248, v248, 2, s77
	v_add_u32_e32 v249, 44, v253
	ds_write_b32 v248, v249
	v_cvt_u32_f32_e32 v248, v242
	v_add_u32_e32 v248, -1, v248
	v_lshl_add_u32 v248, v248, 2, s77
	v_add_u32_e32 v249, 28, v253
	ds_write_b32 v248, v249
	v_cvt_u32_f32_e32 v248, v243
	v_add_u32_e32 v248, -1, v248
	v_lshl_add_u32 v248, v248, 2, s77
	v_add_u32_e32 v249, 60, v253
	ds_write_b32 v248, v249
	s_or_b64 exec, exec, s[80:81]
	v_bfe_u32 v248, v206, 3, 2
	v_lshrrev_b32_e32 v249, 5, v206
	v_lshlrev_b32_e32 v248, 4, v248
	v_lshl_or_b32 v248, v249, 3, v248
	v_and_b32_e32 v249, 7, v206
	v_or_b32_e32 v248, v248, v249
	v_lshl_add_u32 v248, v248, 2, s77
	s_waitcnt lgkmcnt(0)
	ds_read_b32 v254, v248
	v_and_b32_e32 v248, 15, v206
	v_bfe_u32 v249, v248, 1, 2
	v_lshrrev_b32_e32 v250, 3, v248
	v_lshlrev_b32_e32 v249, 4, v249
	v_lshl_or_b32 v249, v250, 3, v249
	v_and_b32_e32 v250, 1, v248
	v_lshl_or_b32 v249, v250, 2, v249
	v_lshl_add_u32 v249, v249, 2, s77
	ds_read_b128 v[248:251], v249
	s_lshr_b32 s76, s19, 6
	s_add_i32 s76, s76, 0x20000
	v_lshrrev_b32_e32 v252, 4, v206
	v_lshl_add_u32 v252, v252, 7, s76
	s_waitcnt lgkmcnt(0)
	v_add_u32_e32 v248, v252, v248
	v_add_u32_e32 v249, v252, v249
	v_add_u32_e32 v250, v252, v250
	v_add_u32_e32 v251, v252, v251
	s_waitcnt vmcnt(0)
	v_cvt_pk_bf16_f32 v152, v147, s0
	v_cvt_pk_bf16_f32 v153, v146, s0
	v_cvt_pk_bf16_f32 v157, v149, s0
	v_cvt_pk_bf16_f32 v158, v148, s0
	v_cvt_pk_bf16_f32 v151, v148, v149
	v_cvt_pk_bf16_f32 v150, v146, v147
	v_lshlrev_b32_e32 v158, 16, v158
	v_lshlrev_b32_e32 v157, 16, v157
	v_lshlrev_b32_e32 v153, 16, v153
	v_lshlrev_b32_e32 v152, 16, v152
	ds_write_b16 v248, v150
	ds_write_b16_d16_hi v249, v150
	ds_write_b16 v250, v151
	ds_write_b16_d16_hi v251, v151
	v_sub_f32_e32 v150, v147, v152
	v_sub_f32_e32 v146, v146, v153
	v_sub_f32_e32 v147, v149, v157
	v_sub_f32_e32 v148, v148, v158
	v_cvt_pk_bf16_f32 v147, v148, v147
	v_cvt_pk_bf16_f32 v146, v146, v150
	ds_write_b16 v248, v146 offset:2176
	ds_write_b16_d16_hi v249, v146 offset:2176
	ds_write_b16 v250, v147 offset:2176
	ds_write_b16_d16_hi v251, v147 offset:2176
	s_waitcnt lgkmcnt(0)
	v_mov_b32_e32 v146, 0x20000
	s_and_b32 s48, s29, 0x6c0
	s_and_b32 s49, s30, 0x700
	s_and_b32 s50, s31, 0x740
	s_and_b32 s51, s34, 0x780
	s_and_b32 s52, s35, 0x7c0
	s_and_b32 s53, s36, 0x640
	s_and_b32 s54, s37, 0x680
	s_and_b32 s55, s38, 0x6c0
	s_and_b32 s67, s26, 0x7c0
	s_and_b64 s[26:27], s[10:11], s[12:13]
	v_lshl_add_u32 v215, v154, 1, v146
	v_mov_b32_e32 v216, 1
	s_lshl_b32 s28, s14, 3
	s_lshl_b32 s30, s15, 3
	s_lshl_b32 s34, s20, 3
	s_movk_i32 s68, 0x7fff
	s_mov_b32 s69, 0
	v_and_b32_e32 v220, 24, v206
	v_lshlrev_b32_e32 v220, 2, v220
	v_and_b32_e32 v221, 2, v206
	v_lshl_or_b32 v220, v221, 3, v220
	v_and_b32_e32 v221, 32, v206
	v_lshrrev_b32_e32 v221, 2, v221
	v_or_b32_e32 v220, v220, v221
	v_and_b32_e32 v221, 4, v206
	v_or_b32_e32 v220, v220, v221
	v_and_b32_e32 v221, 1, v206
	v_lshl_or_b32 v220, v221, 1, v220
	v_mov_b32_e32 v220, v254
	s_lshr_b32 s76, s19, 8
	s_add_i32 s76, s76, 0x20000
	v_add_u32_e32 v220, s76, v220
	v_add_u32_e32 v225, s45, v220
	v_add_u32_e32 v226, s44, v220
	v_add_u32_e32 v227, s60, v220
	v_add_u32_e32 v228, s43, v220
	v_and_b32_e32 v221, 1, v206
	v_mul_u32_u24_e32 v221, 0x880, v221
	v_lshrrev_b32_e32 v220, 4, v206
	v_lshl_add_u32 v221, v220, 5, v221
	v_and_b32_e32 v220, 2, v206
	v_lshl_add_u32 v221, v220, 3, v221
	v_add_u32_e32 v222, 0x20000, v221
	v_cmp_ne_u32_e32 vcc, 0, v220
	v_mov_b32_e32 v220, 0x44444444
	v_mov_b32_e32 v221, 0xeeeeeeee
	s_nop 1
	v_cndmask_b32_e32 v223, v220, v221, vcc
	v_cmp_lt_u32_e64 s[74:75], 47, v206
	v_mov_b32_e32 v224, v184
	ds_read_b128 v[166:169], v224 offset:0
	ds_read_b128 v[170:173], v224 offset:1024
	ds_read_b128 v[174:177], v224 offset:2048
	ds_read_b128 v[178:181], v224 offset:3072
	ds_read_b128 v[182:185], v224 offset:4096
	ds_read_b128 v[186:189], v224 offset:5120
	s_mov_b32 s20, 0
.Lj_loop:
	s_and_b32 s70, s20, 1
	s_waitcnt lgkmcnt(0)
	s_barrier
	s_mul_i32 s38, s70, 0x1100
	v_add_u32_e32 v229, s38, v222
	v_add_u32_e32 v230, s43, v229
	ds_read_b128 v[150:153], v230 offset:0
	ds_read_b128 v[194:197], v230 offset:128
	ds_read_b128 v[198:201], v230 offset:256
	ds_read_b128 v[232:235], v230 offset:384
	s_cmp_lg_u32 s20, 1
	s_cselect_b64 s[10:11], -1, 0
	s_and_b64 s[14:15], s[10:11], s[26:27]
	s_and_saveexec_b64 s[10:11], s[14:15]
	s_cbranch_execz .Lj_norr
	s_lshl_b32 s14, s70, 4
	s_or_b32 s14, s14, 0x26a00
	v_mov_b32_e32 v236, s14
	s_add_i32 s14, s20, -2
	ds_read_b128 v[236:239], v236
	s_cmp_lg_u32 s20, 0
	s_cselect_b32 s14, s14, 0x64
	s_ashr_i32 s15, s14, 31
	s_add_u32 s14, s22, s14
	s_addc_u32 s15, s23, s15
	s_lshl_b64 s[14:15], s[14:15], 4
	s_add_u32 s14, s24, s14
	s_addc_u32 s15, s25, s15
	s_waitcnt lgkmcnt(0)
	v_add_f32_e32 v236, v236, v237
	v_add_f32_e32 v238, v238, v239
	v_add_f32_e32 v236, v236, v238
	global_store_dword v191, v236, s[14:15]
.Lj_norr:
	s_or_b64 exec, exec, s[10:11]
	v_mov_b64_e32 v[146:147], 0
	v_mov_b64_e32 v[148:149], 0
	v_mov_b64_e32 v[154:155], 0
	v_mov_b64_e32 v[156:157], 0
	v_mov_b64_e32 v[158:159], 0
	v_mov_b64_e32 v[160:161], 0
	v_mov_b64_e32 v[162:163], 0
	v_mov_b64_e32 v[164:165], 0
	v_mov_b32_e32 v231, 0
	s_lshl_b32 s10, s70, 13
	s_add_i32 s14, s10, s34
	s_mov_b32 s15, 0
	v_lshl_add_u64 v[244:245], v[192:193], 0, s[14:15]
	s_add_i32 s14, s10, s30
	v_lshl_add_u64 v[246:247], v[192:193], 0, s[14:15]
	s_add_i32 s14, s10, s28
	v_lshl_add_u64 v[248:249], v[192:193], 0, s[14:15]
	s_waitcnt lgkmcnt(3)
	v_smfmac_f32_16x16x64_bf16 v[146:149], v[150:153], v[2:9], v223
	v_smfmac_f32_16x16x64_bf16 v[154:157], v[150:153], v[18:25], v223
	v_smfmac_f32_16x16x64_bf16 v[158:161], v[150:153], v[34:41], v223
	v_smfmac_f32_16x16x64_bf16 v[162:165], v[150:153], v[166:173], v223
	v_or3_b32 v231, v150, v151, v231
	v_or3_b32 v231, v152, v153, v231
	ds_read_b128 v[166:169], v224 offset:6144
	ds_read_b128 v[170:173], v224 offset:7168
	s_cmp_eq_u32 s20, 0
	s_cbranch_scc1 .Lj_nopoll0
	global_load_dwordx2 v[204:205], v[244:245], off sc1
	global_load_dwordx2 v[202:203], v[246:247], off sc1
	global_load_dwordx2 v[218:219], v[248:249], off sc1
.Lj_nopoll0:
	s_waitcnt lgkmcnt(4)
	v_smfmac_f32_16x16x64_bf16 v[146:149], v[194:197], v[10:17], v223
	v_smfmac_f32_16x16x64_bf16 v[154:157], v[194:197], v[26:33], v223
	v_smfmac_f32_16x16x64_bf16 v[158:161], v[194:197], v[42:49], v223
	v_smfmac_f32_16x16x64_bf16 v[162:165], v[194:197], v[174:181], v223
	v_or3_b32 v231, v194, v195, v231
	v_or3_b32 v231, v196, v197, v231
	ds_read_b128 v[174:177], v224 offset:8192
	ds_read_b128 v[178:181], v224 offset:9216
	s_waitcnt lgkmcnt(5)
	v_smfmac_f32_16x16x64_bf16 v[146:149], v[198:201], v[50:57], v223
	v_smfmac_f32_16x16x64_bf16 v[154:157], v[198:201], v[66:73], v223
	v_smfmac_f32_16x16x64_bf16 v[158:161], v[198:201], v[82:89], v223
	v_smfmac_f32_16x16x64_bf16 v[162:165], v[198:201], v[182:189], v223
	v_or3_b32 v231, v198, v199, v231
	v_or3_b32 v231, v200, v201, v231
	ds_read_b128 v[182:185], v224 offset:10240
	ds_read_b128 v[186:189], v224 offset:11264
	s_waitcnt lgkmcnt(6)
	v_smfmac_f32_16x16x64_bf16 v[146:149], v[232:235], v[58:65], v223
	v_smfmac_f32_16x16x64_bf16 v[154:157], v[232:235], v[74:81], v223
	v_smfmac_f32_16x16x64_bf16 v[158:161], v[232:235], v[90:97], v223
	s_waitcnt lgkmcnt(4)
	v_smfmac_f32_16x16x64_bf16 v[162:165], v[232:235], v[166:173], v223
	v_or3_b32 v231, v232, v233, v231
	v_or3_b32 v231, v234, v235, v231
	ds_read_b128 v[166:169], v224 offset:12288
	ds_read_b128 v[170:173], v224 offset:13312
	s_cmp_eq_u32 s20, 0
	s_cbranch_scc1 .Lj_gdone
	s_mov_b32 s29, 0
.Lj_chk:
	s_waitcnt vmcnt(0)
	v_cmp_eq_u32_e32 vcc, s20, v205
	v_cmp_eq_u32_e64 s[14:15], s20, v203
	v_cmp_eq_u32_e64 s[72:73], s20, v219
	s_and_b64 vcc, vcc, s[14:15]
	s_and_b64 vcc, vcc, s[72:73]
	s_cmp_eq_u64 vcc, exec
	s_cbranch_scc1 .Lj_got
	s_add_i32 s29, s29, 1
	s_cmp_gt_u32 s29, 0x10000
	s_cbranch_scc1 .Lj_got
	s_sleep 1
	global_load_dwordx2 v[204:205], v[244:245], off sc1
	global_load_dwordx2 v[202:203], v[246:247], off sc1
	global_load_dwordx2 v[218:219], v[248:249], off sc1
	s_branch .Lj_chk
.Lj_got:
	v_cvt_pk_bf16_f32 v236, v204, v204
	v_lshlrev_b32_e32 v237, 16, v236
	v_sub_f32_e32 v237, v204, v237
	v_add_u32_e32 v238, s38, v225
	v_cvt_pk_bf16_f32 v237, v237, v237
	ds_write_b16 v238, v236
	ds_write_b16 v238, v237 offset:2176
	v_cvt_pk_bf16_f32 v236, v202, v202
	v_lshlrev_b32_e32 v237, 16, v236
	v_sub_f32_e32 v237, v202, v237
	v_add_u32_e32 v238, s38, v226
	v_cvt_pk_bf16_f32 v237, v237, v237
	ds_write_b16 v238, v236
	ds_write_b16 v238, v237 offset:2176
	v_cvt_pk_bf16_f32 v236, v218, v218
	v_lshlrev_b32_e32 v237, 16, v236
	v_sub_f32_e32 v237, v218, v237
	v_add_u32_e32 v238, s38, v227
	v_cvt_pk_bf16_f32 v237, v237, v237
	ds_write_b16 v238, v236
	ds_write_b16 v238, v237 offset:2176
.Lj_gdone:
	s_waitcnt lgkmcnt(0)
	s_barrier
	v_add_u32_e32 v240, s45, v229
	v_add_u32_e32 v241, s44, v229
	v_add_u32_e32 v242, s60, v229
	ds_read_b128 v[150:153], v240 offset:0
	ds_read_b128 v[194:197], v240 offset:128
	ds_read_b128 v[198:201], v240 offset:256
	ds_read_b128 v[232:235], v240 offset:384
	s_waitcnt lgkmcnt(3)
	v_smfmac_f32_16x16x64_bf16 v[146:149], v[150:153], v[98:105], v223
	v_smfmac_f32_16x16x64_bf16 v[154:157], v[150:153], v[114:121], v223
	v_smfmac_f32_16x16x64_bf16 v[158:161], v[150:153], v[130:137], v223
	v_smfmac_f32_16x16x64_bf16 v[162:165], v[150:153], v[174:181], v223
	v_or3_b32 v231, v150, v151, v231
	v_or3_b32 v231, v152, v153, v231
	ds_read_b128 v[174:177], v224 offset:14336
	ds_read_b128 v[178:181], v224 offset:15360
	ds_read_b128 v[150:153], v241 offset:0
	s_waitcnt lgkmcnt(5)
	v_smfmac_f32_16x16x64_bf16 v[146:149], v[194:197], v[106:113], v223
	v_smfmac_f32_16x16x64_bf16 v[154:157], v[194:197], v[122:129], v223
	v_smfmac_f32_16x16x64_bf16 v[158:161], v[194:197], v[138:145], v223
	v_smfmac_f32_16x16x64_bf16 v[162:165], v[194:197], v[182:189], v223
	v_or3_b32 v231, v194, v195, v231
	v_or3_b32 v231, v196, v197, v231
	ds_read_b128 v[182:185], v224 offset:16384
	ds_read_b128 v[186:189], v224 offset:17408
	ds_read_b128 v[194:197], v241 offset:128
	s_waitcnt lgkmcnt(7)
	v_smfmac_f32_16x16x64_bf16 v[146:149], v[198:201], a[0:7], v223
	v_smfmac_f32_16x16x64_bf16 v[154:157], v[198:201], a[16:23], v223
	v_smfmac_f32_16x16x64_bf16 v[158:161], v[198:201], a[32:39], v223
	v_smfmac_f32_16x16x64_bf16 v[162:165], v[198:201], v[166:173], v223
	v_or3_b32 v231, v198, v199, v231
	v_or3_b32 v231, v200, v201, v231
	ds_read_b128 v[166:169], v224 offset:18432
	ds_read_b128 v[170:173], v224 offset:19456
	ds_read_b128 v[198:201], v241 offset:256
	s_waitcnt lgkmcnt(9)
	v_smfmac_f32_16x16x64_bf16 v[146:149], v[232:235], a[8:15], v223
	v_smfmac_f32_16x16x64_bf16 v[154:157], v[232:235], a[24:31], v223
	v_smfmac_f32_16x16x64_bf16 v[158:161], v[232:235], a[40:47], v223
	s_waitcnt lgkmcnt(7)
	v_smfmac_f32_16x16x64_bf16 v[162:165], v[232:235], v[174:181], v223
	v_or3_b32 v231, v232, v233, v231
	v_or3_b32 v231, v234, v235, v231
	ds_read_b128 v[174:177], v224 offset:20480
	ds_read_b128 v[178:181], v224 offset:21504
	ds_read_b128 v[232:235], v241 offset:384
	s_waitcnt lgkmcnt(9)
	v_smfmac_f32_16x16x64_bf16 v[146:149], v[150:153], a[48:55], v223
	v_smfmac_f32_16x16x64_bf16 v[154:157], v[150:153], a[64:71], v223
	v_smfmac_f32_16x16x64_bf16 v[158:161], v[150:153], a[80:87], v223
	s_waitcnt lgkmcnt(7)
	v_smfmac_f32_16x16x64_bf16 v[162:165], v[150:153], v[182:189], v223
	v_or3_b32 v231, v150, v151, v231
	v_or3_b32 v231, v152, v153, v231
	ds_read_b128 v[182:185], v224 offset:22528
	ds_read_b128 v[186:189], v224 offset:23552
	ds_read_b128 v[150:153], v242 offset:0
	s_waitcnt lgkmcnt(9)
	v_smfmac_f32_16x16x64_bf16 v[146:149], v[194:197], a[56:63], v223
	v_smfmac_f32_16x16x64_bf16 v[154:157], v[194:197], a[72:79], v223
	v_smfmac_f32_16x16x64_bf16 v[158:161], v[194:197], a[88:95], v223
	s_waitcnt lgkmcnt(7)
	v_smfmac_f32_16x16x64_bf16 v[162:165], v[194:197], v[166:173], v223
	v_or3_b32 v231, v194, v195, v231
	v_or3_b32 v231, v196, v197, v231
	ds_read_b128 v[166:169], v224 offset:24576
	ds_read_b128 v[170:173], v224 offset:25600
	ds_read_b128 v[194:197], v242 offset:128
	s_waitcnt lgkmcnt(9)
	v_smfmac_f32_16x16x64_bf16 v[146:149], v[198:201], a[96:103], v223
	v_smfmac_f32_16x16x64_bf16 v[154:157], v[198:201], a[112:119], v223
	v_smfmac_f32_16x16x64_bf16 v[158:161], v[198:201], a[128:135], v223
	s_waitcnt lgkmcnt(7)
	v_smfmac_f32_16x16x64_bf16 v[162:165], v[198:201], v[174:181], v223
	v_or3_b32 v231, v198, v199, v231
	v_or3_b32 v231, v200, v201, v231
	ds_read_b128 v[174:177], v224 offset:26624
	ds_read_b128 v[178:181], v224 offset:27648
	ds_read_b128 v[198:201], v242 offset:256
	s_waitcnt lgkmcnt(9)
	v_smfmac_f32_16x16x64_bf16 v[146:149], v[232:235], a[104:111], v223
	v_smfmac_f32_16x16x64_bf16 v[154:157], v[232:235], a[120:127], v223
	v_smfmac_f32_16x16x64_bf16 v[158:161], v[232:235], a[136:143], v223
	s_waitcnt lgkmcnt(7)
	v_smfmac_f32_16x16x64_bf16 v[162:165], v[232:235], v[182:189], v223
	v_or3_b32 v231, v232, v233, v231
	v_or3_b32 v231, v234, v235, v231
	ds_read_b128 v[182:185], v224 offset:28672
	ds_read_b128 v[186:189], v224 offset:29696
	ds_read_b128 v[232:235], v242 offset:384
	s_waitcnt lgkmcnt(9)
	v_smfmac_f32_16x16x64_bf16 v[146:149], v[150:153], a[144:151], v223
	v_smfmac_f32_16x16x64_bf16 v[154:157], v[150:153], a[160:167], v223
	v_smfmac_f32_16x16x64_bf16 v[158:161], v[150:153], a[176:183], v223
	s_waitcnt lgkmcnt(7)
	v_smfmac_f32_16x16x64_bf16 v[162:165], v[150:153], v[166:173], v223
	v_or3_b32 v231, v150, v151, v231
	v_or3_b32 v231, v152, v153, v231
	ds_read_b128 v[166:169], v224 offset:30720
	ds_read_b128 v[170:173], v224 offset:31744
	s_waitcnt lgkmcnt(8)
	v_smfmac_f32_16x16x64_bf16 v[146:149], v[194:197], a[152:159], v223
	v_smfmac_f32_16x16x64_bf16 v[154:157], v[194:197], a[168:175], v223
	v_smfmac_f32_16x16x64_bf16 v[158:161], v[194:197], a[184:191], v223
	s_waitcnt lgkmcnt(6)
	v_smfmac_f32_16x16x64_bf16 v[162:165], v[194:197], v[174:181], v223
	v_or3_b32 v231, v194, v195, v231
	v_or3_b32 v231, v196, v197, v231
	ds_read_b128 v[174:177], v224 offset:2048
	ds_read_b128 v[178:181], v224 offset:3072
	s_waitcnt lgkmcnt(7)
	v_smfmac_f32_16x16x64_bf16 v[146:149], v[198:201], a[192:199], v223
	v_smfmac_f32_16x16x64_bf16 v[154:157], v[198:201], a[208:215], v223
	v_smfmac_f32_16x16x64_bf16 v[158:161], v[198:201], a[224:231], v223
	s_waitcnt lgkmcnt(5)
	v_smfmac_f32_16x16x64_bf16 v[162:165], v[198:201], v[182:189], v223
	v_or3_b32 v231, v198, v199, v231
	v_or3_b32 v231, v200, v201, v231
	ds_read_b128 v[182:185], v224 offset:4096
	ds_read_b128 v[186:189], v224 offset:5120
	s_waitcnt lgkmcnt(6)
	v_smfmac_f32_16x16x64_bf16 v[146:149], v[232:235], a[200:207], v223
	v_smfmac_f32_16x16x64_bf16 v[154:157], v[232:235], a[216:223], v223
	v_smfmac_f32_16x16x64_bf16 v[158:161], v[232:235], a[232:239], v223
	s_waitcnt lgkmcnt(4)
	v_smfmac_f32_16x16x64_bf16 v[162:165], v[232:235], v[166:173], v223
	v_or3_b32 v231, v232, v233, v231
	v_or3_b32 v231, v234, v235, v231
	ds_read_b128 v[166:169], v224 offset:0
	ds_read_b128 v[170:173], v224 offset:1024
	v_and_b32_e32 v231, 0x7fff7fff, v231
	s_cmp_eq_u32 s20, 0
	s_cselect_b64 s[36:37], -1, 0
	s_add_i32 s29, s20, 1
	v_cmp_ne_u32_e32 vcc, 0, v231
	s_and_b32 s14, s29, 1
	s_lshl_b32 s10, s14, 13
	s_mov_b32 s11, 0
	v_lshl_add_u64 v[250:251], v[0:1], 0, s[10:11]
	s_mul_i32 s15, s14, 0x1100
	v_add_u32_e32 v243, s15, v228
	v_mov_b32_e32 v253, s29
	s_nop 3
	s_cmp_eq_u64 vcc, 0
	s_cbranch_scc0 .Lj_nz
	s_cmp_lg_u32 s20, 0
	s_cbranch_scc1 .Lj_stop
.Lj_nz:
	v_add_f32_e32 v236, v146, v148
	v_add_f32_e32 v146, v147, v149
	v_add_f32_e32 v237, v154, v156
	v_add_f32_e32 v154, v155, v157
	v_add_f32_e32 v238, v158, v160
	v_add_f32_e32 v158, v159, v161
	v_add_f32_e32 v239, v162, v164
	v_add_f32_e32 v162, v163, v165
	v_add_f32_e32 v236, v236, v146
	v_add_f32_e32 v237, v237, v154
	v_add_f32_e32 v238, v238, v158
	v_add_f32_e32 v239, v239, v162
	v_cndmask_b32_e64 v236, v236, v237, s[4:5]
	v_cndmask_b32_e64 v236, v236, v238, s[6:7]
	v_cndmask_b32_e64 v156, v236, v239, s[74:75]
	s_cmpk_eq_i32 s20, 0x64
	s_cbranch_scc1 .Lj_nopub
	v_add_f32_e32 v236, v208, v156
	v_cndmask_b32_e64 v252, v156, v236, s[36:37]
	global_store_dwordx2 v[250:251], v[252:253], off sc1
	v_cvt_pk_bf16_f32 v237, v252, v252
	v_lshlrev_b32_e32 v238, 16, v237
	v_sub_f32_e32 v238, v252, v238
	v_cvt_pk_bf16_f32 v238, v238, v238
	ds_write_b16 v243, v237
	ds_write_b16 v243, v238 offset:2176
.Lj_nopub:
	s_cmp_eq_u32 s20, 0
	s_cbranch_scc1 .Lj_nores
	v_mul_f32_e32 v146, v207, v156
	v_mul_f32_e32 v147, v146, v146
	s_nop 1
	v_mov_b32_dpp v147, v147 row_shr:1 row_mask:0xf bank_mask:0xf bound_ctrl:1
	v_fmac_f32_e32 v147, v146, v146
	s_nop 1
	v_add_f32_dpp v146, v147, v147 row_shr:2 row_mask:0xf bank_mask:0xf bound_ctrl:1
	v_mov_b32_e32 v147, v191
	s_nop 0
	v_add_f32_dpp v146, v146, v146 row_shr:4 row_mask:0xf bank_mask:0xf bound_ctrl:1
	s_nop 1
	v_add_f32_dpp v146, v146, v146 row_shr:8 row_mask:0xf bank_mask:0xf bound_ctrl:1
	s_nop 1
	v_mov_b32_dpp v147, v146 row_bcast:15 row_mask:0xa bank_mask:0xf
	v_add_f32_e32 v146, v146, v147
	v_mov_b32_e32 v147, v191
	s_nop 1
	v_mov_b32_dpp v147, v146 row_bcast:31 row_mask:0xc bank_mask:0xf
	s_and_saveexec_b64 s[10:11], s[8:9]
	s_lshl_b32 s14, s14, 4
	s_add_i32 s14, s42, s14
	v_add_f32_e32 v146, v146, v147
	v_mov_b32_e32 v147, s14
	ds_write_b32 v147, v146
	s_or_b64 exec, exec, s[10:11]
.Lj_nores:
	s_mov_b32 s20, s29
	s_cmpk_eq_i32 s20, 0x65
	s_cbranch_scc0 .Lj_loop
	s_branch .LBB0_31
.Lj_stop:
	s_mov_b32 s69, s20
.LBB0_31:
	s_cmp_lt_i32 s69, 1
	s_mov_b64 s[0:1], -1
	s_cbranch_scc0 .LBB0_35
	s_waitcnt lgkmcnt(0)
	s_barrier
	s_cmp_lt_u32 s40, 64
	s_cselect_b64 s[0:1], -1, 0
	s_and_b64 s[4:5], s[12:13], s[0:1]
	s_and_saveexec_b64 s[0:1], s[4:5]
	s_cbranch_execz .LBB0_34
	v_mov_b32_e32 v0, 0x26a10
	ds_read_b128 v[0:3], v0
	s_mul_i32 s4, s18, 0x650
	s_mul_hi_i32 s5, s18, 0x650
	s_add_u32 s4, s16, s4
	s_addc_u32 s5, s17, s5
	s_waitcnt lgkmcnt(0)
	v_mov_b32_e32 v4, v1
	v_mov_b32_e32 v5, v2
	v_mov_b32_e32 v1, v3
	v_pk_add_f32 v[0:1], v[4:5], v[0:1]
	s_lshl_b32 s6, s3, 2
	v_add_f32_e32 v0, v0, v1
	v_mov_b32_e32 v1, s6
	global_store_dword v1, v0, s[4:5] offset:1584

	.amdhsa_kernel _Z11jacobi_mainPKfS0_S0_PyPf
		.amdhsa_group_segment_fixed_size 158272
		.amdhsa_private_segment_fixed_size 0
		.amdhsa_kernarg_size 40
		.amdhsa_user_sgpr_count 2
		.amdhsa_user_sgpr_dispatch_ptr 0
		.amdhsa_user_sgpr_queue_ptr 0
		.amdhsa_user_sgpr_kernarg_segment_ptr 1
		.amdhsa_user_sgpr_dispatch_id 0
		.amdhsa_user_sgpr_kernarg_preload_length 0
		.amdhsa_user_sgpr_kernarg_preload_offset 0
		.amdhsa_user_sgpr_private_segment_size 0
		.amdhsa_uses_dynamic_stack 0
		.amdhsa_enable_private_segment 0
		.amdhsa_system_sgpr_workgroup_id_x 1
		.amdhsa_system_sgpr_workgroup_id_y 0
		.amdhsa_system_sgpr_workgroup_id_z 0
		.amdhsa_system_sgpr_workgroup_info 0
		.amdhsa_system_vgpr_workitem_id 0
		.amdhsa_next_free_vgpr 496
		.amdhsa_next_free_sgpr 96
		.amdhsa_accum_offset 256
		.amdhsa_reserve_vcc 1
		.amdhsa_float_round_mode_32 0
		.amdhsa_float_round_mode_16_64 0
		.amdhsa_float_denorm_mode_32 3
		.amdhsa_float_denorm_mode_16_64 3
		.amdhsa_dx10_clamp 1
		.amdhsa_ieee_mode 1
		.amdhsa_fp16_overflow 0
		.amdhsa_tg_split 0
		.amdhsa_exception_fp_ieee_invalid_op 0
		.amdhsa_exception_fp_denorm_src 0
		.amdhsa_exception_fp_ieee_div_zero 0
		.amdhsa_exception_fp_ieee_overflow 0
		.amdhsa_exception_fp_ieee_underflow 0
		.amdhsa_exception_fp_ieee_inexact 0
		.amdhsa_exception_int_div_zero 0
	.end_amdhsa_kernel

amdhsa.kernels:
  - .agpr_count:     240
    .args:
      - .actual_access:  read_only
        .address_space:  global
        .offset:         0
        .size:           8
        .value_kind:     global_buffer
      - .actual_access:  read_only
        .address_space:  global
        .offset:         8
        .size:           8
        .value_kind:     global_buffer
      - .actual_access:  read_only
        .address_space:  global
        .offset:         16
        .size:           8
        .value_kind:     global_buffer
      - .address_space:  global
        .offset:         24
        .size:           8
        .value_kind:     global_buffer
      - .actual_access:  write_only
        .address_space:  global
        .offset:         32
        .size:           8
        .value_kind:     global_buffer
    .group_segment_fixed_size: 158272
    .kernarg_segment_align: 8
    .kernarg_segment_size: 40
    .language:       OpenCL C
    .language_version:
      - 2
      - 0
    .max_flat_workgroup_size: 256
    .name:           _Z11jacobi_mainPKfS0_S0_PyPf
    .private_segment_fixed_size: 0
    .sgpr_count:     80
    .sgpr_spill_count: 0
    .symbol:         _Z11jacobi_mainPKfS0_S0_PyPf.kd
    .uniform_work_group_size: 1
    .uses_dynamic_stack: false
    .vgpr_count:     496
    .vgpr_spill_count: 0
    .wavefront_size: 64
  - .agpr_count:     0
    .args:
      - .actual_access:  read_only
        .address_space:  global
        .offset:         0
        .size:           8
        .value_kind:     global_buffer
      - .actual_access:  read_only
        .address_space:  global
        .offset:         8
        .size:           8
        .value_kind:     global_buffer
      - .actual_access:  write_only
        .address_space:  global
        .offset:         16
        .size:           8
        .value_kind:     global_buffer
      - .offset:         24
        .size:           4
        .value_kind:     by_value
    .group_segment_fixed_size: 26116
    .kernarg_segment_align: 8
    .kernarg_segment_size: 28
    .language:       OpenCL C
    .language_version:
      - 2
      - 0
    .max_flat_workgroup_size: 1024
    .name:           _Z12final_kernelPKfS0_Pfi
    .private_segment_fixed_size: 0
    .sgpr_count:     19
    .sgpr_spill_count: 0
    .symbol:         _Z12final_kernelPKfS0_Pfi.kd
    .uniform_work_group_size: 1
    .uses_dynamic_stack: false
    .vgpr_count:     35
    .vgpr_spill_count: 0
    .wavefront_size: 64
